# v31: v25 + K-loop priorities inverted: the loading wave half runs at s_setprio 1, the MFMA segments at 0
# baseline (speedup 1.0000x reference)
; #define PG8_STAGE(bufoff, gbase, voff) do { _Pragma("unroll") for (int _i = 0; _i < 2; ++_i) \
;         __builtin_amdgcn_global_load_lds((const unsigned*)((const char*)(gbase) + (voff)[_i]), (LAS unsigned*)(lds + (bufoff) + ldsw + _i * 8192), 16, 0, 0); } while (0)
; #define PG8_LDA(dst, b, h) do { if constexpr (F8) { _Pragma("unroll") for (int m = 0; m < 4; ++m) dst##8[m] = PG8_LD8(lds, PG8_SA(b, h) + aoff + m * 2048); } \
;         else { _Pragma("unroll") for (int m = 0; m < 4; ++m) _Pragma("unroll") for (int k = 0; k < 2; ++k) dst[m][k] = *(const LAS bf16x8*)(lds + PG8_SA(b, h) + aoff + m * 2048 + k * 1024); } } while (0)
; #define PG8_WAIT_V(n) asm volatile("s_waitcnt vmcnt(" #n ")" ::: "memory")
; #define PG8_WAIT_L(n) asm volatile("s_waitcnt lgkmcnt(" #n ")" ::: "memory")
; #define PG8_BAR __builtin_amdgcn_s_barrier()
; #define PG8_SCHED __builtin_amdgcn_sched_barrier(0)
; template <bool GATHER, bool F8, class Epi, class Sched>
; __device__ __forceinline__ void gemm_phase(LAS unsigned char* lds, const int nt, const unsigned lda, const unsigned ldb, const Sched& S, const Epi& E) {
;     ...
;         for (int t = 0; t < nt; t += 2) {
;             const bool last = (t == nt - 2);
;             const char* a1 = cA + (size_t)(t + 1) * kstep;
;             const char* a2 = last ? nA : cA + (size_t)(t + 2) * kstep; const char* b2 = last ? nB : cB + (size_t)(t + 2) * kstep;
;             const char* a3 = a2 + kstep; const char* b3 = b2 + kstep;
;             unsigned w0[2], w1[2];
;             if constexpr (GATHER) {
; #pragma unroll
;                 for (int i = 0; i < 2; ++i) { w0[i] = last ? vN0[i] : vA0[i]; w1[i] = last ? vN1[i] : vA1[i]; }
;             } else {
; #pragma unroll
;                 for (int i = 0; i < 2; ++i) { w0[i] = voffA[i]; w1[i] = voffA[i]; }
;             }
;             PG8_LDB(B0, 0, 0); PG8_LDB(B1, 0, 1); PG8_SCHED; PG8_LDA(At, 0, 0); PG8_STAGE(PG8_SA(1, 1), a1 + hA, vA1);
;             PG8_WAIT_V(8); PG8_WAIT_L(0); PG8_BAR; PG8_MMA(0, 0, At, B0); PG8_MMA(0, 1, At, B1); PG8_BAR; PG8_SCHED;
;             PG8_LDA(At, 0, 1); PG8_STAGE(PG8_SB(0, 0), b2, voffB); PG8_STAGE(PG8_SB(0, 1), b2 + hB, voffB); PG8_STAGE(PG8_SA(0, 0), a2, w0);
;             PG8_WAIT_V(8); PG8_WAIT_L(0); PG8_BAR; PG8_MMA(1, 0, At, B0); PG8_MMA(1, 1, At, B1); PG8_BAR; PG8_SCHED;
.LBB0_247:
	ds_read_b128 v[148:151], v181
	ds_read_b128 v[152:155], v181 offset:1024
	ds_read_b128 v[156:159], v181 offset:2048
	ds_read_b128 v[160:163], v181 offset:3072
	ds_read_b128 v[190:193], v182
	ds_read_b128 v[194:197], v182 offset:1024
	ds_read_b128 v[200:203], v182 offset:2048
	ds_read_b128 v[204:207], v182 offset:3072
	s_add_u32 s34, s10, 0xfff80080
	s_addc_u32 s35, s11, -1
	s_cmp_eq_u32 s33, 28
	s_cselect_b32 s37, s1, s35
	s_cselect_b32 s36, s0, s34
	s_cselect_b32 s35, s31, s27
	s_cselect_b32 s34, s30, s14
	s_add_i32 m0, s42, 0xc000
	ds_read_b128 v[208:211], v183
	ds_read_b128 v[212:215], v183 offset:1024
	ds_read_b128 v[216:219], v183 offset:2048
	ds_read_b128 v[220:223], v183 offset:3072
	ds_read_b128 v[224:227], v183 offset:4096
	ds_read_b128 v[228:231], v183 offset:5120
	ds_read_b128 v[232:235], v183 offset:6144
	ds_read_b128 v[236:239], v183 offset:7168
	global_load_lds_dwordx4 v140, s[10:11]
	s_add_i32 m0, s42, 0xe000
	s_nop 0
	global_load_lds_dwordx4 v142, s[10:11]
	s_waitcnt vmcnt(8)
	s_waitcnt lgkmcnt(0)
	s_barrier
	s_setprio 0
	s_waitcnt lgkmcnt(0)
	v_mfma_f32_16x16x32_bf16 v[126:129], v[148:151], v[208:211], v[126:129]
	v_mfma_f32_16x16x32_bf16 v[122:125], v[156:159], v[208:211], v[122:125]
	v_mfma_f32_16x16x32_bf16 v[110:113], v[148:151], v[216:219], v[110:113]
	v_mfma_f32_16x16x32_bf16 v[106:109], v[156:159], v[216:219], v[106:109]
	v_mfma_f32_16x16x32_bf16 v[94:97], v[148:151], v[224:227], v[94:97]
	v_mfma_f32_16x16x32_bf16 v[90:93], v[156:159], v[224:227], v[90:93]
	v_mfma_f32_16x16x32_bf16 v[78:81], v[148:151], v[232:235], v[78:81]
	v_mfma_f32_16x16x32_bf16 v[74:77], v[156:159], v[232:235], v[74:77]
	v_mfma_f32_16x16x32_bf16 v[126:129], v[152:155], v[212:215], v[126:129]
	v_mfma_f32_16x16x32_bf16 v[122:125], v[160:163], v[212:215], v[122:125]
	v_mfma_f32_16x16x32_bf16 v[110:113], v[152:155], v[220:223], v[110:113]
	v_mfma_f32_16x16x32_bf16 v[106:109], v[160:163], v[220:223], v[106:109]
	v_mfma_f32_16x16x32_bf16 v[94:97], v[152:155], v[228:231], v[94:97]
	v_mfma_f32_16x16x32_bf16 v[90:93], v[160:163], v[228:231], v[90:93]
	v_mfma_f32_16x16x32_bf16 v[78:81], v[152:155], v[236:239], v[78:81]
	v_mfma_f32_16x16x32_bf16 v[74:77], v[160:163], v[236:239], v[74:77]
	s_setprio 1
	s_setprio 0
	v_mfma_f32_16x16x32_bf16 v[118:121], v[190:193], v[208:211], v[118:121]
	v_mfma_f32_16x16x32_bf16 v[114:117], v[200:203], v[208:211], v[114:117]
	v_mfma_f32_16x16x32_bf16 v[102:105], v[190:193], v[216:219], v[102:105]
	v_mfma_f32_16x16x32_bf16 v[98:101], v[200:203], v[216:219], v[98:101]
	v_mfma_f32_16x16x32_bf16 v[86:89], v[190:193], v[224:227], v[86:89]
	v_mfma_f32_16x16x32_bf16 v[82:85], v[200:203], v[224:227], v[82:85]
	v_mfma_f32_16x16x32_bf16 v[70:73], v[190:193], v[232:235], v[70:73]
	v_mfma_f32_16x16x32_bf16 v[66:69], v[200:203], v[232:235], v[66:69]
	v_mfma_f32_16x16x32_bf16 v[118:121], v[194:197], v[212:215], v[118:121]
	v_mfma_f32_16x16x32_bf16 v[114:117], v[204:207], v[212:215], v[114:117]
	v_mfma_f32_16x16x32_bf16 v[102:105], v[194:197], v[220:223], v[102:105]
	v_mfma_f32_16x16x32_bf16 v[98:101], v[204:207], v[220:223], v[98:101]
	v_mfma_f32_16x16x32_bf16 v[86:89], v[194:197], v[228:231], v[86:89]
	v_mfma_f32_16x16x32_bf16 v[82:85], v[204:207], v[228:231], v[82:85]
	v_mfma_f32_16x16x32_bf16 v[70:73], v[194:197], v[236:239], v[70:73]
	v_mfma_f32_16x16x32_bf16 v[66:69], v[204:207], v[236:239], v[66:69]
	s_setprio 1
	s_barrier
	s_add_i32 s38, s58, s29
	s_mov_b32 m0, s38
	ds_read_b128 v[208:211], v183 offset:16384
	ds_read_b128 v[212:215], v183 offset:17408
	ds_read_b128 v[216:219], v183 offset:18432
	ds_read_b128 v[220:223], v183 offset:19456
	ds_read_b128 v[224:227], v183 offset:20480
	ds_read_b128 v[228:231], v183 offset:21504
	ds_read_b128 v[232:235], v183 offset:22528
	ds_read_b128 v[236:239], v183 offset:23552
	global_load_lds_dwordx4 v132, s[34:35]
	s_add_i32 m0, s38, 0x2000
	s_add_u32 s64, s34, 0x80000
	s_addc_u32 s65, s35, 0
	s_add_i32 s38, s59, s29
	global_load_lds_dwordx4 v136, s[34:35]
	s_mov_b32 m0, s38
	s_nop 0
	global_load_lds_dwordx4 v132, s[64:65]
	s_add_i32 m0, s38, 0x2000
	s_nop 0
	global_load_lds_dwordx4 v136, s[64:65]
	s_mov_b32 m0, s42
	s_nop 0
	s_mov_b64 s[98:99], s[36:37]
	global_load_lds_dwordx4 v130, s[36:37]
	s_mov_b32 m0, s43
	s_nop 0
	global_load_lds_dwordx4 v134, s[36:37]
	s_waitcnt vmcnt(8)
	s_waitcnt lgkmcnt(0)
	s_barrier
	s_setprio 0
	s_waitcnt lgkmcnt(0)
	v_mfma_f32_16x16x32_bf16 v[62:65], v[148:151], v[208:211], v[62:65]
	v_mfma_f32_16x16x32_bf16 v[50:53], v[156:159], v[208:211], v[50:53]
	v_mfma_f32_16x16x32_bf16 v[38:41], v[148:151], v[216:219], v[38:41]
	v_mfma_f32_16x16x32_bf16 v[34:37], v[156:159], v[216:219], v[34:37]
	v_mfma_f32_16x16x32_bf16 v[22:25], v[148:151], v[224:227], v[22:25]
	v_mfma_f32_16x16x32_bf16 v[18:21], v[156:159], v[224:227], v[18:21]
	v_mfma_f32_16x16x32_bf16 v[6:9], v[148:151], v[232:235], v[6:9]
	v_mfma_f32_16x16x32_bf16 v[2:5], v[156:159], v[232:235], v[2:5]
	v_mfma_f32_16x16x32_bf16 v[62:65], v[152:155], v[212:215], v[62:65]
	v_mfma_f32_16x16x32_bf16 v[50:53], v[160:163], v[212:215], v[50:53]
	v_mfma_f32_16x16x32_bf16 v[38:41], v[152:155], v[220:223], v[38:41]
	v_mfma_f32_16x16x32_bf16 v[34:37], v[160:163], v[220:223], v[34:37]
	v_mfma_f32_16x16x32_bf16 v[22:25], v[152:155], v[228:231], v[22:25]
	v_mfma_f32_16x16x32_bf16 v[18:21], v[160:163], v[228:231], v[18:21]
	v_mfma_f32_16x16x32_bf16 v[6:9], v[152:155], v[236:239], v[6:9]
	v_mfma_f32_16x16x32_bf16 v[2:5], v[160:163], v[236:239], v[2:5]
	s_setprio 1
	s_setprio 0
	v_mfma_f32_16x16x32_bf16 v[58:61], v[190:193], v[208:211], v[58:61]
	v_mfma_f32_16x16x32_bf16 v[54:57], v[200:203], v[208:211], v[54:57]
	v_mfma_f32_16x16x32_bf16 v[46:49], v[190:193], v[216:219], v[46:49]
	v_mfma_f32_16x16x32_bf16 v[42:45], v[200:203], v[216:219], v[42:45]
	v_mfma_f32_16x16x32_bf16 v[30:33], v[190:193], v[224:227], v[30:33]
	v_mfma_f32_16x16x32_bf16 v[26:29], v[200:203], v[224:227], v[26:29]
	v_mfma_f32_16x16x32_bf16 v[14:17], v[190:193], v[232:235], v[14:17]
	v_mfma_f32_16x16x32_bf16 v[10:13], v[200:203], v[232:235], v[10:13]
	v_mfma_f32_16x16x32_bf16 v[58:61], v[194:197], v[212:215], v[58:61]
	v_mfma_f32_16x16x32_bf16 v[54:57], v[204:207], v[212:215], v[54:57]
	v_mfma_f32_16x16x32_bf16 v[46:49], v[194:197], v[220:223], v[46:49]
	v_mfma_f32_16x16x32_bf16 v[42:45], v[204:207], v[220:223], v[42:45]
	v_mfma_f32_16x16x32_bf16 v[30:33], v[194:197], v[228:231], v[30:33]
	v_mfma_f32_16x16x32_bf16 v[26:29], v[204:207], v[228:231], v[26:29]
	v_mfma_f32_16x16x32_bf16 v[14:17], v[194:197], v[236:239], v[14:17]
	v_mfma_f32_16x16x32_bf16 v[10:13], v[204:207], v[236:239], v[10:13]
	s_setprio 1
	s_barrier
; #define PG8_STAGE(bufoff, gbase, voff) do { _Pragma("unroll") for (int _i = 0; _i < 2; ++_i) \
;         __builtin_amdgcn_global_load_lds((const unsigned*)((const char*)(gbase) + (voff)[_i]), (LAS unsigned*)(lds + (bufoff) + ldsw + _i * 8192), 16, 0, 0); } while (0)
; #define PG8_LDA(dst, b, h) do { if constexpr (F8) { _Pragma("unroll") for (int m = 0; m < 4; ++m) dst##8[m] = PG8_LD8(lds, PG8_SA(b, h) + aoff + m * 2048); } \
;         else { _Pragma("unroll") for (int m = 0; m < 4; ++m) _Pragma("unroll") for (int k = 0; k < 2; ++k) dst[m][k] = *(const LAS bf16x8*)(lds + PG8_SA(b, h) + aoff + m * 2048 + k * 1024); } } while (0)
; #define PG8_LDB(dst, b, h) do { if constexpr (F8) { _Pragma("unroll") for (int n = 0; n < 2; ++n) dst##8[n] = PG8_LD8(ldsB, PG8_SBR(b, h) + boff + n * 2048); } \
;         else { _Pragma("unroll") for (int n = 0; n < 2; ++n) _Pragma("unroll") for (int k = 0; k < 2; ++k) dst[n][k] = *(const LAS bf16x8*)(ldsB + PG8_SBR(b, h) + boff + n * 2048 + k * 1024); } } while (0)
; #define PG8_WAIT_V(n) asm volatile("s_waitcnt vmcnt(" #n ")" ::: "memory")
; #define PG8_WAIT_L(n) asm volatile("s_waitcnt lgkmcnt(" #n ")" ::: "memory")
; #define PG8_BAR __builtin_amdgcn_s_barrier()
; #define PG8_SCHED __builtin_amdgcn_sched_barrier(0)
; template <bool GATHER, bool F8, class Epi, class Sched>
; __device__ __forceinline__ void gemm_phase(LAS unsigned char* lds, const int nt, const unsigned lda, const unsigned ldb, const Sched& S, const Epi& E) {
;     ...
;             PG8_LDB(B0, 1, 0); PG8_LDB(B1, 1, 1); PG8_SCHED; PG8_LDA(At, 1, 0); PG8_STAGE(PG8_SA(0, 1), a2 + hA, w1);
;             PG8_WAIT_V(8); PG8_WAIT_L(0); PG8_BAR; PG8_MMA(0, 0, At, B0); PG8_MMA(0, 1, At, B1); PG8_BAR; PG8_SCHED;
;             PG8_LDA(At, 1, 1); PG8_STAGE(PG8_SB(1, 0), b3, voffB); PG8_STAGE(PG8_SB(1, 1), b3 + hB, voffB); PG8_STAGE(PG8_SA(1, 0), a3, w0);
;             PG8_WAIT_V(8); PG8_WAIT_L(0); PG8_BAR; PG8_MMA(1, 0, At, B0); PG8_MMA(1, 1, At, B1); PG8_BAR; PG8_SCHED;
;         }
;         if (wr == 0) PG8_BAR;
;     __device__ __forceinline__ void operator()(f32x4 (&acc)[2][2][4][2], const GUnit& u, int wr, int wc, int fr, int fq) const {
;         const int row0 = u.pm * BM + wr * 64 + fr, pn = u.pn + pn0;
;         if (pn < 12) {
	s_add_i32 s38, 0, 0x18000
	v_add_u32_e32 v138, s38, v178
	s_add_i32 s64, 0, 0x1c000
	ds_read_b128 v[148:151], v138
	ds_read_b128 v[152:155], v138 offset:1024
	ds_read_b128 v[156:159], v138 offset:2048
	ds_read_b128 v[160:163], v138 offset:3072
	v_add_u32_e32 v138, s64, v178
	ds_read_b128 v[190:193], v138
	ds_read_b128 v[194:197], v138 offset:1024
	ds_read_b128 v[200:203], v138 offset:2048
	ds_read_b128 v[204:207], v138 offset:3072
	s_add_u32 s36, s36, 0x80000
	s_addc_u32 s37, s37, 0
	s_mov_b32 m0, s44
	ds_read_b128 v[208:211], v183 offset:32768
	ds_read_b128 v[212:215], v183 offset:33792
	ds_read_b128 v[216:219], v183 offset:34816
	ds_read_b128 v[220:223], v183 offset:35840
	ds_read_b128 v[224:227], v183 offset:36864
	ds_read_b128 v[228:231], v183 offset:37888
	ds_read_b128 v[232:235], v183 offset:38912
	ds_read_b128 v[236:239], v183 offset:39936
	global_load_lds_dwordx4 v130, s[36:37]
	s_mov_b32 m0, s45
	s_nop 0
	global_load_lds_dwordx4 v134, s[36:37]
	s_waitcnt vmcnt(8)
	s_waitcnt lgkmcnt(0)
	s_barrier
	s_setprio 0
	s_waitcnt lgkmcnt(0)
	v_mfma_f32_16x16x32_bf16 v[126:129], v[148:151], v[208:211], v[126:129]
	v_mfma_f32_16x16x32_bf16 v[122:125], v[156:159], v[208:211], v[122:125]
	v_mfma_f32_16x16x32_bf16 v[110:113], v[148:151], v[216:219], v[110:113]
	v_mfma_f32_16x16x32_bf16 v[106:109], v[156:159], v[216:219], v[106:109]
	v_mfma_f32_16x16x32_bf16 v[94:97], v[148:151], v[224:227], v[94:97]
	v_mfma_f32_16x16x32_bf16 v[90:93], v[156:159], v[224:227], v[90:93]
	v_mfma_f32_16x16x32_bf16 v[78:81], v[148:151], v[232:235], v[78:81]
	v_mfma_f32_16x16x32_bf16 v[74:77], v[156:159], v[232:235], v[74:77]
	v_mfma_f32_16x16x32_bf16 v[126:129], v[152:155], v[212:215], v[126:129]
	v_mfma_f32_16x16x32_bf16 v[122:125], v[160:163], v[212:215], v[122:125]
	v_mfma_f32_16x16x32_bf16 v[110:113], v[152:155], v[220:223], v[110:113]
	v_mfma_f32_16x16x32_bf16 v[106:109], v[160:163], v[220:223], v[106:109]
	v_mfma_f32_16x16x32_bf16 v[94:97], v[152:155], v[228:231], v[94:97]
	v_mfma_f32_16x16x32_bf16 v[90:93], v[160:163], v[228:231], v[90:93]
	v_mfma_f32_16x16x32_bf16 v[78:81], v[152:155], v[236:239], v[78:81]
	v_mfma_f32_16x16x32_bf16 v[74:77], v[160:163], v[236:239], v[74:77]
	s_setprio 1
	s_setprio 0
	v_mfma_f32_16x16x32_bf16 v[118:121], v[190:193], v[208:211], v[118:121]
	v_mfma_f32_16x16x32_bf16 v[114:117], v[200:203], v[208:211], v[114:117]
	v_mfma_f32_16x16x32_bf16 v[102:105], v[190:193], v[216:219], v[102:105]
	v_mfma_f32_16x16x32_bf16 v[98:101], v[200:203], v[216:219], v[98:101]
	v_mfma_f32_16x16x32_bf16 v[86:89], v[190:193], v[224:227], v[86:89]
	v_mfma_f32_16x16x32_bf16 v[82:85], v[200:203], v[224:227], v[82:85]
	v_mfma_f32_16x16x32_bf16 v[70:73], v[190:193], v[232:235], v[70:73]
	v_mfma_f32_16x16x32_bf16 v[66:69], v[200:203], v[232:235], v[66:69]
	v_mfma_f32_16x16x32_bf16 v[118:121], v[194:197], v[212:215], v[118:121]
	v_mfma_f32_16x16x32_bf16 v[114:117], v[204:207], v[212:215], v[114:117]
	v_mfma_f32_16x16x32_bf16 v[102:105], v[194:197], v[220:223], v[102:105]
	v_mfma_f32_16x16x32_bf16 v[98:101], v[204:207], v[220:223], v[98:101]
	v_mfma_f32_16x16x32_bf16 v[86:89], v[194:197], v[228:231], v[86:89]
	v_mfma_f32_16x16x32_bf16 v[82:85], v[204:207], v[228:231], v[82:85]
	v_mfma_f32_16x16x32_bf16 v[70:73], v[194:197], v[236:239], v[70:73]
	v_mfma_f32_16x16x32_bf16 v[66:69], v[204:207], v[236:239], v[66:69]
	s_setprio 1
	s_barrier
	s_add_i32 s36, s38, s29
	s_add_i32 m0, s36, 0xffffff80
	ds_read_b128 v[208:211], v183 offset:49152
	ds_read_b128 v[212:215], v183 offset:50176
	ds_read_b128 v[216:219], v183 offset:51200
	ds_read_b128 v[220:223], v183 offset:52224
	ds_read_b128 v[224:227], v183 offset:53248
	ds_read_b128 v[228:231], v183 offset:54272
	ds_read_b128 v[232:235], v183 offset:55296
	ds_read_b128 v[236:239], v183 offset:56320
	global_load_lds_dwordx4 v132, s[34:35] offset:128
	s_add_i32 m0, s36, 0x1f80
	s_add_i32 s36, s64, s29
	global_load_lds_dwordx4 v136, s[34:35] offset:128
	s_add_u32 s34, s34, 0x80080
	s_addc_u32 s35, s35, 0
	s_mov_b32 m0, s36
	s_nop 0
	global_load_lds_dwordx4 v132, s[34:35]
	s_add_i32 m0, s36, 0x2000
	s_nop 0
	global_load_lds_dwordx4 v136, s[34:35]
	s_add_i32 m0, s46, 0xffffff80
	s_nop 0
	global_load_lds_dwordx4 v130, s[98:99] offset:128
	s_add_i32 m0, s47, 0xffffff80
	s_nop 0
	global_load_lds_dwordx4 v134, s[98:99] offset:128
	s_waitcnt vmcnt(8)
	s_waitcnt lgkmcnt(0)
	s_barrier
	s_setprio 0
	s_waitcnt lgkmcnt(0)
	v_mfma_f32_16x16x32_bf16 v[62:65], v[148:151], v[208:211], v[62:65]
	v_mfma_f32_16x16x32_bf16 v[50:53], v[156:159], v[208:211], v[50:53]
	v_mfma_f32_16x16x32_bf16 v[38:41], v[148:151], v[216:219], v[38:41]
	v_mfma_f32_16x16x32_bf16 v[34:37], v[156:159], v[216:219], v[34:37]
	v_mfma_f32_16x16x32_bf16 v[22:25], v[148:151], v[224:227], v[22:25]
	v_mfma_f32_16x16x32_bf16 v[18:21], v[156:159], v[224:227], v[18:21]
	v_mfma_f32_16x16x32_bf16 v[6:9], v[148:151], v[232:235], v[6:9]
	v_mfma_f32_16x16x32_bf16 v[2:5], v[156:159], v[232:235], v[2:5]
	v_mfma_f32_16x16x32_bf16 v[62:65], v[152:155], v[212:215], v[62:65]
	v_mfma_f32_16x16x32_bf16 v[50:53], v[160:163], v[212:215], v[50:53]
	v_mfma_f32_16x16x32_bf16 v[38:41], v[152:155], v[220:223], v[38:41]
	v_mfma_f32_16x16x32_bf16 v[34:37], v[160:163], v[220:223], v[34:37]
	v_mfma_f32_16x16x32_bf16 v[22:25], v[152:155], v[228:231], v[22:25]
	v_mfma_f32_16x16x32_bf16 v[18:21], v[160:163], v[228:231], v[18:21]
	v_mfma_f32_16x16x32_bf16 v[6:9], v[152:155], v[236:239], v[6:9]
	v_mfma_f32_16x16x32_bf16 v[2:5], v[160:163], v[236:239], v[2:5]
	s_setprio 1
	s_setprio 0
	v_mfma_f32_16x16x32_bf16 v[58:61], v[190:193], v[208:211], v[58:61]
	v_mfma_f32_16x16x32_bf16 v[54:57], v[200:203], v[208:211], v[54:57]
	v_mfma_f32_16x16x32_bf16 v[46:49], v[190:193], v[216:219], v[46:49]
	v_mfma_f32_16x16x32_bf16 v[42:45], v[200:203], v[216:219], v[42:45]
	v_mfma_f32_16x16x32_bf16 v[30:33], v[190:193], v[224:227], v[30:33]
	v_mfma_f32_16x16x32_bf16 v[26:29], v[200:203], v[224:227], v[26:29]
	v_mfma_f32_16x16x32_bf16 v[14:17], v[190:193], v[232:235], v[14:17]
	v_mfma_f32_16x16x32_bf16 v[10:13], v[200:203], v[232:235], v[10:13]
	v_mfma_f32_16x16x32_bf16 v[58:61], v[194:197], v[212:215], v[58:61]
	v_mfma_f32_16x16x32_bf16 v[54:57], v[204:207], v[212:215], v[54:57]
	v_mfma_f32_16x16x32_bf16 v[46:49], v[194:197], v[220:223], v[46:49]
	v_mfma_f32_16x16x32_bf16 v[42:45], v[204:207], v[220:223], v[42:45]
	v_mfma_f32_16x16x32_bf16 v[30:33], v[194:197], v[228:231], v[30:33]
	v_mfma_f32_16x16x32_bf16 v[26:29], v[204:207], v[228:231], v[26:29]
	v_mfma_f32_16x16x32_bf16 v[14:17], v[194:197], v[236:239], v[14:17]
	v_mfma_f32_16x16x32_bf16 v[10:13], v[204:207], v[236:239], v[10:13]
	s_setprio 1
	s_barrier
	s_add_i32 s33, s33, 2
	s_add_u32 s10, s10, 0x100
	s_addc_u32 s11, s11, 0
	s_add_u32 s14, s14, 0x100
	s_addc_u32 s27, s27, 0
	s_cmp_gt_u32 s33, 29
	s_cbranch_scc0 .LBB0_247
	s_and_b64 vcc, exec, s[20:21]
	s_cbranch_vccz .LBB0_251
	s_barrier
	v_lshl_add_u32 v148, s26, 8, v177
	s_cmp_gt_i32 s28, 11
	s_mov_b64 s[10:11], -1
	s_cbranch_scc1 .LBB0_252

; #define PG8_STAGE(bufoff, gbase, voff) do { _Pragma("unroll") for (int _i = 0; _i < 2; ++_i) \
;         __builtin_amdgcn_global_load_lds((const unsigned*)((const char*)(gbase) + (voff)[_i]), (LAS unsigned*)(lds + (bufoff) + ldsw + _i * 8192), 16, 0, 0); } while (0)
; #define PG8_LDA(dst, b, h) do { if constexpr (F8) { _Pragma("unroll") for (int m = 0; m < 4; ++m) dst##8[m] = PG8_LD8(lds, PG8_SA(b, h) + aoff + m * 2048); } \
;         else { _Pragma("unroll") for (int m = 0; m < 4; ++m) _Pragma("unroll") for (int k = 0; k < 2; ++k) dst[m][k] = *(const LAS bf16x8*)(lds + PG8_SA(b, h) + aoff + m * 2048 + k * 1024); } } while (0)
; #define PG8_WAIT_V(n) asm volatile("s_waitcnt vmcnt(" #n ")" ::: "memory")
; #define PG8_WAIT_L(n) asm volatile("s_waitcnt lgkmcnt(" #n ")" ::: "memory")
; #define PG8_BAR __builtin_amdgcn_s_barrier()
; #define PG8_SCHED __builtin_amdgcn_sched_barrier(0)
; template <bool GATHER, bool F8, class Epi, class Sched>
; __device__ __forceinline__ void gemm_phase(LAS unsigned char* lds, const int nt, const unsigned lda, const unsigned ldb, const Sched& S, const Epi& E) {
;     ...
;         for (int t = 0; t < nt; t += 2) {
;             const bool last = (t == nt - 2);
;             const char* a1 = cA + (size_t)(t + 1) * kstep;
;             const char* a2 = last ? nA : cA + (size_t)(t + 2) * kstep; const char* b2 = last ? nB : cB + (size_t)(t + 2) * kstep;
;             const char* a3 = a2 + kstep; const char* b3 = b2 + kstep;
;             unsigned w0[2], w1[2];
;             if constexpr (GATHER) {
; #pragma unroll
;                 for (int i = 0; i < 2; ++i) { w0[i] = last ? vN0[i] : vA0[i]; w1[i] = last ? vN1[i] : vA1[i]; }
;             } else {
; #pragma unroll
;                 for (int i = 0; i < 2; ++i) { w0[i] = voffA[i]; w1[i] = voffA[i]; }
;             }
;             PG8_LDB(B0, 0, 0); PG8_LDB(B1, 0, 1); PG8_SCHED; PG8_LDA(At, 0, 0); PG8_STAGE(PG8_SA(1, 1), a1 + hA, vA1);
;             PG8_WAIT_V(8); PG8_WAIT_L(0); PG8_BAR; PG8_MMA(0, 0, At, B0); PG8_MMA(0, 1, At, B1); PG8_BAR; PG8_SCHED;
;             PG8_LDA(At, 0, 1); PG8_STAGE(PG8_SB(0, 0), b2, voffB); PG8_STAGE(PG8_SB(0, 1), b2 + hB, voffB); PG8_STAGE(PG8_SA(0, 0), a2, w0);
;             PG8_WAIT_V(8); PG8_WAIT_L(0); PG8_BAR; PG8_MMA(1, 0, At, B0); PG8_MMA(1, 1, At, B1); PG8_BAR; PG8_SCHED;
.LBB0_387:
	ds_read_b128 v[18:21], v1
	ds_read_b128 v[22:25], v1 offset:1024
	ds_read_b128 v[26:29], v1 offset:2048
	ds_read_b128 v[30:33], v1 offset:3072
	ds_read_b128 v[2:5], v1 offset:16384
	ds_read_b128 v[6:9], v1 offset:17408
	ds_read_b128 v[10:13], v1 offset:18432
	ds_read_b128 v[14:17], v1 offset:19456
	s_add_u32 s26, s24, 0xfffc0080
	s_addc_u32 s27, s25, -1
	s_cmp_eq_u32 s55, 12
	s_cselect_b32 s29, s1, s27
	s_cselect_b32 s28, s0, s26
	s_cselect_b32 s27, s21, s54
	s_cselect_b32 s26, s20, s30
	s_add_i32 m0, s23, 0xc000
	ds_read_b128 v[180:183], v191
	ds_read_b128 v[184:187], v191 offset:1024
	ds_read_b128 v[200:203], v191 offset:2048
	ds_read_b128 v[204:207], v191 offset:3072
	ds_read_b128 v[208:211], v191 offset:4096
	ds_read_b128 v[212:215], v191 offset:5120
	ds_read_b128 v[216:219], v191 offset:6144
	ds_read_b128 v[220:223], v191 offset:7168
	global_load_lds_dwordx4 v172, s[24:25]
	s_add_i32 m0, s23, 0xe000
	s_nop 0
	global_load_lds_dwordx4 v174, s[24:25]
	s_waitcnt vmcnt(8)
	s_waitcnt lgkmcnt(0)
	s_barrier
	s_setprio 0
	s_waitcnt lgkmcnt(0)
	v_mfma_scale_f32_16x16x128_f8f6f4 v[158:161], v[18:25], v[180:187], v[158:161], v192, v192 op_sel_hi:[0,0,0]
	v_mfma_scale_f32_16x16x128_f8f6f4 v[150:153], v[26:33], v[180:187], v[150:153], v192, v192 op_sel_hi:[0,0,0]
	v_mfma_scale_f32_16x16x128_f8f6f4 v[142:145], v[18:25], v[200:207], v[142:145], v192, v192 op_sel_hi:[0,0,0]
	v_mfma_scale_f32_16x16x128_f8f6f4 v[134:137], v[26:33], v[200:207], v[134:137], v192, v192 op_sel_hi:[0,0,0]
	v_mfma_scale_f32_16x16x128_f8f6f4 v[126:129], v[18:25], v[208:215], v[126:129], v192, v192 op_sel_hi:[0,0,0]
	v_mfma_scale_f32_16x16x128_f8f6f4 v[118:121], v[26:33], v[208:215], v[118:121], v192, v192 op_sel_hi:[0,0,0]
	v_mfma_scale_f32_16x16x128_f8f6f4 v[110:113], v[18:25], v[216:223], v[110:113], v192, v192 op_sel_hi:[0,0,0]
	v_mfma_scale_f32_16x16x128_f8f6f4 v[102:105], v[26:33], v[216:223], v[102:105], v192, v192 op_sel_hi:[0,0,0]
	s_setprio 1
	s_setprio 0
	v_mfma_scale_f32_16x16x128_f8f6f4 v[154:157], v[2:9], v[180:187], v[154:157], v192, v192 op_sel_hi:[0,0,0]
	v_mfma_scale_f32_16x16x128_f8f6f4 v[146:149], v[10:17], v[180:187], v[146:149], v192, v192 op_sel_hi:[0,0,0]
	v_mfma_scale_f32_16x16x128_f8f6f4 v[138:141], v[2:9], v[200:207], v[138:141], v192, v192 op_sel_hi:[0,0,0]
	v_mfma_scale_f32_16x16x128_f8f6f4 v[130:133], v[10:17], v[200:207], v[130:133], v192, v192 op_sel_hi:[0,0,0]
	v_mfma_scale_f32_16x16x128_f8f6f4 v[122:125], v[2:9], v[208:215], v[122:125], v192, v192 op_sel_hi:[0,0,0]
	v_mfma_scale_f32_16x16x128_f8f6f4 v[114:117], v[10:17], v[208:215], v[114:117], v192, v192 op_sel_hi:[0,0,0]
	v_mfma_scale_f32_16x16x128_f8f6f4 v[106:109], v[2:9], v[216:223], v[106:109], v192, v192 op_sel_hi:[0,0,0]
	v_mfma_scale_f32_16x16x128_f8f6f4 v[98:101], v[10:17], v[216:223], v[98:101], v192, v192 op_sel_hi:[0,0,0]
	s_setprio 1
	s_barrier
	s_mov_b32 m0, s38
	s_add_u32 s56, s26, 0x40000
	ds_read_b128 v[200:203], v191 offset:16384
	ds_read_b128 v[204:207], v191 offset:17408
	ds_read_b128 v[208:211], v191 offset:18432
	ds_read_b128 v[212:215], v191 offset:19456
	ds_read_b128 v[216:219], v191 offset:20480
	ds_read_b128 v[220:223], v191 offset:21504
	ds_read_b128 v[224:227], v191 offset:22528
	ds_read_b128 v[228:231], v191 offset:23552
	global_load_lds_dwordx4 v166, s[26:27]
	s_mov_b32 m0, s39
	s_addc_u32 s57, s27, 0
	global_load_lds_dwordx4 v162, s[26:27]
	s_mov_b32 m0, s40
	s_nop 0
	global_load_lds_dwordx4 v166, s[56:57]
	s_mov_b32 m0, s41
	s_nop 0
	global_load_lds_dwordx4 v162, s[56:57]
	s_mov_b32 m0, s23
	s_nop 0
	s_mov_b64 s[98:99], s[28:29]
	global_load_lds_dwordx4 v168, s[28:29]
	s_mov_b32 m0, s42
	s_nop 0
	global_load_lds_dwordx4 v164, s[28:29]
	s_waitcnt vmcnt(8)
	s_waitcnt lgkmcnt(0)
	s_barrier
	s_setprio 0
	s_waitcnt lgkmcnt(0)
	v_mfma_scale_f32_16x16x128_f8f6f4 v[86:89], v[18:25], v[200:207], v[86:89], v192, v192 op_sel_hi:[0,0,0]
	v_mfma_scale_f32_16x16x128_f8f6f4 v[78:81], v[26:33], v[200:207], v[78:81], v192, v192 op_sel_hi:[0,0,0]
	v_mfma_scale_f32_16x16x128_f8f6f4 v[70:73], v[18:25], v[208:215], v[70:73], v192, v192 op_sel_hi:[0,0,0]
	v_mfma_scale_f32_16x16x128_f8f6f4 v[62:65], v[26:33], v[208:215], v[62:65], v192, v192 op_sel_hi:[0,0,0]
	v_mfma_scale_f32_16x16x128_f8f6f4 v[54:57], v[18:25], v[216:223], v[54:57], v192, v192 op_sel_hi:[0,0,0]
	v_mfma_scale_f32_16x16x128_f8f6f4 v[46:49], v[26:33], v[216:223], v[46:49], v192, v192 op_sel_hi:[0,0,0]
	v_mfma_scale_f32_16x16x128_f8f6f4 v[38:41], v[18:25], v[224:231], v[38:41], v192, v192 op_sel_hi:[0,0,0]
	v_mfma_scale_f32_16x16x128_f8f6f4 v[34:37], v[26:33], v[224:231], v[34:37], v192, v192 op_sel_hi:[0,0,0]
	s_setprio 1
	s_setprio 0
	v_mfma_scale_f32_16x16x128_f8f6f4 v[94:97], v[2:9], v[200:207], v[94:97], v192, v192 op_sel_hi:[0,0,0]
	v_mfma_scale_f32_16x16x128_f8f6f4 v[90:93], v[10:17], v[200:207], v[90:93], v192, v192 op_sel_hi:[0,0,0]
	v_mfma_scale_f32_16x16x128_f8f6f4 v[82:85], v[2:9], v[208:215], v[82:85], v192, v192 op_sel_hi:[0,0,0]
	v_mfma_scale_f32_16x16x128_f8f6f4 v[74:77], v[10:17], v[208:215], v[74:77], v192, v192 op_sel_hi:[0,0,0]
	v_mfma_scale_f32_16x16x128_f8f6f4 v[66:69], v[2:9], v[216:223], v[66:69], v192, v192 op_sel_hi:[0,0,0]
	v_mfma_scale_f32_16x16x128_f8f6f4 v[58:61], v[10:17], v[216:223], v[58:61], v192, v192 op_sel_hi:[0,0,0]
	v_mfma_scale_f32_16x16x128_f8f6f4 v[50:53], v[2:9], v[224:231], v[50:53], v192, v192 op_sel_hi:[0,0,0]
	v_mfma_scale_f32_16x16x128_f8f6f4 v[42:45], v[10:17], v[224:231], v[42:45], v192, v192 op_sel_hi:[0,0,0]
	s_setprio 1
	s_barrier
; #define PG8_STAGE(bufoff, gbase, voff) do { _Pragma("unroll") for (int _i = 0; _i < 2; ++_i) \
;         __builtin_amdgcn_global_load_lds((const unsigned*)((const char*)(gbase) + (voff)[_i]), (LAS unsigned*)(lds + (bufoff) + ldsw + _i * 8192), 16, 0, 0); } while (0)
; #define PG8_LDA(dst, b, h) do { if constexpr (F8) { _Pragma("unroll") for (int m = 0; m < 4; ++m) dst##8[m] = PG8_LD8(lds, PG8_SA(b, h) + aoff + m * 2048); } \
;         else { _Pragma("unroll") for (int m = 0; m < 4; ++m) _Pragma("unroll") for (int k = 0; k < 2; ++k) dst[m][k] = *(const LAS bf16x8*)(lds + PG8_SA(b, h) + aoff + m * 2048 + k * 1024); } } while (0)
; #define PG8_LDB(dst, b, h) do { if constexpr (F8) { _Pragma("unroll") for (int n = 0; n < 2; ++n) dst##8[n] = PG8_LD8(ldsB, PG8_SBR(b, h) + boff + n * 2048); } \
;         else { _Pragma("unroll") for (int n = 0; n < 2; ++n) _Pragma("unroll") for (int k = 0; k < 2; ++k) dst[n][k] = *(const LAS bf16x8*)(ldsB + PG8_SBR(b, h) + boff + n * 2048 + k * 1024); } } while (0)
; #define PG8_WAIT_V(n) asm volatile("s_waitcnt vmcnt(" #n ")" ::: "memory")
; #define PG8_WAIT_L(n) asm volatile("s_waitcnt lgkmcnt(" #n ")" ::: "memory")
; #define PG8_BAR __builtin_amdgcn_s_barrier()
; #define PG8_SCHED __builtin_amdgcn_sched_barrier(0)
; template <bool GATHER, bool F8, class Epi, class Sched>
; __device__ __forceinline__ void gemm_phase(LAS unsigned char* lds, const int nt, const unsigned lda, const unsigned ldb, const Sched& S, const Epi& E) {
;     ...
;             PG8_LDB(B0, 1, 0); PG8_LDB(B1, 1, 1); PG8_SCHED; PG8_LDA(At, 1, 0); PG8_STAGE(PG8_SA(0, 1), a2 + hA, w1);
;             PG8_WAIT_V(8); PG8_WAIT_L(0); PG8_BAR; PG8_MMA(0, 0, At, B0); PG8_MMA(0, 1, At, B1); PG8_BAR; PG8_SCHED;
;             PG8_LDA(At, 1, 1); PG8_STAGE(PG8_SB(1, 0), b3, voffB); PG8_STAGE(PG8_SB(1, 1), b3 + hB, voffB); PG8_STAGE(PG8_SA(1, 0), a3, w0);
;             PG8_WAIT_V(8); PG8_WAIT_L(0); PG8_BAR; PG8_MMA(1, 0, At, B0); PG8_MMA(1, 1, At, B1); PG8_BAR; PG8_SCHED;
;         }
;         if (wr == 0) PG8_BAR;
	ds_read_b128 v[2:5], v1 offset:32768
	ds_read_b128 v[6:9], v1 offset:33792
	ds_read_b128 v[10:13], v1 offset:34816
	ds_read_b128 v[14:17], v1 offset:35840
	ds_read_b128 v[18:21], v1 offset:49152
	ds_read_b128 v[22:25], v1 offset:50176
	ds_read_b128 v[26:29], v1 offset:51200
	ds_read_b128 v[30:33], v1 offset:52224
	s_add_u32 s28, s28, 0x40000
	s_addc_u32 s29, s29, 0
	s_mov_b32 m0, s43
	ds_read_b128 v[200:203], v191 offset:32768
	ds_read_b128 v[204:207], v191 offset:33792
	ds_read_b128 v[208:211], v191 offset:34816
	ds_read_b128 v[212:215], v191 offset:35840
	ds_read_b128 v[216:219], v191 offset:36864
	ds_read_b128 v[220:223], v191 offset:37888
	ds_read_b128 v[224:227], v191 offset:38912
	ds_read_b128 v[228:231], v191 offset:39936
	global_load_lds_dwordx4 v168, s[28:29]
	s_mov_b32 m0, s44
	s_nop 0
	global_load_lds_dwordx4 v164, s[28:29]
	s_waitcnt vmcnt(8)
	s_waitcnt lgkmcnt(0)
	s_barrier
	s_setprio 0
	s_waitcnt lgkmcnt(0)
	v_mfma_scale_f32_16x16x128_f8f6f4 v[158:161], v[2:9], v[200:207], v[158:161], v192, v192 op_sel_hi:[0,0,0]
	v_mfma_scale_f32_16x16x128_f8f6f4 v[150:153], v[10:17], v[200:207], v[150:153], v192, v192 op_sel_hi:[0,0,0]
	v_mfma_scale_f32_16x16x128_f8f6f4 v[142:145], v[2:9], v[208:215], v[142:145], v192, v192 op_sel_hi:[0,0,0]
	v_mfma_scale_f32_16x16x128_f8f6f4 v[134:137], v[10:17], v[208:215], v[134:137], v192, v192 op_sel_hi:[0,0,0]
	v_mfma_scale_f32_16x16x128_f8f6f4 v[126:129], v[2:9], v[216:223], v[126:129], v192, v192 op_sel_hi:[0,0,0]
	v_mfma_scale_f32_16x16x128_f8f6f4 v[118:121], v[10:17], v[216:223], v[118:121], v192, v192 op_sel_hi:[0,0,0]
	v_mfma_scale_f32_16x16x128_f8f6f4 v[110:113], v[2:9], v[224:231], v[110:113], v192, v192 op_sel_hi:[0,0,0]
	v_mfma_scale_f32_16x16x128_f8f6f4 v[102:105], v[10:17], v[224:231], v[102:105], v192, v192 op_sel_hi:[0,0,0]
	s_setprio 1
	s_setprio 0
	v_mfma_scale_f32_16x16x128_f8f6f4 v[154:157], v[18:25], v[200:207], v[154:157], v192, v192 op_sel_hi:[0,0,0]
	v_mfma_scale_f32_16x16x128_f8f6f4 v[146:149], v[26:33], v[200:207], v[146:149], v192, v192 op_sel_hi:[0,0,0]
	v_mfma_scale_f32_16x16x128_f8f6f4 v[138:141], v[18:25], v[208:215], v[138:141], v192, v192 op_sel_hi:[0,0,0]
	v_mfma_scale_f32_16x16x128_f8f6f4 v[130:133], v[26:33], v[208:215], v[130:133], v192, v192 op_sel_hi:[0,0,0]
	v_mfma_scale_f32_16x16x128_f8f6f4 v[122:125], v[18:25], v[216:223], v[122:125], v192, v192 op_sel_hi:[0,0,0]
	v_mfma_scale_f32_16x16x128_f8f6f4 v[114:117], v[26:33], v[216:223], v[114:117], v192, v192 op_sel_hi:[0,0,0]
	v_mfma_scale_f32_16x16x128_f8f6f4 v[106:109], v[18:25], v[224:231], v[106:109], v192, v192 op_sel_hi:[0,0,0]
	v_mfma_scale_f32_16x16x128_f8f6f4 v[98:101], v[26:33], v[224:231], v[98:101], v192, v192 op_sel_hi:[0,0,0]
	s_setprio 1
	s_barrier
	s_add_i32 m0, s45, 0xffffff80
	ds_read_b128 v[200:203], v191 offset:49152
	ds_read_b128 v[204:207], v191 offset:50176
	ds_read_b128 v[208:211], v191 offset:51200
	ds_read_b128 v[212:215], v191 offset:52224
	ds_read_b128 v[216:219], v191 offset:53248
	ds_read_b128 v[220:223], v191 offset:54272
	ds_read_b128 v[224:227], v191 offset:55296
	ds_read_b128 v[228:231], v191 offset:56320
	global_load_lds_dwordx4 v166, s[26:27] offset:128
	s_add_i32 m0, s46, 0xffffff80
	s_nop 0
	global_load_lds_dwordx4 v162, s[26:27] offset:128
	s_add_u32 s26, s26, 0x40080
	s_addc_u32 s27, s27, 0
	s_mov_b32 m0, s49
	s_nop 0
	global_load_lds_dwordx4 v166, s[26:27]
	s_mov_b32 m0, s50
	s_nop 0
	global_load_lds_dwordx4 v162, s[26:27]
	s_add_i32 m0, s47, 0xffffff80
	s_nop 0
	global_load_lds_dwordx4 v168, s[98:99] offset:128
	s_add_i32 m0, s48, 0xffffff80
	s_nop 0
	global_load_lds_dwordx4 v164, s[98:99] offset:128
	s_waitcnt vmcnt(8)
	s_waitcnt lgkmcnt(0)
	s_barrier
	s_setprio 0
	s_waitcnt lgkmcnt(0)
	v_mfma_scale_f32_16x16x128_f8f6f4 v[86:89], v[2:9], v[200:207], v[86:89], v192, v192 op_sel_hi:[0,0,0]
	v_mfma_scale_f32_16x16x128_f8f6f4 v[78:81], v[10:17], v[200:207], v[78:81], v192, v192 op_sel_hi:[0,0,0]
	v_mfma_scale_f32_16x16x128_f8f6f4 v[70:73], v[2:9], v[208:215], v[70:73], v192, v192 op_sel_hi:[0,0,0]
	v_mfma_scale_f32_16x16x128_f8f6f4 v[62:65], v[10:17], v[208:215], v[62:65], v192, v192 op_sel_hi:[0,0,0]
	v_mfma_scale_f32_16x16x128_f8f6f4 v[54:57], v[2:9], v[216:223], v[54:57], v192, v192 op_sel_hi:[0,0,0]
	v_mfma_scale_f32_16x16x128_f8f6f4 v[46:49], v[10:17], v[216:223], v[46:49], v192, v192 op_sel_hi:[0,0,0]
	v_mfma_scale_f32_16x16x128_f8f6f4 v[38:41], v[2:9], v[224:231], v[38:41], v192, v192 op_sel_hi:[0,0,0]
	v_mfma_scale_f32_16x16x128_f8f6f4 v[34:37], v[10:17], v[224:231], v[34:37], v192, v192 op_sel_hi:[0,0,0]
	s_setprio 1
	s_setprio 0
	v_mfma_scale_f32_16x16x128_f8f6f4 v[94:97], v[18:25], v[200:207], v[94:97], v192, v192 op_sel_hi:[0,0,0]
	v_mfma_scale_f32_16x16x128_f8f6f4 v[90:93], v[26:33], v[200:207], v[90:93], v192, v192 op_sel_hi:[0,0,0]
	v_mfma_scale_f32_16x16x128_f8f6f4 v[82:85], v[18:25], v[208:215], v[82:85], v192, v192 op_sel_hi:[0,0,0]
	v_mfma_scale_f32_16x16x128_f8f6f4 v[74:77], v[26:33], v[208:215], v[74:77], v192, v192 op_sel_hi:[0,0,0]
	v_mfma_scale_f32_16x16x128_f8f6f4 v[66:69], v[18:25], v[216:223], v[66:69], v192, v192 op_sel_hi:[0,0,0]
	v_mfma_scale_f32_16x16x128_f8f6f4 v[58:61], v[26:33], v[216:223], v[58:61], v192, v192 op_sel_hi:[0,0,0]
	v_mfma_scale_f32_16x16x128_f8f6f4 v[50:53], v[18:25], v[224:231], v[50:53], v192, v192 op_sel_hi:[0,0,0]
	v_mfma_scale_f32_16x16x128_f8f6f4 v[42:45], v[26:33], v[224:231], v[42:45], v192, v192 op_sel_hi:[0,0,0]
	s_setprio 1
	s_barrier
	s_add_i32 s55, s55, 2
	s_add_u32 s24, s24, 0x100
	s_addc_u32 s25, s25, 0
	s_add_u32 s30, s30, 0x100
	s_addc_u32 s54, s54, 0
	s_cmp_gt_u32 s55, 13
	s_cbranch_scc0 .LBB0_387
	s_and_b64 vcc, exec, s[10:11]
	s_cbranch_vccz .LBB0_390
	s_barrier

; #define PG8_STAGE(bufoff, gbase, voff) do { _Pragma("unroll") for (int _i = 0; _i < 2; ++_i) \
;         __builtin_amdgcn_global_load_lds((const unsigned*)((const char*)(gbase) + (voff)[_i]), (LAS unsigned*)(lds + (bufoff) + ldsw + _i * 8192), 16, 0, 0); } while (0)
; #define PG8_LDA(dst, b, h) do { if constexpr (F8) { _Pragma("unroll") for (int m = 0; m < 4; ++m) dst##8[m] = PG8_LD8(lds, PG8_SA(b, h) + aoff + m * 2048); } \
;         else { _Pragma("unroll") for (int m = 0; m < 4; ++m) _Pragma("unroll") for (int k = 0; k < 2; ++k) dst[m][k] = *(const LAS bf16x8*)(lds + PG8_SA(b, h) + aoff + m * 2048 + k * 1024); } } while (0)
; #define PG8_WAIT_V(n) asm volatile("s_waitcnt vmcnt(" #n ")" ::: "memory")
; #define PG8_WAIT_L(n) asm volatile("s_waitcnt lgkmcnt(" #n ")" ::: "memory")
; #define PG8_BAR __builtin_amdgcn_s_barrier()
; #define PG8_SCHED __builtin_amdgcn_sched_barrier(0)
; template <bool GATHER, bool F8, class Epi, class Sched>
; __device__ __forceinline__ void gemm_phase(LAS unsigned char* lds, const int nt, const unsigned lda, const unsigned ldb, const Sched& S, const Epi& E) {
;     ...
;         for (int t = 0; t < nt; t += 2) {
;             const bool last = (t == nt - 2);
;             const char* a1 = cA + (size_t)(t + 1) * kstep;
;             const char* a2 = last ? nA : cA + (size_t)(t + 2) * kstep; const char* b2 = last ? nB : cB + (size_t)(t + 2) * kstep;
;             const char* a3 = a2 + kstep; const char* b3 = b2 + kstep;
;             unsigned w0[2], w1[2];
;             if constexpr (GATHER) {
; #pragma unroll
;                 for (int i = 0; i < 2; ++i) { w0[i] = last ? vN0[i] : vA0[i]; w1[i] = last ? vN1[i] : vA1[i]; }
;             } else {
; #pragma unroll
;                 for (int i = 0; i < 2; ++i) { w0[i] = voffA[i]; w1[i] = voffA[i]; }
;             }
;             PG8_LDB(B0, 0, 0); PG8_LDB(B1, 0, 1); PG8_SCHED; PG8_LDA(At, 0, 0); PG8_STAGE(PG8_SA(1, 1), a1 + hA, vA1);
;             PG8_WAIT_V(8); PG8_WAIT_L(0); PG8_BAR; PG8_MMA(0, 0, At, B0); PG8_MMA(0, 1, At, B1); PG8_BAR; PG8_SCHED;
;             PG8_LDA(At, 0, 1); PG8_STAGE(PG8_SB(0, 0), b2, voffB); PG8_STAGE(PG8_SB(0, 1), b2 + hB, voffB); PG8_STAGE(PG8_SA(0, 0), a2, w0);
;             PG8_WAIT_V(8); PG8_WAIT_L(0); PG8_BAR; PG8_MMA(1, 0, At, B0); PG8_MMA(1, 1, At, B1); PG8_BAR; PG8_SCHED;
.LBB0_891:
	v_add_u32_e32 v3, s47, v199
	ds_read_b128 v[38:41], v3
	ds_read_b128 v[42:45], v3 offset:1024
	ds_read_b128 v[70:73], v3 offset:2048
	ds_read_b128 v[74:77], v3 offset:3072
	v_add_u32_e32 v3, s48, v199
	ds_read_b128 v[102:105], v3
	ds_read_b128 v[106:109], v3 offset:1024
	ds_read_b128 v[134:137], v3 offset:2048
	ds_read_b128 v[138:141], v3 offset:3072
	s_add_u32 s28, s26, 0xfff80080
	s_addc_u32 s29, s27, -1
	s_cmp_eq_u32 s52, 12
	s_cselect_b32 s31, s1, s29
	s_cselect_b32 s30, s0, s28
	s_cselect_b32 s29, s23, s34
	s_cselect_b32 s28, s22, s25
	s_add_i32 m0, s40, 0xc000
	ds_read_b128 v[158:161], v217
	ds_read_b128 v[162:165], v217 offset:1024
	ds_read_b128 v[174:177], v217 offset:2048
	ds_read_b128 v[178:181], v217 offset:3072
	ds_read_b128 v[182:185], v217 offset:4096
	ds_read_b128 v[186:189], v217 offset:5120
	ds_read_b128 v[190:193], v217 offset:6144
	ds_read_b128 v[194:197], v217 offset:7168
	global_load_lds_dwordx4 v208, s[26:27]
	s_add_i32 m0, s40, 0xe000
	s_nop 0
	global_load_lds_dwordx4 v210, s[26:27]
	s_waitcnt vmcnt(8)
	s_waitcnt lgkmcnt(0)
	s_barrier
	s_setprio 0
	s_waitcnt lgkmcnt(0)
	v_mfma_f32_16x16x32_bf16 v[66:69], v[38:41], v[158:161], v[66:69]
	v_mfma_f32_16x16x32_bf16 v[62:65], v[70:73], v[158:161], v[62:65]
	v_mfma_f32_16x16x32_bf16 v[98:101], v[38:41], v[174:177], v[98:101]
	v_mfma_f32_16x16x32_bf16 v[94:97], v[70:73], v[174:177], v[94:97]
	v_mfma_f32_16x16x32_bf16 v[122:125], v[38:41], v[182:185], v[122:125]
	v_mfma_f32_16x16x32_bf16 v[118:121], v[70:73], v[182:185], v[118:121]
	v_mfma_f32_16x16x32_bf16 v[130:133], v[38:41], v[190:193], v[130:133]
	v_mfma_f32_16x16x32_bf16 v[126:129], v[70:73], v[190:193], v[126:129]
	v_mfma_f32_16x16x32_bf16 v[66:69], v[42:45], v[162:165], v[66:69]
	v_mfma_f32_16x16x32_bf16 v[62:65], v[74:77], v[162:165], v[62:65]
	v_mfma_f32_16x16x32_bf16 v[98:101], v[42:45], v[178:181], v[98:101]
	v_mfma_f32_16x16x32_bf16 v[94:97], v[74:77], v[178:181], v[94:97]
	v_mfma_f32_16x16x32_bf16 v[122:125], v[42:45], v[186:189], v[122:125]
	v_mfma_f32_16x16x32_bf16 v[118:121], v[74:77], v[186:189], v[118:121]
	v_mfma_f32_16x16x32_bf16 v[130:133], v[42:45], v[194:197], v[130:133]
	v_mfma_f32_16x16x32_bf16 v[126:129], v[74:77], v[194:197], v[126:129]
	s_setprio 1
	s_setprio 0
	v_mfma_f32_16x16x32_bf16 v[170:173], v[102:105], v[158:161], v[170:173]
	v_mfma_f32_16x16x32_bf16 v[154:157], v[102:105], v[174:177], v[154:157]
	v_mfma_f32_16x16x32_bf16 v[150:153], v[134:137], v[174:177], v[150:153]
	v_mfma_f32_16x16x32_bf16 v[146:149], v[102:105], v[182:185], v[146:149]
	v_mfma_f32_16x16x32_bf16 v[142:145], v[134:137], v[182:185], v[142:145]
	v_mfma_f32_16x16x32_bf16 v[114:117], v[102:105], v[190:193], v[114:117]
	v_mfma_f32_16x16x32_bf16 v[110:113], v[134:137], v[190:193], v[110:113]
	v_mfma_f32_16x16x32_bf16 v[170:173], v[106:109], v[162:165], v[170:173]
	v_mfma_f32_16x16x32_bf16 v[158:161], v[134:137], v[158:161], v[166:169]
	v_mfma_f32_16x16x32_bf16 v[154:157], v[106:109], v[178:181], v[154:157]
	v_mfma_f32_16x16x32_bf16 v[150:153], v[138:141], v[178:181], v[150:153]
	v_mfma_f32_16x16x32_bf16 v[146:149], v[106:109], v[186:189], v[146:149]
	v_mfma_f32_16x16x32_bf16 v[142:145], v[138:141], v[186:189], v[142:145]
	v_mfma_f32_16x16x32_bf16 v[114:117], v[106:109], v[194:197], v[114:117]
	v_mfma_f32_16x16x32_bf16 v[110:113], v[138:141], v[194:197], v[110:113]
	v_mfma_f32_16x16x32_bf16 v[158:161], v[138:141], v[162:165], v[158:161]
	s_setprio 1
	s_barrier
	s_add_i32 s53, s47, s39
	s_mov_b32 m0, s53
	ds_read_b128 v[162:165], v217 offset:16384
	ds_read_b128 v[166:169], v217 offset:17408
	ds_read_b128 v[174:177], v217 offset:18432
	ds_read_b128 v[178:181], v217 offset:19456
	ds_read_b128 v[182:185], v217 offset:20480
	ds_read_b128 v[186:189], v217 offset:21504
	ds_read_b128 v[190:193], v217 offset:22528
	ds_read_b128 v[194:197], v217 offset:23552
	global_load_lds_dwordx4 v202, s[28:29]
	s_add_i32 m0, s53, 0x2000
	s_add_u32 s54, s28, 0x80000
	s_addc_u32 s55, s29, 0
	s_add_i32 s53, s48, s39
	global_load_lds_dwordx4 v206, s[28:29]
	s_mov_b32 m0, s53
	s_nop 0
	global_load_lds_dwordx4 v202, s[54:55]
	s_add_i32 m0, s53, 0x2000
	s_nop 0
	global_load_lds_dwordx4 v206, s[54:55]
	s_mov_b32 m0, s40
	s_nop 0
	s_mov_b64 s[98:99], s[30:31]
	global_load_lds_dwordx4 v200, s[30:31]
	s_mov_b32 m0, s41
	s_nop 0
	global_load_lds_dwordx4 v204, s[30:31]
	s_waitcnt vmcnt(8)
	s_waitcnt lgkmcnt(0)
	s_barrier
	s_setprio 0
	s_waitcnt lgkmcnt(0)
	v_mfma_f32_16x16x32_bf16 v[90:93], v[38:41], v[162:165], v[90:93]
	v_mfma_f32_16x16x32_bf16 v[86:89], v[70:73], v[162:165], v[86:89]
	v_mfma_f32_16x16x32_bf16 v[58:61], v[38:41], v[174:177], v[58:61]
	v_mfma_f32_16x16x32_bf16 v[54:57], v[70:73], v[174:177], v[54:57]
	v_mfma_f32_16x16x32_bf16 v[34:37], v[38:41], v[182:185], v[34:37]
	v_mfma_f32_16x16x32_bf16 v[30:33], v[70:73], v[182:185], v[30:33]
	v_mfma_f32_16x16x32_bf16 v[18:21], v[38:41], v[190:193], v[18:21]
	v_mfma_f32_16x16x32_bf16 v[14:17], v[70:73], v[190:193], v[14:17]
	v_mfma_f32_16x16x32_bf16 v[90:93], v[42:45], v[166:169], v[90:93]
	v_mfma_f32_16x16x32_bf16 v[86:89], v[74:77], v[166:169], v[86:89]
	v_mfma_f32_16x16x32_bf16 v[58:61], v[42:45], v[178:181], v[58:61]
	v_mfma_f32_16x16x32_bf16 v[54:57], v[74:77], v[178:181], v[54:57]
	v_mfma_f32_16x16x32_bf16 v[34:37], v[42:45], v[186:189], v[34:37]
	v_mfma_f32_16x16x32_bf16 v[30:33], v[74:77], v[186:189], v[30:33]
	v_mfma_f32_16x16x32_bf16 v[18:21], v[42:45], v[194:197], v[18:21]
	v_mfma_f32_16x16x32_bf16 v[14:17], v[74:77], v[194:197], v[14:17]
	s_setprio 1
	s_setprio 0
	v_mfma_f32_16x16x32_bf16 v[46:49], v[102:105], v[174:177], v[46:49]
	v_mfma_f32_16x16x32_bf16 v[50:53], v[134:137], v[174:177], v[50:53]
	v_mfma_f32_16x16x32_bf16 v[22:25], v[102:105], v[182:185], v[22:25]
	v_mfma_f32_16x16x32_bf16 v[26:29], v[134:137], v[182:185], v[26:29]
	v_mfma_f32_16x16x32_bf16 v[4:7], v[102:105], v[190:193], v[6:9]
	v_mfma_f32_16x16x32_bf16 v[8:11], v[134:137], v[190:193], v[10:13]
	v_mfma_f32_16x16x32_bf16 v[38:41], v[102:105], v[162:165], v[78:81]
	v_mfma_f32_16x16x32_bf16 v[42:45], v[134:137], v[162:165], v[82:85]
	v_mfma_f32_16x16x32_bf16 v[46:49], v[106:109], v[178:181], v[46:49]
	v_mfma_f32_16x16x32_bf16 v[50:53], v[138:141], v[178:181], v[50:53]
	v_mfma_f32_16x16x32_bf16 v[22:25], v[106:109], v[186:189], v[22:25]
	v_mfma_f32_16x16x32_bf16 v[26:29], v[138:141], v[186:189], v[26:29]
	v_mfma_f32_16x16x32_bf16 v[4:7], v[106:109], v[194:197], v[4:7]
	v_mfma_f32_16x16x32_bf16 v[10:13], v[138:141], v[194:197], v[8:11]
	v_mfma_f32_16x16x32_bf16 v[38:41], v[106:109], v[166:169], v[38:41]
	v_mfma_f32_16x16x32_bf16 v[42:45], v[138:141], v[166:169], v[42:45]
	s_setprio 1
	s_barrier
; #define PG8_STAGE(bufoff, gbase, voff) do { _Pragma("unroll") for (int _i = 0; _i < 2; ++_i) \
;         __builtin_amdgcn_global_load_lds((const unsigned*)((const char*)(gbase) + (voff)[_i]), (LAS unsigned*)(lds + (bufoff) + ldsw + _i * 8192), 16, 0, 0); } while (0)
; #define PG8_LDA(dst, b, h) do { if constexpr (F8) { _Pragma("unroll") for (int m = 0; m < 4; ++m) dst##8[m] = PG8_LD8(lds, PG8_SA(b, h) + aoff + m * 2048); } \
;         else { _Pragma("unroll") for (int m = 0; m < 4; ++m) _Pragma("unroll") for (int k = 0; k < 2; ++k) dst[m][k] = *(const LAS bf16x8*)(lds + PG8_SA(b, h) + aoff + m * 2048 + k * 1024); } } while (0)
; #define PG8_LDB(dst, b, h) do { if constexpr (F8) { _Pragma("unroll") for (int n = 0; n < 2; ++n) dst##8[n] = PG8_LD8(ldsB, PG8_SBR(b, h) + boff + n * 2048); } \
;         else { _Pragma("unroll") for (int n = 0; n < 2; ++n) _Pragma("unroll") for (int k = 0; k < 2; ++k) dst[n][k] = *(const LAS bf16x8*)(ldsB + PG8_SBR(b, h) + boff + n * 2048 + k * 1024); } } while (0)
; #define PG8_WAIT_V(n) asm volatile("s_waitcnt vmcnt(" #n ")" ::: "memory")
; #define PG8_WAIT_L(n) asm volatile("s_waitcnt lgkmcnt(" #n ")" ::: "memory")
; template <bool GATHER, bool F8, class Epi, class Sched>
; __device__ __forceinline__ void gemm_phase(LAS unsigned char* lds, const int nt, const unsigned lda, const unsigned ldb, const Sched& S, const Epi& E) {
;     ...
;             PG8_LDB(B0, 0, 0); PG8_LDB(B1, 0, 1); PG8_SCHED; PG8_LDA(At, 0, 0); PG8_STAGE(PG8_SA(1, 1), a1 + hA, vA1);
;             PG8_WAIT_V(8); PG8_WAIT_L(0); PG8_BAR; PG8_MMA(0, 0, At, B0); PG8_MMA(0, 1, At, B1); PG8_BAR; PG8_SCHED;
;             PG8_LDA(At, 0, 1); PG8_STAGE(PG8_SB(0, 0), b2, voffB); PG8_STAGE(PG8_SB(0, 1), b2 + hB, voffB); PG8_STAGE(PG8_SA(0, 0), a2, w0);
;             PG8_WAIT_V(8); PG8_WAIT_L(0); PG8_BAR; PG8_MMA(1, 0, At, B0); PG8_MMA(1, 1, At, B1); PG8_BAR; PG8_SCHED;
;             PG8_LDB(B0, 1, 0); PG8_LDB(B1, 1, 1); PG8_SCHED; PG8_LDA(At, 1, 0); PG8_STAGE(PG8_SA(0, 1), a2 + hA, w1);
;             PG8_WAIT_V(8); PG8_WAIT_L(0); PG8_BAR; PG8_MMA(0, 0, At, B0); PG8_MMA(0, 1, At, B1); PG8_BAR; PG8_SCHED;
;             PG8_LDA(At, 1, 1); PG8_STAGE(PG8_SB(1, 0), b3, voffB); PG8_STAGE(PG8_SB(1, 1), b3 + hB, voffB); PG8_STAGE(PG8_SA(1, 0), a3, w0);
;             PG8_WAIT_V(8); PG8_WAIT_L(0); PG8_BAR; PG8_MMA(1, 0, At, B0); PG8_MMA(1, 1, At, B1); PG8_BAR; PG8_SCHED;
	s_add_i32 s53, 0, 0x18000
	v_add_u32_e32 v3, s53, v199
	s_add_i32 s54, 0, 0x1c000
	ds_read_b128 v[70:73], v3
	ds_read_b128 v[74:77], v3 offset:1024
	ds_read_b128 v[78:81], v3 offset:2048
	ds_read_b128 v[82:85], v3 offset:3072
	v_add_u32_e32 v3, s54, v199
	ds_read_b128 v[102:105], v3
	ds_read_b128 v[106:109], v3 offset:1024
	ds_read_b128 v[134:137], v3 offset:2048
	ds_read_b128 v[138:141], v3 offset:3072
	s_add_u32 s30, s30, 0x80000
	s_addc_u32 s31, s31, 0
	s_mov_b32 m0, s42
	ds_read_b128 v[162:165], v217 offset:32768
	ds_read_b128 v[166:169], v217 offset:33792
	ds_read_b128 v[174:177], v217 offset:34816
	ds_read_b128 v[178:181], v217 offset:35840
	ds_read_b128 v[182:185], v217 offset:36864
	ds_read_b128 v[186:189], v217 offset:37888
	ds_read_b128 v[190:193], v217 offset:38912
	ds_read_b128 v[194:197], v217 offset:39936
	global_load_lds_dwordx4 v200, s[30:31]
	s_mov_b32 m0, s43
	s_nop 0
	global_load_lds_dwordx4 v204, s[30:31]
	s_waitcnt vmcnt(8)
	s_waitcnt lgkmcnt(0)
	s_barrier
	s_setprio 0
	s_waitcnt lgkmcnt(0)
	v_mfma_f32_16x16x32_bf16 v[66:69], v[70:73], v[162:165], v[66:69]
	v_mfma_f32_16x16x32_bf16 v[62:65], v[78:81], v[162:165], v[62:65]
	v_mfma_f32_16x16x32_bf16 v[98:101], v[70:73], v[174:177], v[98:101]
	v_mfma_f32_16x16x32_bf16 v[94:97], v[78:81], v[174:177], v[94:97]
	v_mfma_f32_16x16x32_bf16 v[122:125], v[70:73], v[182:185], v[122:125]
	v_mfma_f32_16x16x32_bf16 v[118:121], v[78:81], v[182:185], v[118:121]
	v_mfma_f32_16x16x32_bf16 v[130:133], v[70:73], v[190:193], v[130:133]
	v_mfma_f32_16x16x32_bf16 v[126:129], v[78:81], v[190:193], v[126:129]
	v_mfma_f32_16x16x32_bf16 v[66:69], v[74:77], v[166:169], v[66:69]
	v_mfma_f32_16x16x32_bf16 v[62:65], v[82:85], v[166:169], v[62:65]
	v_mfma_f32_16x16x32_bf16 v[98:101], v[74:77], v[178:181], v[98:101]
	v_mfma_f32_16x16x32_bf16 v[94:97], v[82:85], v[178:181], v[94:97]
	v_mfma_f32_16x16x32_bf16 v[122:125], v[74:77], v[186:189], v[122:125]
	v_mfma_f32_16x16x32_bf16 v[118:121], v[82:85], v[186:189], v[118:121]
	v_mfma_f32_16x16x32_bf16 v[130:133], v[74:77], v[194:197], v[130:133]
	v_mfma_f32_16x16x32_bf16 v[126:129], v[82:85], v[194:197], v[126:129]
	s_setprio 1
	s_setprio 0
	v_mfma_f32_16x16x32_bf16 v[170:173], v[102:105], v[162:165], v[170:173]
	v_mfma_f32_16x16x32_bf16 v[158:161], v[134:137], v[162:165], v[158:161]
	v_mfma_f32_16x16x32_bf16 v[154:157], v[102:105], v[174:177], v[154:157]
	v_mfma_f32_16x16x32_bf16 v[150:153], v[134:137], v[174:177], v[150:153]
	v_mfma_f32_16x16x32_bf16 v[146:149], v[102:105], v[182:185], v[146:149]
	v_mfma_f32_16x16x32_bf16 v[142:145], v[134:137], v[182:185], v[142:145]
	v_mfma_f32_16x16x32_bf16 v[114:117], v[102:105], v[190:193], v[114:117]
	v_mfma_f32_16x16x32_bf16 v[110:113], v[134:137], v[190:193], v[110:113]
	v_mfma_f32_16x16x32_bf16 v[170:173], v[106:109], v[166:169], v[170:173]
	v_mfma_f32_16x16x32_bf16 v[166:169], v[138:141], v[166:169], v[158:161]
	v_mfma_f32_16x16x32_bf16 v[154:157], v[106:109], v[178:181], v[154:157]
	v_mfma_f32_16x16x32_bf16 v[150:153], v[138:141], v[178:181], v[150:153]
	v_mfma_f32_16x16x32_bf16 v[146:149], v[106:109], v[186:189], v[146:149]
	v_mfma_f32_16x16x32_bf16 v[142:145], v[138:141], v[186:189], v[142:145]
	v_mfma_f32_16x16x32_bf16 v[114:117], v[106:109], v[194:197], v[114:117]
	v_mfma_f32_16x16x32_bf16 v[110:113], v[138:141], v[194:197], v[110:113]
	s_setprio 1
	s_barrier
	s_add_i32 s30, s53, s39
	s_add_i32 m0, s30, 0xffffff80
	ds_read_b128 v[158:161], v217 offset:49152
	ds_read_b128 v[162:165], v217 offset:50176
	ds_read_b128 v[174:177], v217 offset:51200
	ds_read_b128 v[178:181], v217 offset:52224
	ds_read_b128 v[182:185], v217 offset:53248
	ds_read_b128 v[186:189], v217 offset:54272
	ds_read_b128 v[190:193], v217 offset:55296
	ds_read_b128 v[194:197], v217 offset:56320
	global_load_lds_dwordx4 v202, s[28:29] offset:128
	s_add_i32 m0, s30, 0x1f80
	s_add_i32 s30, s54, s39
	global_load_lds_dwordx4 v206, s[28:29] offset:128
	s_add_u32 s28, s28, 0x80080
	s_addc_u32 s29, s29, 0
	s_mov_b32 m0, s30
	s_nop 0
	global_load_lds_dwordx4 v202, s[28:29]
	s_add_i32 m0, s30, 0x2000
	s_nop 0
	global_load_lds_dwordx4 v206, s[28:29]
	s_add_i32 m0, s45, 0xffffff80
	s_nop 0
	global_load_lds_dwordx4 v200, s[98:99] offset:128
	s_add_i32 m0, s46, 0xffffff80
	s_nop 0
	global_load_lds_dwordx4 v204, s[98:99] offset:128
	s_waitcnt vmcnt(8)
	s_waitcnt lgkmcnt(0)
	s_barrier
	s_setprio 0
	s_waitcnt lgkmcnt(0)
	v_mfma_f32_16x16x32_bf16 v[90:93], v[70:73], v[158:161], v[90:93]
	v_mfma_f32_16x16x32_bf16 v[86:89], v[78:81], v[158:161], v[86:89]
	v_mfma_f32_16x16x32_bf16 v[58:61], v[70:73], v[174:177], v[58:61]
	v_mfma_f32_16x16x32_bf16 v[54:57], v[78:81], v[174:177], v[54:57]
	v_mfma_f32_16x16x32_bf16 v[34:37], v[70:73], v[182:185], v[34:37]
	v_mfma_f32_16x16x32_bf16 v[30:33], v[78:81], v[182:185], v[30:33]
	v_mfma_f32_16x16x32_bf16 v[18:21], v[70:73], v[190:193], v[18:21]
	v_mfma_f32_16x16x32_bf16 v[14:17], v[78:81], v[190:193], v[14:17]
	v_mfma_f32_16x16x32_bf16 v[90:93], v[74:77], v[162:165], v[90:93]
	v_mfma_f32_16x16x32_bf16 v[86:89], v[82:85], v[162:165], v[86:89]
	v_mfma_f32_16x16x32_bf16 v[58:61], v[74:77], v[178:181], v[58:61]
	v_mfma_f32_16x16x32_bf16 v[54:57], v[82:85], v[178:181], v[54:57]
	v_mfma_f32_16x16x32_bf16 v[34:37], v[74:77], v[186:189], v[34:37]
	v_mfma_f32_16x16x32_bf16 v[30:33], v[82:85], v[186:189], v[30:33]
	v_mfma_f32_16x16x32_bf16 v[18:21], v[74:77], v[194:197], v[18:21]
	v_mfma_f32_16x16x32_bf16 v[14:17], v[82:85], v[194:197], v[14:17]
	s_setprio 1
	s_setprio 0
	v_mfma_f32_16x16x32_bf16 v[38:41], v[102:105], v[158:161], v[38:41]
	v_mfma_f32_16x16x32_bf16 v[78:81], v[106:109], v[162:165], v[38:41]
	v_mfma_f32_16x16x32_bf16 v[38:41], v[134:137], v[158:161], v[42:45]
	v_mfma_f32_16x16x32_bf16 v[82:85], v[138:141], v[162:165], v[38:41]
	v_mfma_f32_16x16x32_bf16 v[38:41], v[102:105], v[174:177], v[46:49]
	v_mfma_f32_16x16x32_bf16 v[46:49], v[106:109], v[178:181], v[38:41]
	v_mfma_f32_16x16x32_bf16 v[38:41], v[134:137], v[174:177], v[50:53]
	v_mfma_f32_16x16x32_bf16 v[22:25], v[102:105], v[182:185], v[22:25]
	v_mfma_f32_16x16x32_bf16 v[26:29], v[134:137], v[182:185], v[26:29]
	v_mfma_f32_16x16x32_bf16 v[4:7], v[102:105], v[190:193], v[4:7]
	v_mfma_f32_16x16x32_bf16 v[10:13], v[134:137], v[190:193], v[10:13]
	v_mfma_f32_16x16x32_bf16 v[50:53], v[138:141], v[178:181], v[38:41]
	v_mfma_f32_16x16x32_bf16 v[22:25], v[106:109], v[186:189], v[22:25]
	v_mfma_f32_16x16x32_bf16 v[26:29], v[138:141], v[186:189], v[26:29]
	v_mfma_f32_16x16x32_bf16 v[6:9], v[106:109], v[194:197], v[4:7]
	v_mfma_f32_16x16x32_bf16 v[10:13], v[138:141], v[194:197], v[10:13]
	s_setprio 1
	s_barrier
	s_add_i32 s52, s52, 2
	s_add_u32 s26, s26, 0x100
	s_addc_u32 s27, s27, 0
	s_add_u32 s25, s25, 0x100
	s_addc_u32 s34, s34, 0
	s_cmp_gt_u32 s52, 13
	s_cbranch_scc0 .LBB0_891
	s_and_b64 vcc, exec, s[12:13]
	s_cbranch_vccz .LBB0_894
	s_barrier

; #define PG8_STAGE(bufoff, gbase, voff) do { _Pragma("unroll") for (int _i = 0; _i < 2; ++_i) \
;         __builtin_amdgcn_global_load_lds((const unsigned*)((const char*)(gbase) + (voff)[_i]), (LAS unsigned*)(lds + (bufoff) + ldsw + _i * 8192), 16, 0, 0); } while (0)
; #define PG8_LDA(dst, b, h) do { if constexpr (F8) { _Pragma("unroll") for (int m = 0; m < 4; ++m) dst##8[m] = PG8_LD8(lds, PG8_SA(b, h) + aoff + m * 2048); } \
;         else { _Pragma("unroll") for (int m = 0; m < 4; ++m) _Pragma("unroll") for (int k = 0; k < 2; ++k) dst[m][k] = *(const LAS bf16x8*)(lds + PG8_SA(b, h) + aoff + m * 2048 + k * 1024); } } while (0)
; #define PG8_LDB(dst, b, h) do { if constexpr (F8) { _Pragma("unroll") for (int n = 0; n < 2; ++n) dst##8[n] = PG8_LD8(ldsB, PG8_SBR(b, h) + boff + n * 2048); } \
;         else { _Pragma("unroll") for (int n = 0; n < 2; ++n) _Pragma("unroll") for (int k = 0; k < 2; ++k) dst[n][k] = *(const LAS bf16x8*)(ldsB + PG8_SBR(b, h) + boff + n * 2048 + k * 1024); } } while (0)
; #define PG8_WAIT_V(n) asm volatile("s_waitcnt vmcnt(" #n ")" ::: "memory")
; #define PG8_WAIT_L(n) asm volatile("s_waitcnt lgkmcnt(" #n ")" ::: "memory")
; template <bool GATHER, bool F8, class Epi, class Sched>
; __device__ __forceinline__ void gemm_phase(LAS unsigned char* lds, const int nt, const unsigned lda, const unsigned ldb, const Sched& S, const Epi& E) {
;     ...
;             PG8_LDB(B0, 0, 0); PG8_LDB(B1, 0, 1); PG8_SCHED; PG8_LDA(At, 0, 0); PG8_STAGE(PG8_SA(1, 1), a1 + hA, vA1);
;             PG8_WAIT_V(8); PG8_WAIT_L(0); PG8_BAR; PG8_MMA(0, 0, At, B0); PG8_MMA(0, 1, At, B1); PG8_BAR; PG8_SCHED;
;             PG8_LDA(At, 0, 1); PG8_STAGE(PG8_SB(0, 0), b2, voffB); PG8_STAGE(PG8_SB(0, 1), b2 + hB, voffB); PG8_STAGE(PG8_SA(0, 0), a2, w0);
;             PG8_WAIT_V(8); PG8_WAIT_L(0); PG8_BAR; PG8_MMA(1, 0, At, B0); PG8_MMA(1, 1, At, B1); PG8_BAR; PG8_SCHED;
;             PG8_LDB(B0, 1, 0); PG8_LDB(B1, 1, 1); PG8_SCHED; PG8_LDA(At, 1, 0); PG8_STAGE(PG8_SA(0, 1), a2 + hA, w1);
;             PG8_WAIT_V(8); PG8_WAIT_L(0); PG8_BAR; PG8_MMA(0, 0, At, B0); PG8_MMA(0, 1, At, B1); PG8_BAR; PG8_SCHED;
;             PG8_LDA(At, 1, 1); PG8_STAGE(PG8_SB(1, 0), b3, voffB); PG8_STAGE(PG8_SB(1, 1), b3 + hB, voffB); PG8_STAGE(PG8_SA(1, 0), a3, w0);
;             PG8_WAIT_V(8); PG8_WAIT_L(0); PG8_BAR; PG8_MMA(1, 0, At, B0); PG8_MMA(1, 1, At, B1); PG8_BAR; PG8_SCHED;
.LBB0_1034:
	ds_read_b128 v[130:133], v209
	ds_read_b128 v[134:137], v209 offset:1024
	ds_read_b128 v[138:141], v209 offset:2048
	ds_read_b128 v[142:145], v209 offset:3072
	ds_read_b128 v[146:149], v210
	ds_read_b128 v[150:153], v210 offset:1024
	ds_read_b128 v[154:157], v210 offset:2048
	ds_read_b128 v[158:161], v210 offset:3072
	s_add_u32 s24, s22, 0xfff80080
	s_addc_u32 s25, s23, -1
	s_cmp_eq_u32 s48, 28
	s_cselect_b32 s27, s1, s25
	s_cselect_b32 s26, s0, s24
	s_cselect_b32 s25, s19, s28
	s_cselect_b32 s24, s18, s21
	s_add_i32 m0, s36, 0xc000
	ds_read_b128 v[162:165], v211
	ds_read_b128 v[166:169], v211 offset:1024
	ds_read_b128 v[170:173], v211 offset:2048
	ds_read_b128 v[174:177], v211 offset:3072
	ds_read_b128 v[194:197], v211 offset:4096
	ds_read_b128 v[200:203], v211 offset:5120
	ds_read_b128 v[204:207], v211 offset:6144
	ds_read_b128 v[214:217], v211 offset:7168
	global_load_lds_dwordx4 v186, s[22:23]
	s_add_i32 m0, s36, 0xe000
	s_nop 0
	global_load_lds_dwordx4 v188, s[22:23]
	s_waitcnt vmcnt(8)
	s_waitcnt lgkmcnt(0)
	s_barrier
	s_setprio 0
	s_waitcnt lgkmcnt(0)
	v_mfma_f32_16x16x32_bf16 v[126:129], v[130:133], v[162:165], v[126:129]
	v_mfma_f32_16x16x32_bf16 v[122:125], v[138:141], v[162:165], v[122:125]
	v_mfma_f32_16x16x32_bf16 v[110:113], v[130:133], v[170:173], v[110:113]
	v_mfma_f32_16x16x32_bf16 v[106:109], v[138:141], v[170:173], v[106:109]
	v_mfma_f32_16x16x32_bf16 v[94:97], v[130:133], v[194:197], v[94:97]
	v_mfma_f32_16x16x32_bf16 v[90:93], v[138:141], v[194:197], v[90:93]
	v_mfma_f32_16x16x32_bf16 v[78:81], v[130:133], v[204:207], v[78:81]
	v_mfma_f32_16x16x32_bf16 v[74:77], v[138:141], v[204:207], v[74:77]
	v_mfma_f32_16x16x32_bf16 v[126:129], v[134:137], v[166:169], v[126:129]
	v_mfma_f32_16x16x32_bf16 v[122:125], v[142:145], v[166:169], v[122:125]
	v_mfma_f32_16x16x32_bf16 v[110:113], v[134:137], v[174:177], v[110:113]
	v_mfma_f32_16x16x32_bf16 v[106:109], v[142:145], v[174:177], v[106:109]
	v_mfma_f32_16x16x32_bf16 v[94:97], v[134:137], v[200:203], v[94:97]
	v_mfma_f32_16x16x32_bf16 v[90:93], v[142:145], v[200:203], v[90:93]
	v_mfma_f32_16x16x32_bf16 v[78:81], v[134:137], v[214:217], v[78:81]
	v_mfma_f32_16x16x32_bf16 v[74:77], v[142:145], v[214:217], v[74:77]
	s_setprio 1
	s_setprio 0
	v_mfma_f32_16x16x32_bf16 v[118:121], v[146:149], v[162:165], v[118:121]
	v_mfma_f32_16x16x32_bf16 v[114:117], v[154:157], v[162:165], v[114:117]
	v_mfma_f32_16x16x32_bf16 v[102:105], v[146:149], v[170:173], v[102:105]
	v_mfma_f32_16x16x32_bf16 v[98:101], v[154:157], v[170:173], v[98:101]
	v_mfma_f32_16x16x32_bf16 v[86:89], v[146:149], v[194:197], v[86:89]
	v_mfma_f32_16x16x32_bf16 v[82:85], v[154:157], v[194:197], v[82:85]
	v_mfma_f32_16x16x32_bf16 v[70:73], v[146:149], v[204:207], v[70:73]
	v_mfma_f32_16x16x32_bf16 v[66:69], v[154:157], v[204:207], v[66:69]
	v_mfma_f32_16x16x32_bf16 v[118:121], v[150:153], v[166:169], v[118:121]
	v_mfma_f32_16x16x32_bf16 v[114:117], v[158:161], v[166:169], v[114:117]
	v_mfma_f32_16x16x32_bf16 v[102:105], v[150:153], v[174:177], v[102:105]
	v_mfma_f32_16x16x32_bf16 v[98:101], v[158:161], v[174:177], v[98:101]
	v_mfma_f32_16x16x32_bf16 v[86:89], v[150:153], v[200:203], v[86:89]
	v_mfma_f32_16x16x32_bf16 v[82:85], v[158:161], v[200:203], v[82:85]
	v_mfma_f32_16x16x32_bf16 v[70:73], v[150:153], v[214:217], v[70:73]
	v_mfma_f32_16x16x32_bf16 v[66:69], v[158:161], v[214:217], v[66:69]
	s_setprio 1
	s_barrier
	s_add_i32 s49, s44, s35
	s_mov_b32 m0, s49
	ds_read_b128 v[162:165], v211 offset:16384
	ds_read_b128 v[166:169], v211 offset:17408
	ds_read_b128 v[170:173], v211 offset:18432
	ds_read_b128 v[174:177], v211 offset:19456
	ds_read_b128 v[194:197], v211 offset:20480
	ds_read_b128 v[200:203], v211 offset:21504
	ds_read_b128 v[204:207], v211 offset:22528
	ds_read_b128 v[214:217], v211 offset:23552
	global_load_lds_dwordx4 v180, s[24:25]
	s_add_i32 m0, s49, 0x2000
	s_add_u32 s50, s24, 0x80000
	s_addc_u32 s51, s25, 0
	s_add_i32 s49, s45, s35
	global_load_lds_dwordx4 v184, s[24:25]
	s_mov_b32 m0, s49
	s_nop 0
	global_load_lds_dwordx4 v180, s[50:51]
	s_add_i32 m0, s49, 0x2000
	s_nop 0
	global_load_lds_dwordx4 v184, s[50:51]
	s_mov_b32 m0, s36
	s_nop 0
	s_mov_b64 s[98:99], s[26:27]
	global_load_lds_dwordx4 v178, s[26:27]
	s_mov_b32 m0, s37
	s_nop 0
	global_load_lds_dwordx4 v182, s[26:27]
	s_waitcnt vmcnt(8)
	s_waitcnt lgkmcnt(0)
	s_barrier
	s_setprio 0
	s_waitcnt lgkmcnt(0)
	v_mfma_f32_16x16x32_bf16 v[54:57], v[130:133], v[162:165], v[54:57]
	v_mfma_f32_16x16x32_bf16 v[50:53], v[138:141], v[162:165], v[50:53]
	v_mfma_f32_16x16x32_bf16 v[38:41], v[130:133], v[170:173], v[38:41]
	v_mfma_f32_16x16x32_bf16 v[34:37], v[138:141], v[170:173], v[34:37]
	v_mfma_f32_16x16x32_bf16 v[22:25], v[130:133], v[194:197], v[22:25]
	v_mfma_f32_16x16x32_bf16 v[18:21], v[138:141], v[194:197], v[18:21]
	v_mfma_f32_16x16x32_bf16 v[6:9], v[130:133], v[204:207], v[6:9]
	v_mfma_f32_16x16x32_bf16 v[2:5], v[138:141], v[204:207], v[2:5]
	v_mfma_f32_16x16x32_bf16 v[54:57], v[134:137], v[166:169], v[54:57]
	v_mfma_f32_16x16x32_bf16 v[50:53], v[142:145], v[166:169], v[50:53]
	v_mfma_f32_16x16x32_bf16 v[38:41], v[134:137], v[174:177], v[38:41]
	v_mfma_f32_16x16x32_bf16 v[34:37], v[142:145], v[174:177], v[34:37]
	v_mfma_f32_16x16x32_bf16 v[22:25], v[134:137], v[200:203], v[22:25]
	v_mfma_f32_16x16x32_bf16 v[18:21], v[142:145], v[200:203], v[18:21]
	v_mfma_f32_16x16x32_bf16 v[6:9], v[134:137], v[214:217], v[6:9]
	v_mfma_f32_16x16x32_bf16 v[2:5], v[142:145], v[214:217], v[2:5]
	s_setprio 1
	s_setprio 0
	v_mfma_f32_16x16x32_bf16 v[62:65], v[146:149], v[162:165], v[62:65]
	v_mfma_f32_16x16x32_bf16 v[58:61], v[154:157], v[162:165], v[58:61]
	v_mfma_f32_16x16x32_bf16 v[46:49], v[146:149], v[170:173], v[46:49]
	v_mfma_f32_16x16x32_bf16 v[42:45], v[154:157], v[170:173], v[42:45]
	v_mfma_f32_16x16x32_bf16 v[30:33], v[146:149], v[194:197], v[30:33]
	v_mfma_f32_16x16x32_bf16 v[26:29], v[154:157], v[194:197], v[26:29]
	v_mfma_f32_16x16x32_bf16 v[14:17], v[146:149], v[204:207], v[14:17]
	v_mfma_f32_16x16x32_bf16 v[10:13], v[154:157], v[204:207], v[10:13]
	v_mfma_f32_16x16x32_bf16 v[62:65], v[150:153], v[166:169], v[62:65]
	v_mfma_f32_16x16x32_bf16 v[58:61], v[158:161], v[166:169], v[58:61]
	v_mfma_f32_16x16x32_bf16 v[46:49], v[150:153], v[174:177], v[46:49]
	v_mfma_f32_16x16x32_bf16 v[42:45], v[158:161], v[174:177], v[42:45]
	v_mfma_f32_16x16x32_bf16 v[30:33], v[150:153], v[200:203], v[30:33]
	v_mfma_f32_16x16x32_bf16 v[26:29], v[158:161], v[200:203], v[26:29]
	v_mfma_f32_16x16x32_bf16 v[14:17], v[150:153], v[214:217], v[14:17]
	v_mfma_f32_16x16x32_bf16 v[10:13], v[158:161], v[214:217], v[10:13]
	s_setprio 1
	s_barrier
; #define PG8_STAGE(bufoff, gbase, voff) do { _Pragma("unroll") for (int _i = 0; _i < 2; ++_i) \
;         __builtin_amdgcn_global_load_lds((const unsigned*)((const char*)(gbase) + (voff)[_i]), (LAS unsigned*)(lds + (bufoff) + ldsw + _i * 8192), 16, 0, 0); } while (0)
; #define PG8_LDA(dst, b, h) do { if constexpr (F8) { _Pragma("unroll") for (int m = 0; m < 4; ++m) dst##8[m] = PG8_LD8(lds, PG8_SA(b, h) + aoff + m * 2048); } \
;         else { _Pragma("unroll") for (int m = 0; m < 4; ++m) _Pragma("unroll") for (int k = 0; k < 2; ++k) dst[m][k] = *(const LAS bf16x8*)(lds + PG8_SA(b, h) + aoff + m * 2048 + k * 1024); } } while (0)
; #define PG8_LDB(dst, b, h) do { if constexpr (F8) { _Pragma("unroll") for (int n = 0; n < 2; ++n) dst##8[n] = PG8_LD8(ldsB, PG8_SBR(b, h) + boff + n * 2048); } \
;         else { _Pragma("unroll") for (int n = 0; n < 2; ++n) _Pragma("unroll") for (int k = 0; k < 2; ++k) dst[n][k] = *(const LAS bf16x8*)(ldsB + PG8_SBR(b, h) + boff + n * 2048 + k * 1024); } } while (0)
; #define PG8_WAIT_V(n) asm volatile("s_waitcnt vmcnt(" #n ")" ::: "memory")
; #define PG8_WAIT_L(n) asm volatile("s_waitcnt lgkmcnt(" #n ")" ::: "memory")
; template <bool GATHER, bool F8, class Epi, class Sched>
; __device__ __forceinline__ void gemm_phase(LAS unsigned char* lds, const int nt, const unsigned lda, const unsigned ldb, const Sched& S, const Epi& E) {
;     ...
;             PG8_LDB(B0, 0, 0); PG8_LDB(B1, 0, 1); PG8_SCHED; PG8_LDA(At, 0, 0); PG8_STAGE(PG8_SA(1, 1), a1 + hA, vA1);
;             PG8_WAIT_V(8); PG8_WAIT_L(0); PG8_BAR; PG8_MMA(0, 0, At, B0); PG8_MMA(0, 1, At, B1); PG8_BAR; PG8_SCHED;
;             PG8_LDA(At, 0, 1); PG8_STAGE(PG8_SB(0, 0), b2, voffB); PG8_STAGE(PG8_SB(0, 1), b2 + hB, voffB); PG8_STAGE(PG8_SA(0, 0), a2, w0);
;             PG8_WAIT_V(8); PG8_WAIT_L(0); PG8_BAR; PG8_MMA(1, 0, At, B0); PG8_MMA(1, 1, At, B1); PG8_BAR; PG8_SCHED;
;             PG8_LDB(B0, 1, 0); PG8_LDB(B1, 1, 1); PG8_SCHED; PG8_LDA(At, 1, 0); PG8_STAGE(PG8_SA(0, 1), a2 + hA, w1);
;             PG8_WAIT_V(8); PG8_WAIT_L(0); PG8_BAR; PG8_MMA(0, 0, At, B0); PG8_MMA(0, 1, At, B1); PG8_BAR; PG8_SCHED;
;             PG8_LDA(At, 1, 1); PG8_STAGE(PG8_SB(1, 0), b3, voffB); PG8_STAGE(PG8_SB(1, 1), b3 + hB, voffB); PG8_STAGE(PG8_SA(1, 0), a3, w0);
;             PG8_WAIT_V(8); PG8_WAIT_L(0); PG8_BAR; PG8_MMA(1, 0, At, B0); PG8_MMA(1, 1, At, B1); PG8_BAR; PG8_SCHED;
	s_add_i32 s49, 0, 0x18000
	s_add_i32 s50, 0, 0x1c000
	v_add_u32_e32 v142, s49, v199
	v_add_u32_e32 v158, s50, v199
	ds_read_b128 v[130:133], v142
	ds_read_b128 v[134:137], v142 offset:1024
	ds_read_b128 v[138:141], v142 offset:2048
	ds_read_b128 v[142:145], v142 offset:3072
	ds_read_b128 v[146:149], v158
	ds_read_b128 v[150:153], v158 offset:1024
	ds_read_b128 v[154:157], v158 offset:2048
	ds_read_b128 v[158:161], v158 offset:3072
	s_add_u32 s26, s26, 0x80000
	s_addc_u32 s27, s27, 0
	s_mov_b32 m0, s38
	ds_read_b128 v[162:165], v211 offset:32768
	ds_read_b128 v[166:169], v211 offset:33792
	ds_read_b128 v[170:173], v211 offset:34816
	ds_read_b128 v[174:177], v211 offset:35840
	ds_read_b128 v[194:197], v211 offset:36864
	ds_read_b128 v[200:203], v211 offset:37888
	ds_read_b128 v[204:207], v211 offset:38912
	ds_read_b128 v[214:217], v211 offset:39936
	global_load_lds_dwordx4 v178, s[26:27]
	s_mov_b32 m0, s39
	s_nop 0
	global_load_lds_dwordx4 v182, s[26:27]
	s_waitcnt vmcnt(8)
	s_waitcnt lgkmcnt(0)
	s_barrier
	s_setprio 0
	s_waitcnt lgkmcnt(0)
	v_mfma_f32_16x16x32_bf16 v[126:129], v[130:133], v[162:165], v[126:129]
	v_mfma_f32_16x16x32_bf16 v[122:125], v[138:141], v[162:165], v[122:125]
	v_mfma_f32_16x16x32_bf16 v[110:113], v[130:133], v[170:173], v[110:113]
	v_mfma_f32_16x16x32_bf16 v[106:109], v[138:141], v[170:173], v[106:109]
	v_mfma_f32_16x16x32_bf16 v[94:97], v[130:133], v[194:197], v[94:97]
	v_mfma_f32_16x16x32_bf16 v[90:93], v[138:141], v[194:197], v[90:93]
	v_mfma_f32_16x16x32_bf16 v[78:81], v[130:133], v[204:207], v[78:81]
	v_mfma_f32_16x16x32_bf16 v[74:77], v[138:141], v[204:207], v[74:77]
	v_mfma_f32_16x16x32_bf16 v[126:129], v[134:137], v[166:169], v[126:129]
	v_mfma_f32_16x16x32_bf16 v[122:125], v[142:145], v[166:169], v[122:125]
	v_mfma_f32_16x16x32_bf16 v[110:113], v[134:137], v[174:177], v[110:113]
	v_mfma_f32_16x16x32_bf16 v[106:109], v[142:145], v[174:177], v[106:109]
	v_mfma_f32_16x16x32_bf16 v[94:97], v[134:137], v[200:203], v[94:97]
	v_mfma_f32_16x16x32_bf16 v[90:93], v[142:145], v[200:203], v[90:93]
	v_mfma_f32_16x16x32_bf16 v[78:81], v[134:137], v[214:217], v[78:81]
	v_mfma_f32_16x16x32_bf16 v[74:77], v[142:145], v[214:217], v[74:77]
	s_setprio 1
	s_setprio 0
	v_mfma_f32_16x16x32_bf16 v[118:121], v[146:149], v[162:165], v[118:121]
	v_mfma_f32_16x16x32_bf16 v[114:117], v[154:157], v[162:165], v[114:117]
	v_mfma_f32_16x16x32_bf16 v[102:105], v[146:149], v[170:173], v[102:105]
	v_mfma_f32_16x16x32_bf16 v[98:101], v[154:157], v[170:173], v[98:101]
	v_mfma_f32_16x16x32_bf16 v[86:89], v[146:149], v[194:197], v[86:89]
	v_mfma_f32_16x16x32_bf16 v[82:85], v[154:157], v[194:197], v[82:85]
	v_mfma_f32_16x16x32_bf16 v[70:73], v[146:149], v[204:207], v[70:73]
	v_mfma_f32_16x16x32_bf16 v[66:69], v[154:157], v[204:207], v[66:69]
	v_mfma_f32_16x16x32_bf16 v[118:121], v[150:153], v[166:169], v[118:121]
	v_mfma_f32_16x16x32_bf16 v[114:117], v[158:161], v[166:169], v[114:117]
	v_mfma_f32_16x16x32_bf16 v[102:105], v[150:153], v[174:177], v[102:105]
	v_mfma_f32_16x16x32_bf16 v[98:101], v[158:161], v[174:177], v[98:101]
	v_mfma_f32_16x16x32_bf16 v[86:89], v[150:153], v[200:203], v[86:89]
	v_mfma_f32_16x16x32_bf16 v[82:85], v[158:161], v[200:203], v[82:85]
	v_mfma_f32_16x16x32_bf16 v[70:73], v[150:153], v[214:217], v[70:73]
	v_mfma_f32_16x16x32_bf16 v[66:69], v[158:161], v[214:217], v[66:69]
	s_setprio 1
	s_barrier
	s_add_i32 s26, s49, s35
	s_add_i32 m0, s26, 0xffffff80
	ds_read_b128 v[162:165], v211 offset:49152
	ds_read_b128 v[166:169], v211 offset:50176
	ds_read_b128 v[170:173], v211 offset:51200
	ds_read_b128 v[174:177], v211 offset:52224
	ds_read_b128 v[194:197], v211 offset:53248
	ds_read_b128 v[200:203], v211 offset:54272
	ds_read_b128 v[204:207], v211 offset:55296
	ds_read_b128 v[214:217], v211 offset:56320
	global_load_lds_dwordx4 v180, s[24:25] offset:128
	s_add_i32 m0, s26, 0x1f80
	s_add_i32 s26, s50, s35
	global_load_lds_dwordx4 v184, s[24:25] offset:128
	s_add_u32 s24, s24, 0x80080
	s_addc_u32 s25, s25, 0
	s_mov_b32 m0, s26
	s_nop 0
	global_load_lds_dwordx4 v180, s[24:25]
	s_add_i32 m0, s26, 0x2000
	s_nop 0
	global_load_lds_dwordx4 v184, s[24:25]
	s_add_i32 m0, s41, 0xffffff80
	s_nop 0
	global_load_lds_dwordx4 v178, s[98:99] offset:128
	s_add_i32 m0, s42, 0xffffff80
	s_nop 0
	global_load_lds_dwordx4 v182, s[98:99] offset:128
	s_waitcnt vmcnt(8)
	s_waitcnt lgkmcnt(0)
	s_barrier
	s_setprio 0
	s_waitcnt lgkmcnt(0)
	v_mfma_f32_16x16x32_bf16 v[54:57], v[130:133], v[162:165], v[54:57]
	v_mfma_f32_16x16x32_bf16 v[50:53], v[138:141], v[162:165], v[50:53]
	v_mfma_f32_16x16x32_bf16 v[38:41], v[130:133], v[170:173], v[38:41]
	v_mfma_f32_16x16x32_bf16 v[34:37], v[138:141], v[170:173], v[34:37]
	v_mfma_f32_16x16x32_bf16 v[22:25], v[130:133], v[194:197], v[22:25]
	v_mfma_f32_16x16x32_bf16 v[18:21], v[138:141], v[194:197], v[18:21]
	v_mfma_f32_16x16x32_bf16 v[6:9], v[130:133], v[204:207], v[6:9]
	v_mfma_f32_16x16x32_bf16 v[2:5], v[138:141], v[204:207], v[2:5]
	v_mfma_f32_16x16x32_bf16 v[54:57], v[134:137], v[166:169], v[54:57]
	v_mfma_f32_16x16x32_bf16 v[50:53], v[142:145], v[166:169], v[50:53]
	v_mfma_f32_16x16x32_bf16 v[38:41], v[134:137], v[174:177], v[38:41]
	v_mfma_f32_16x16x32_bf16 v[34:37], v[142:145], v[174:177], v[34:37]
	v_mfma_f32_16x16x32_bf16 v[22:25], v[134:137], v[200:203], v[22:25]
	v_mfma_f32_16x16x32_bf16 v[18:21], v[142:145], v[200:203], v[18:21]
	v_mfma_f32_16x16x32_bf16 v[6:9], v[134:137], v[214:217], v[6:9]
	v_mfma_f32_16x16x32_bf16 v[2:5], v[142:145], v[214:217], v[2:5]
	s_setprio 1
	s_setprio 0
	v_mfma_f32_16x16x32_bf16 v[62:65], v[146:149], v[162:165], v[62:65]
	v_mfma_f32_16x16x32_bf16 v[58:61], v[154:157], v[162:165], v[58:61]
	v_mfma_f32_16x16x32_bf16 v[46:49], v[146:149], v[170:173], v[46:49]
	v_mfma_f32_16x16x32_bf16 v[42:45], v[154:157], v[170:173], v[42:45]
	v_mfma_f32_16x16x32_bf16 v[30:33], v[146:149], v[194:197], v[30:33]
	v_mfma_f32_16x16x32_bf16 v[26:29], v[154:157], v[194:197], v[26:29]
	v_mfma_f32_16x16x32_bf16 v[14:17], v[146:149], v[204:207], v[14:17]
	v_mfma_f32_16x16x32_bf16 v[10:13], v[154:157], v[204:207], v[10:13]
	v_mfma_f32_16x16x32_bf16 v[62:65], v[150:153], v[166:169], v[62:65]
	v_mfma_f32_16x16x32_bf16 v[58:61], v[158:161], v[166:169], v[58:61]
	v_mfma_f32_16x16x32_bf16 v[46:49], v[150:153], v[174:177], v[46:49]
	v_mfma_f32_16x16x32_bf16 v[42:45], v[158:161], v[174:177], v[42:45]
	v_mfma_f32_16x16x32_bf16 v[30:33], v[150:153], v[200:203], v[30:33]
	v_mfma_f32_16x16x32_bf16 v[26:29], v[158:161], v[200:203], v[26:29]
	v_mfma_f32_16x16x32_bf16 v[14:17], v[150:153], v[214:217], v[14:17]
	v_mfma_f32_16x16x32_bf16 v[10:13], v[158:161], v[214:217], v[10:13]
	s_setprio 1
	s_barrier
	s_add_i32 s48, s48, 2
	s_add_u32 s22, s22, 0x100
	s_addc_u32 s23, s23, 0
	s_add_u32 s21, s21, 0x100
	s_addc_u32 s28, s28, 0
	s_cmp_gt_u32 s48, 29
	s_cbranch_scc0 .LBB0_1034
	s_and_b64 vcc, exec, s[16:17]
	s_cbranch_vccz .LBB0_1037
	s_barrier

; #define PG8_STAGE(bufoff, gbase, voff) do { _Pragma("unroll") for (int _i = 0; _i < 2; ++_i) \
;         __builtin_amdgcn_global_load_lds((const unsigned*)((const char*)(gbase) + (voff)[_i]), (LAS unsigned*)(lds + (bufoff) + ldsw + _i * 8192), 16, 0, 0); } while (0)
; #define PG8_LDA(dst, b, h) do { if constexpr (F8) { _Pragma("unroll") for (int m = 0; m < 4; ++m) dst##8[m] = PG8_LD8(lds, PG8_SA(b, h) + aoff + m * 2048); } \
;         else { _Pragma("unroll") for (int m = 0; m < 4; ++m) _Pragma("unroll") for (int k = 0; k < 2; ++k) dst[m][k] = *(const LAS bf16x8*)(lds + PG8_SA(b, h) + aoff + m * 2048 + k * 1024); } } while (0)
; #define PG8_LDB(dst, b, h) do { if constexpr (F8) { _Pragma("unroll") for (int n = 0; n < 2; ++n) dst##8[n] = PG8_LD8(ldsB, PG8_SBR(b, h) + boff + n * 2048); } \
;         else { _Pragma("unroll") for (int n = 0; n < 2; ++n) _Pragma("unroll") for (int k = 0; k < 2; ++k) dst[n][k] = *(const LAS bf16x8*)(ldsB + PG8_SBR(b, h) + boff + n * 2048 + k * 1024); } } while (0)
; #define PG8_WAIT_V(n) asm volatile("s_waitcnt vmcnt(" #n ")" ::: "memory")
; #define PG8_WAIT_L(n) asm volatile("s_waitcnt lgkmcnt(" #n ")" ::: "memory")
; template <bool GATHER, bool F8, class Epi, class Sched>
; __device__ __forceinline__ void gemm_phase(LAS unsigned char* lds, const int nt, const unsigned lda, const unsigned ldb, const Sched& S, const Epi& E) {
;     ...
;             PG8_LDB(B0, 0, 0); PG8_LDB(B1, 0, 1); PG8_SCHED; PG8_LDA(At, 0, 0); PG8_STAGE(PG8_SA(1, 1), a1 + hA, vA1);
;             PG8_WAIT_V(8); PG8_WAIT_L(0); PG8_BAR; PG8_MMA(0, 0, At, B0); PG8_MMA(0, 1, At, B1); PG8_BAR; PG8_SCHED;
;             PG8_LDA(At, 0, 1); PG8_STAGE(PG8_SB(0, 0), b2, voffB); PG8_STAGE(PG8_SB(0, 1), b2 + hB, voffB); PG8_STAGE(PG8_SA(0, 0), a2, w0);
;             PG8_WAIT_V(8); PG8_WAIT_L(0); PG8_BAR; PG8_MMA(1, 0, At, B0); PG8_MMA(1, 1, At, B1); PG8_BAR; PG8_SCHED;
;             PG8_LDB(B0, 1, 0); PG8_LDB(B1, 1, 1); PG8_SCHED; PG8_LDA(At, 1, 0); PG8_STAGE(PG8_SA(0, 1), a2 + hA, w1);
;             PG8_WAIT_V(8); PG8_WAIT_L(0); PG8_BAR; PG8_MMA(0, 0, At, B0); PG8_MMA(0, 1, At, B1); PG8_BAR; PG8_SCHED;
;             PG8_LDA(At, 1, 1); PG8_STAGE(PG8_SB(1, 0), b3, voffB); PG8_STAGE(PG8_SB(1, 1), b3 + hB, voffB); PG8_STAGE(PG8_SA(1, 0), a3, w0);
;             PG8_WAIT_V(8); PG8_WAIT_L(0); PG8_BAR; PG8_MMA(1, 0, At, B0); PG8_MMA(1, 1, At, B1); PG8_BAR; PG8_SCHED;
.LBB0_1152:
	ds_read_b128 v[152:155], v146
	ds_read_b128 v[156:159], v146 offset:1024
	ds_read_b128 v[160:163], v146 offset:2048
	ds_read_b128 v[164:167], v146 offset:3072
	ds_read_b128 v[168:171], v148
	ds_read_b128 v[172:175], v148 offset:1024
	ds_read_b128 v[176:179], v148 offset:2048
	ds_read_b128 v[180:183], v148 offset:3072
	s_add_u32 s12, s0, s10
	s_addc_u32 s13, s1, s11
	s_add_u32 s12, s12, 0x100
	s_addc_u32 s13, s13, 0
	s_add_u32 s38, s24, s10
	s_addc_u32 s39, s25, s11
	s_cmpk_eq_i32 s10, 0xf00
	s_cselect_b32 s15, s1, s13
	s_cselect_b32 s14, s0, s12
	s_cselect_b32 s13, s7, s39
	s_cselect_b32 s12, s6, s38
	s_mov_b32 m0, s27
	v_lshl_add_u64 v[196:197], v[140:141], 0, s[10:11]
	ds_read_b128 v[184:187], v149
	ds_read_b128 v[188:191], v149 offset:1024
	ds_read_b128 v[192:195], v149 offset:2048
	ds_read_b128 v[200:203], v149 offset:3072
	ds_read_b128 v[204:207], v149 offset:4096
	ds_read_b128 v[208:211], v149 offset:5120
	ds_read_b128 v[212:215], v149 offset:6144
	ds_read_b128 v[216:219], v149 offset:7168
	global_load_lds_dwordx4 v[196:197], off
	v_lshl_add_u64 v[196:197], v[142:143], 0, s[10:11]
	s_mov_b32 m0, s28
	s_nop 0
	global_load_lds_dwordx4 v[196:197], off
	s_waitcnt vmcnt(8)
	s_waitcnt lgkmcnt(0)
	s_barrier
	s_setprio 0
	s_waitcnt lgkmcnt(0)
	v_mfma_f32_16x16x32_bf16 v[126:129], v[152:155], v[184:187], v[126:129]
	v_mfma_f32_16x16x32_bf16 v[122:125], v[160:163], v[184:187], v[122:125]
	v_mfma_f32_16x16x32_bf16 v[114:117], v[152:155], v[192:195], v[114:117]
	v_mfma_f32_16x16x32_bf16 v[106:109], v[160:163], v[192:195], v[106:109]
	v_mfma_f32_16x16x32_bf16 v[98:101], v[152:155], v[204:207], v[98:101]
	v_mfma_f32_16x16x32_bf16 v[90:93], v[160:163], v[204:207], v[90:93]
	v_mfma_f32_16x16x32_bf16 v[82:85], v[152:155], v[212:215], v[82:85]
	v_mfma_f32_16x16x32_bf16 v[74:77], v[160:163], v[212:215], v[74:77]
	v_mfma_f32_16x16x32_bf16 v[126:129], v[156:159], v[188:191], v[126:129]
	v_mfma_f32_16x16x32_bf16 v[122:125], v[164:167], v[188:191], v[122:125]
	v_mfma_f32_16x16x32_bf16 v[114:117], v[156:159], v[200:203], v[114:117]
	v_mfma_f32_16x16x32_bf16 v[106:109], v[164:167], v[200:203], v[106:109]
	v_mfma_f32_16x16x32_bf16 v[98:101], v[156:159], v[208:211], v[98:101]
	v_mfma_f32_16x16x32_bf16 v[90:93], v[164:167], v[208:211], v[90:93]
	v_mfma_f32_16x16x32_bf16 v[82:85], v[156:159], v[216:219], v[82:85]
	v_mfma_f32_16x16x32_bf16 v[74:77], v[164:167], v[216:219], v[74:77]
	s_setprio 1
	s_setprio 0
	v_mfma_f32_16x16x32_bf16 v[118:121], v[168:171], v[184:187], v[118:121]
	v_mfma_f32_16x16x32_bf16 v[110:113], v[176:179], v[184:187], v[110:113]
	v_mfma_f32_16x16x32_bf16 v[102:105], v[168:171], v[192:195], v[102:105]
	v_mfma_f32_16x16x32_bf16 v[94:97], v[176:179], v[192:195], v[94:97]
	v_mfma_f32_16x16x32_bf16 v[86:89], v[168:171], v[204:207], v[86:89]
	v_mfma_f32_16x16x32_bf16 v[78:81], v[176:179], v[204:207], v[78:81]
	v_mfma_f32_16x16x32_bf16 v[62:65], v[168:171], v[212:215], v[62:65]
	v_mfma_f32_16x16x32_bf16 v[58:61], v[176:179], v[212:215], v[58:61]
	v_mfma_f32_16x16x32_bf16 v[118:121], v[172:175], v[188:191], v[118:121]
	v_mfma_f32_16x16x32_bf16 v[110:113], v[180:183], v[188:191], v[110:113]
	v_mfma_f32_16x16x32_bf16 v[102:105], v[172:175], v[200:203], v[102:105]
	v_mfma_f32_16x16x32_bf16 v[94:97], v[180:183], v[200:203], v[94:97]
	v_mfma_f32_16x16x32_bf16 v[86:89], v[172:175], v[208:211], v[86:89]
	v_mfma_f32_16x16x32_bf16 v[78:81], v[180:183], v[208:211], v[78:81]
	v_mfma_f32_16x16x32_bf16 v[62:65], v[172:175], v[216:219], v[62:65]
	v_mfma_f32_16x16x32_bf16 v[58:61], v[180:183], v[216:219], v[58:61]
	s_setprio 1
	s_barrier
	s_mov_b32 m0, s29
	v_lshl_add_u64 v[196:197], s[12:13], 0, v[134:135]
	s_add_u32 s38, s12, 0x80000
	ds_read_b128 v[184:187], v149 offset:16384
	ds_read_b128 v[188:191], v149 offset:17408
	ds_read_b128 v[192:195], v149 offset:18432
	ds_read_b128 v[200:203], v149 offset:19456
	ds_read_b128 v[204:207], v149 offset:20480
	ds_read_b128 v[208:211], v149 offset:21504
	ds_read_b128 v[212:215], v149 offset:22528
	ds_read_b128 v[216:219], v149 offset:23552
	global_load_lds_dwordx4 v[196:197], off
	v_lshl_add_u64 v[220:221], s[12:13], 0, v[138:139]
	s_mov_b32 m0, s30
	s_addc_u32 s39, s13, 0
	global_load_lds_dwordx4 v[220:221], off
	v_lshl_add_u64 v[222:223], s[38:39], 0, v[134:135]
	s_mov_b32 m0, s31
	v_lshl_add_u64 v[224:225], s[14:15], 0, v[136:137]
	global_load_lds_dwordx4 v[222:223], off
	v_lshl_add_u64 v[222:223], s[38:39], 0, v[138:139]
	s_mov_b32 m0, s33
	s_nop 0
	global_load_lds_dwordx4 v[222:223], off
	v_lshl_add_u64 v[222:223], s[14:15], 0, v[132:133]
	s_mov_b32 m0, s3
	s_nop 0
	global_load_lds_dwordx4 v[222:223], off
	s_mov_b32 m0, s19
	s_nop 0
	global_load_lds_dwordx4 v[224:225], off
	s_waitcnt vmcnt(8)
	s_waitcnt lgkmcnt(0)
	s_barrier
; #define PG8_STAGE(bufoff, gbase, voff) do { _Pragma("unroll") for (int _i = 0; _i < 2; ++_i) \
;         __builtin_amdgcn_global_load_lds((const unsigned*)((const char*)(gbase) + (voff)[_i]), (LAS unsigned*)(lds + (bufoff) + ldsw + _i * 8192), 16, 0, 0); } while (0)
; #define PG8_LDA(dst, b, h) do { if constexpr (F8) { _Pragma("unroll") for (int m = 0; m < 4; ++m) dst##8[m] = PG8_LD8(lds, PG8_SA(b, h) + aoff + m * 2048); } \
;         else { _Pragma("unroll") for (int m = 0; m < 4; ++m) _Pragma("unroll") for (int k = 0; k < 2; ++k) dst[m][k] = *(const LAS bf16x8*)(lds + PG8_SA(b, h) + aoff + m * 2048 + k * 1024); } } while (0)
; #define PG8_LDB(dst, b, h) do { if constexpr (F8) { _Pragma("unroll") for (int n = 0; n < 2; ++n) dst##8[n] = PG8_LD8(ldsB, PG8_SBR(b, h) + boff + n * 2048); } \
;         else { _Pragma("unroll") for (int n = 0; n < 2; ++n) _Pragma("unroll") for (int k = 0; k < 2; ++k) dst[n][k] = *(const LAS bf16x8*)(ldsB + PG8_SBR(b, h) + boff + n * 2048 + k * 1024); } } while (0)
; #define PG8_WAIT_V(n) asm volatile("s_waitcnt vmcnt(" #n ")" ::: "memory")
; #define PG8_WAIT_L(n) asm volatile("s_waitcnt lgkmcnt(" #n ")" ::: "memory")
; template <bool GATHER, bool F8, class Epi, class Sched>
; __device__ __forceinline__ void gemm_phase(LAS unsigned char* lds, const int nt, const unsigned lda, const unsigned ldb, const Sched& S, const Epi& E) {
;     ...
;             PG8_LDB(B0, 0, 0); PG8_LDB(B1, 0, 1); PG8_SCHED; PG8_LDA(At, 0, 0); PG8_STAGE(PG8_SA(1, 1), a1 + hA, vA1);
;             PG8_WAIT_V(8); PG8_WAIT_L(0); PG8_BAR; PG8_MMA(0, 0, At, B0); PG8_MMA(0, 1, At, B1); PG8_BAR; PG8_SCHED;
;             PG8_LDA(At, 0, 1); PG8_STAGE(PG8_SB(0, 0), b2, voffB); PG8_STAGE(PG8_SB(0, 1), b2 + hB, voffB); PG8_STAGE(PG8_SA(0, 0), a2, w0);
;             PG8_WAIT_V(8); PG8_WAIT_L(0); PG8_BAR; PG8_MMA(1, 0, At, B0); PG8_MMA(1, 1, At, B1); PG8_BAR; PG8_SCHED;
;             PG8_LDB(B0, 1, 0); PG8_LDB(B1, 1, 1); PG8_SCHED; PG8_LDA(At, 1, 0); PG8_STAGE(PG8_SA(0, 1), a2 + hA, w1);
;             PG8_WAIT_V(8); PG8_WAIT_L(0); PG8_BAR; PG8_MMA(0, 0, At, B0); PG8_MMA(0, 1, At, B1); PG8_BAR; PG8_SCHED;
;             PG8_LDA(At, 1, 1); PG8_STAGE(PG8_SB(1, 0), b3, voffB); PG8_STAGE(PG8_SB(1, 1), b3 + hB, voffB); PG8_STAGE(PG8_SA(1, 0), a3, w0);
;             PG8_WAIT_V(8); PG8_WAIT_L(0); PG8_BAR; PG8_MMA(1, 0, At, B0); PG8_MMA(1, 1, At, B1); PG8_BAR; PG8_SCHED;
	s_setprio 0
	s_waitcnt lgkmcnt(0)
	v_mfma_f32_16x16x32_bf16 v[54:57], v[152:155], v[184:187], v[54:57]
	v_mfma_f32_16x16x32_bf16 v[50:53], v[160:163], v[184:187], v[50:53]
	v_mfma_f32_16x16x32_bf16 v[30:33], v[152:155], v[192:195], v[30:33]
	v_mfma_f32_16x16x32_bf16 v[26:29], v[160:163], v[192:195], v[26:29]
	v_mfma_f32_16x16x32_bf16 v[14:17], v[152:155], v[204:207], v[14:17]
	v_mfma_f32_16x16x32_bf16 v[10:13], v[160:163], v[204:207], v[10:13]
	v_mfma_f32_16x16x32_bf16 v[6:9], v[152:155], v[212:215], v[6:9]
	v_mfma_f32_16x16x32_bf16 v[2:5], v[160:163], v[212:215], v[2:5]
	v_mfma_f32_16x16x32_bf16 v[54:57], v[156:159], v[188:191], v[54:57]
	v_mfma_f32_16x16x32_bf16 v[50:53], v[164:167], v[188:191], v[50:53]
	v_mfma_f32_16x16x32_bf16 v[30:33], v[156:159], v[200:203], v[30:33]
	v_mfma_f32_16x16x32_bf16 v[26:29], v[164:167], v[200:203], v[26:29]
	v_mfma_f32_16x16x32_bf16 v[14:17], v[156:159], v[208:211], v[14:17]
	v_mfma_f32_16x16x32_bf16 v[10:13], v[164:167], v[208:211], v[10:13]
	v_mfma_f32_16x16x32_bf16 v[6:9], v[156:159], v[216:219], v[6:9]
	v_mfma_f32_16x16x32_bf16 v[2:5], v[164:167], v[216:219], v[2:5]
	s_setprio 1
	s_setprio 0
	v_mfma_f32_16x16x32_bf16 v[66:69], v[168:171], v[184:187], v[66:69]
	v_mfma_f32_16x16x32_bf16 v[70:73], v[176:179], v[184:187], v[70:73]
	v_mfma_f32_16x16x32_bf16 v[42:45], v[168:171], v[192:195], v[42:45]
	v_mfma_f32_16x16x32_bf16 v[46:49], v[176:179], v[192:195], v[46:49]
	v_mfma_f32_16x16x32_bf16 v[34:37], v[168:171], v[204:207], v[34:37]
	v_mfma_f32_16x16x32_bf16 v[38:41], v[176:179], v[204:207], v[38:41]
	v_mfma_f32_16x16x32_bf16 v[18:21], v[168:171], v[212:215], v[18:21]
	v_mfma_f32_16x16x32_bf16 v[22:25], v[176:179], v[212:215], v[22:25]
	v_mfma_f32_16x16x32_bf16 v[66:69], v[172:175], v[188:191], v[66:69]
	v_mfma_f32_16x16x32_bf16 v[70:73], v[180:183], v[188:191], v[70:73]
	v_mfma_f32_16x16x32_bf16 v[42:45], v[172:175], v[200:203], v[42:45]
	v_mfma_f32_16x16x32_bf16 v[46:49], v[180:183], v[200:203], v[46:49]
	v_mfma_f32_16x16x32_bf16 v[34:37], v[172:175], v[208:211], v[34:37]
	v_mfma_f32_16x16x32_bf16 v[38:41], v[180:183], v[208:211], v[38:41]
	v_mfma_f32_16x16x32_bf16 v[18:21], v[172:175], v[216:219], v[18:21]
	v_mfma_f32_16x16x32_bf16 v[22:25], v[180:183], v[216:219], v[22:25]
	s_setprio 1
	s_barrier
	ds_read_b128 v[152:155], v150
	ds_read_b128 v[156:159], v150 offset:1024
	ds_read_b128 v[160:163], v150 offset:2048
	ds_read_b128 v[164:167], v150 offset:3072
	ds_read_b128 v[168:171], v151
	ds_read_b128 v[172:175], v151 offset:1024
	ds_read_b128 v[176:179], v151 offset:2048
	ds_read_b128 v[180:183], v151 offset:3072
	s_add_u32 s14, s14, 0x80000
	s_addc_u32 s15, s15, 0
	s_mov_b32 m0, s20
	v_lshl_add_u64 v[226:227], s[14:15], 0, v[132:133]
	ds_read_b128 v[184:187], v149 offset:32768
	ds_read_b128 v[188:191], v149 offset:33792
	ds_read_b128 v[192:195], v149 offset:34816
	ds_read_b128 v[200:203], v149 offset:35840
	ds_read_b128 v[204:207], v149 offset:36864
	ds_read_b128 v[208:211], v149 offset:37888
	ds_read_b128 v[212:215], v149 offset:38912
	ds_read_b128 v[216:219], v149 offset:39936
	global_load_lds_dwordx4 v[226:227], off
	v_lshl_add_u64 v[226:227], s[14:15], 0, v[136:137]
	s_mov_b32 m0, s21
	s_nop 0
	global_load_lds_dwordx4 v[226:227], off
	s_waitcnt vmcnt(8)
	s_waitcnt lgkmcnt(0)
	s_barrier
	s_setprio 0
	s_waitcnt lgkmcnt(0)
	v_mfma_f32_16x16x32_bf16 v[126:129], v[152:155], v[184:187], v[126:129]
	v_mfma_f32_16x16x32_bf16 v[122:125], v[160:163], v[184:187], v[122:125]
	v_mfma_f32_16x16x32_bf16 v[114:117], v[152:155], v[192:195], v[114:117]
	v_mfma_f32_16x16x32_bf16 v[106:109], v[160:163], v[192:195], v[106:109]
	v_mfma_f32_16x16x32_bf16 v[98:101], v[152:155], v[204:207], v[98:101]
	v_mfma_f32_16x16x32_bf16 v[90:93], v[160:163], v[204:207], v[90:93]
	v_mfma_f32_16x16x32_bf16 v[82:85], v[152:155], v[212:215], v[82:85]
	v_mfma_f32_16x16x32_bf16 v[74:77], v[160:163], v[212:215], v[74:77]
	v_mfma_f32_16x16x32_bf16 v[126:129], v[156:159], v[188:191], v[126:129]
	v_mfma_f32_16x16x32_bf16 v[122:125], v[164:167], v[188:191], v[122:125]
	v_mfma_f32_16x16x32_bf16 v[114:117], v[156:159], v[200:203], v[114:117]
	v_mfma_f32_16x16x32_bf16 v[106:109], v[164:167], v[200:203], v[106:109]
	v_mfma_f32_16x16x32_bf16 v[98:101], v[156:159], v[208:211], v[98:101]
	v_mfma_f32_16x16x32_bf16 v[90:93], v[164:167], v[208:211], v[90:93]
	v_mfma_f32_16x16x32_bf16 v[82:85], v[156:159], v[216:219], v[82:85]
	v_mfma_f32_16x16x32_bf16 v[74:77], v[164:167], v[216:219], v[74:77]
	s_setprio 1
	s_setprio 0
	v_mfma_f32_16x16x32_bf16 v[118:121], v[168:171], v[184:187], v[118:121]
	v_mfma_f32_16x16x32_bf16 v[110:113], v[176:179], v[184:187], v[110:113]
	v_mfma_f32_16x16x32_bf16 v[102:105], v[168:171], v[192:195], v[102:105]
	v_mfma_f32_16x16x32_bf16 v[94:97], v[176:179], v[192:195], v[94:97]
	v_mfma_f32_16x16x32_bf16 v[86:89], v[168:171], v[204:207], v[86:89]
	v_mfma_f32_16x16x32_bf16 v[78:81], v[176:179], v[204:207], v[78:81]
	v_mfma_f32_16x16x32_bf16 v[62:65], v[168:171], v[212:215], v[62:65]
	v_mfma_f32_16x16x32_bf16 v[58:61], v[176:179], v[212:215], v[58:61]
	v_mfma_f32_16x16x32_bf16 v[118:121], v[172:175], v[188:191], v[118:121]
	v_mfma_f32_16x16x32_bf16 v[110:113], v[180:183], v[188:191], v[110:113]
	v_mfma_f32_16x16x32_bf16 v[102:105], v[172:175], v[200:203], v[102:105]
	v_mfma_f32_16x16x32_bf16 v[94:97], v[180:183], v[200:203], v[94:97]
	v_mfma_f32_16x16x32_bf16 v[86:89], v[172:175], v[208:211], v[86:89]
	v_mfma_f32_16x16x32_bf16 v[78:81], v[180:183], v[208:211], v[78:81]
	v_mfma_f32_16x16x32_bf16 v[62:65], v[172:175], v[216:219], v[62:65]
	v_mfma_f32_16x16x32_bf16 v[58:61], v[180:183], v[216:219], v[58:61]
	s_setprio 1
	s_barrier
; #define PG8_STAGE(bufoff, gbase, voff) do { _Pragma("unroll") for (int _i = 0; _i < 2; ++_i) \
;         __builtin_amdgcn_global_load_lds((const unsigned*)((const char*)(gbase) + (voff)[_i]), (LAS unsigned*)(lds + (bufoff) + ldsw + _i * 8192), 16, 0, 0); } while (0)
; #define PG8_LDA(dst, b, h) do { if constexpr (F8) { _Pragma("unroll") for (int m = 0; m < 4; ++m) dst##8[m] = PG8_LD8(lds, PG8_SA(b, h) + aoff + m * 2048); } \
;         else { _Pragma("unroll") for (int m = 0; m < 4; ++m) _Pragma("unroll") for (int k = 0; k < 2; ++k) dst[m][k] = *(const LAS bf16x8*)(lds + PG8_SA(b, h) + aoff + m * 2048 + k * 1024); } } while (0)
; #define PG8_LDB(dst, b, h) do { if constexpr (F8) { _Pragma("unroll") for (int n = 0; n < 2; ++n) dst##8[n] = PG8_LD8(ldsB, PG8_SBR(b, h) + boff + n * 2048); } \
;         else { _Pragma("unroll") for (int n = 0; n < 2; ++n) _Pragma("unroll") for (int k = 0; k < 2; ++k) dst[n][k] = *(const LAS bf16x8*)(ldsB + PG8_SBR(b, h) + boff + n * 2048 + k * 1024); } } while (0)
; #define PG8_WAIT_V(n) asm volatile("s_waitcnt vmcnt(" #n ")" ::: "memory")
; #define PG8_WAIT_L(n) asm volatile("s_waitcnt lgkmcnt(" #n ")" ::: "memory")
; template <bool GATHER, bool F8, class Epi, class Sched>
; __device__ __forceinline__ void gemm_phase(LAS unsigned char* lds, const int nt, const unsigned lda, const unsigned ldb, const Sched& S, const Epi& E) {
;     ...
;             PG8_LDB(B0, 0, 0); PG8_LDB(B1, 0, 1); PG8_SCHED; PG8_LDA(At, 0, 0); PG8_STAGE(PG8_SA(1, 1), a1 + hA, vA1);
;             PG8_WAIT_V(8); PG8_WAIT_L(0); PG8_BAR; PG8_MMA(0, 0, At, B0); PG8_MMA(0, 1, At, B1); PG8_BAR; PG8_SCHED;
;             PG8_LDA(At, 0, 1); PG8_STAGE(PG8_SB(0, 0), b2, voffB); PG8_STAGE(PG8_SB(0, 1), b2 + hB, voffB); PG8_STAGE(PG8_SA(0, 0), a2, w0);
;             PG8_WAIT_V(8); PG8_WAIT_L(0); PG8_BAR; PG8_MMA(1, 0, At, B0); PG8_MMA(1, 1, At, B1); PG8_BAR; PG8_SCHED;
;             PG8_LDB(B0, 1, 0); PG8_LDB(B1, 1, 1); PG8_SCHED; PG8_LDA(At, 1, 0); PG8_STAGE(PG8_SA(0, 1), a2 + hA, w1);
;             PG8_WAIT_V(8); PG8_WAIT_L(0); PG8_BAR; PG8_MMA(0, 0, At, B0); PG8_MMA(0, 1, At, B1); PG8_BAR; PG8_SCHED;
;             PG8_LDA(At, 1, 1); PG8_STAGE(PG8_SB(1, 0), b3, voffB); PG8_STAGE(PG8_SB(1, 1), b3 + hB, voffB); PG8_STAGE(PG8_SA(1, 0), a3, w0);
;             PG8_WAIT_V(8); PG8_WAIT_L(0); PG8_BAR; PG8_MMA(1, 0, At, B0); PG8_MMA(1, 1, At, B1); PG8_BAR; PG8_SCHED;
	s_mov_b32 m0, s34
	v_lshl_add_u64 v[196:197], v[196:197], 0, s[8:9]
	s_add_u32 s12, s12, 0x80080
	ds_read_b128 v[184:187], v149 offset:49152
	ds_read_b128 v[188:191], v149 offset:50176
	ds_read_b128 v[192:195], v149 offset:51200
	ds_read_b128 v[200:203], v149 offset:52224
	ds_read_b128 v[204:207], v149 offset:53248
	ds_read_b128 v[208:211], v149 offset:54272
	ds_read_b128 v[212:215], v149 offset:55296
	ds_read_b128 v[216:219], v149 offset:56320
	global_load_lds_dwordx4 v[196:197], off
	v_lshl_add_u64 v[196:197], v[220:221], 0, s[8:9]
	s_mov_b32 m0, s35
	s_addc_u32 s13, s13, 0
	global_load_lds_dwordx4 v[196:197], off
	v_lshl_add_u64 v[196:197], s[12:13], 0, v[134:135]
	s_mov_b32 m0, s36
	s_nop 0
	global_load_lds_dwordx4 v[196:197], off
	v_lshl_add_u64 v[196:197], s[12:13], 0, v[138:139]
	s_mov_b32 m0, s37
	s_nop 0
	global_load_lds_dwordx4 v[196:197], off
	v_lshl_add_u64 v[196:197], v[222:223], 0, s[8:9]
	s_mov_b32 m0, s22
	s_nop 0
	global_load_lds_dwordx4 v[196:197], off
	v_lshl_add_u64 v[196:197], v[224:225], 0, s[8:9]
	s_mov_b32 m0, s23
	s_nop 0
	global_load_lds_dwordx4 v[196:197], off
	s_waitcnt vmcnt(8)
	s_waitcnt lgkmcnt(0)
	s_barrier
	s_setprio 0
	s_waitcnt lgkmcnt(0)
	v_mfma_f32_16x16x32_bf16 v[54:57], v[152:155], v[184:187], v[54:57]
	v_mfma_f32_16x16x32_bf16 v[50:53], v[160:163], v[184:187], v[50:53]
	v_mfma_f32_16x16x32_bf16 v[30:33], v[152:155], v[192:195], v[30:33]
	v_mfma_f32_16x16x32_bf16 v[26:29], v[160:163], v[192:195], v[26:29]
	v_mfma_f32_16x16x32_bf16 v[14:17], v[152:155], v[204:207], v[14:17]
	v_mfma_f32_16x16x32_bf16 v[10:13], v[160:163], v[204:207], v[10:13]
	v_mfma_f32_16x16x32_bf16 v[6:9], v[152:155], v[212:215], v[6:9]
	v_mfma_f32_16x16x32_bf16 v[2:5], v[160:163], v[212:215], v[2:5]
	v_mfma_f32_16x16x32_bf16 v[54:57], v[156:159], v[188:191], v[54:57]
	v_mfma_f32_16x16x32_bf16 v[50:53], v[164:167], v[188:191], v[50:53]
	v_mfma_f32_16x16x32_bf16 v[30:33], v[156:159], v[200:203], v[30:33]
	v_mfma_f32_16x16x32_bf16 v[26:29], v[164:167], v[200:203], v[26:29]
	v_mfma_f32_16x16x32_bf16 v[14:17], v[156:159], v[208:211], v[14:17]
	v_mfma_f32_16x16x32_bf16 v[10:13], v[164:167], v[208:211], v[10:13]
	v_mfma_f32_16x16x32_bf16 v[6:9], v[156:159], v[216:219], v[6:9]
	v_mfma_f32_16x16x32_bf16 v[2:5], v[164:167], v[216:219], v[2:5]
	s_setprio 1
	s_setprio 0
	v_mfma_f32_16x16x32_bf16 v[66:69], v[168:171], v[184:187], v[66:69]
	v_mfma_f32_16x16x32_bf16 v[70:73], v[176:179], v[184:187], v[70:73]
	v_mfma_f32_16x16x32_bf16 v[42:45], v[168:171], v[192:195], v[42:45]
	v_mfma_f32_16x16x32_bf16 v[46:49], v[176:179], v[192:195], v[46:49]
	v_mfma_f32_16x16x32_bf16 v[34:37], v[168:171], v[204:207], v[34:37]
	v_mfma_f32_16x16x32_bf16 v[38:41], v[176:179], v[204:207], v[38:41]
	v_mfma_f32_16x16x32_bf16 v[18:21], v[168:171], v[212:215], v[18:21]
	v_mfma_f32_16x16x32_bf16 v[22:25], v[176:179], v[212:215], v[22:25]
	v_mfma_f32_16x16x32_bf16 v[66:69], v[172:175], v[188:191], v[66:69]
	v_mfma_f32_16x16x32_bf16 v[70:73], v[180:183], v[188:191], v[70:73]
	v_mfma_f32_16x16x32_bf16 v[42:45], v[172:175], v[200:203], v[42:45]
	v_mfma_f32_16x16x32_bf16 v[46:49], v[180:183], v[200:203], v[46:49]
	v_mfma_f32_16x16x32_bf16 v[34:37], v[172:175], v[208:211], v[34:37]
	v_mfma_f32_16x16x32_bf16 v[38:41], v[180:183], v[208:211], v[38:41]
	v_mfma_f32_16x16x32_bf16 v[18:21], v[172:175], v[216:219], v[18:21]
	v_mfma_f32_16x16x32_bf16 v[22:25], v[180:183], v[216:219], v[22:25]
	s_setprio 1
	s_barrier
	s_add_i32 s26, s26, 2
	s_add_u32 s10, s10, 0x100
	s_addc_u32 s11, s11, 0
	s_cmp_gt_u32 s26, 29
	s_cbranch_scc0 .LBB0_1152
	s_cmpk_lt_u32 s18, 0x100
	s_cbranch_scc0 .LBB0_1155
	s_barrier

; #define PG8_STAGE(bufoff, gbase, voff) do { _Pragma("unroll") for (int _i = 0; _i < 2; ++_i) \
;         __builtin_amdgcn_global_load_lds((const unsigned*)((const char*)(gbase) + (voff)[_i]), (LAS unsigned*)(lds + (bufoff) + ldsw + _i * 8192), 16, 0, 0); } while (0)
; #define PG8_LDA(dst, b, h) do { if constexpr (F8) { _Pragma("unroll") for (int m = 0; m < 4; ++m) dst##8[m] = PG8_LD8(lds, PG8_SA(b, h) + aoff + m * 2048); } \
;         else { _Pragma("unroll") for (int m = 0; m < 4; ++m) _Pragma("unroll") for (int k = 0; k < 2; ++k) dst[m][k] = *(const LAS bf16x8*)(lds + PG8_SA(b, h) + aoff + m * 2048 + k * 1024); } } while (0)
; #define PG8_LDB(dst, b, h) do { if constexpr (F8) { _Pragma("unroll") for (int n = 0; n < 2; ++n) dst##8[n] = PG8_LD8(ldsB, PG8_SBR(b, h) + boff + n * 2048); } \
;         else { _Pragma("unroll") for (int n = 0; n < 2; ++n) _Pragma("unroll") for (int k = 0; k < 2; ++k) dst[n][k] = *(const LAS bf16x8*)(ldsB + PG8_SBR(b, h) + boff + n * 2048 + k * 1024); } } while (0)
; #define PG8_WAIT_V(n) asm volatile("s_waitcnt vmcnt(" #n ")" ::: "memory")
; #define PG8_WAIT_L(n) asm volatile("s_waitcnt lgkmcnt(" #n ")" ::: "memory")
; template <bool GATHER, bool F8, class Epi, class Sched>
; __device__ __forceinline__ void gemm_phase(LAS unsigned char* lds, const int nt, const unsigned lda, const unsigned ldb, const Sched& S, const Epi& E) {
;     ...
;             PG8_LDB(B0, 0, 0); PG8_LDB(B1, 0, 1); PG8_SCHED; PG8_LDA(At, 0, 0); PG8_STAGE(PG8_SA(1, 1), a1 + hA, vA1);
;             PG8_WAIT_V(8); PG8_WAIT_L(0); PG8_BAR; PG8_MMA(0, 0, At, B0); PG8_MMA(0, 1, At, B1); PG8_BAR; PG8_SCHED;
;             PG8_LDA(At, 0, 1); PG8_STAGE(PG8_SB(0, 0), b2, voffB); PG8_STAGE(PG8_SB(0, 1), b2 + hB, voffB); PG8_STAGE(PG8_SA(0, 0), a2, w0);
;             PG8_WAIT_V(8); PG8_WAIT_L(0); PG8_BAR; PG8_MMA(1, 0, At, B0); PG8_MMA(1, 1, At, B1); PG8_BAR; PG8_SCHED;
;             PG8_LDB(B0, 1, 0); PG8_LDB(B1, 1, 1); PG8_SCHED; PG8_LDA(At, 1, 0); PG8_STAGE(PG8_SA(0, 1), a2 + hA, w1);
;             PG8_WAIT_V(8); PG8_WAIT_L(0); PG8_BAR; PG8_MMA(0, 0, At, B0); PG8_MMA(0, 1, At, B1); PG8_BAR; PG8_SCHED;
;             PG8_LDA(At, 1, 1); PG8_STAGE(PG8_SB(1, 0), b3, voffB); PG8_STAGE(PG8_SB(1, 1), b3 + hB, voffB); PG8_STAGE(PG8_SA(1, 0), a3, w0);
;             PG8_WAIT_V(8); PG8_WAIT_L(0); PG8_BAR; PG8_MMA(1, 0, At, B0); PG8_MMA(1, 1, At, B1); PG8_BAR; PG8_SCHED;
.LBB0_1432:
	ds_read_b128 v[130:133], v184
	ds_read_b128 v[134:137], v184 offset:1024
	ds_read_b128 v[138:141], v184 offset:2048
	ds_read_b128 v[142:145], v184 offset:3072
	ds_read_b128 v[146:149], v185
	ds_read_b128 v[150:153], v185 offset:1024
	ds_read_b128 v[170:173], v185 offset:2048
	ds_read_b128 v[174:177], v185 offset:3072
	s_add_u32 s28, s26, 0xfffe0080
	s_addc_u32 s29, s27, -1
	s_cmp_eq_u32 s53, 4
	s_cselect_b32 s31, s1, s29
	s_cselect_b32 s30, s0, s28
	s_cselect_b32 s29, s23, s34
	s_cselect_b32 s28, s22, s25
	s_add_i32 m0, s40, 0xc000
	ds_read_b128 v[178:181], v186
	ds_read_b128 v[190:193], v186 offset:1024
	ds_read_b128 v[194:197], v186 offset:2048
	ds_read_b128 v[200:203], v186 offset:3072
	ds_read_b128 v[204:207], v186 offset:4096
	ds_read_b128 v[208:211], v186 offset:5120
	ds_read_b128 v[212:215], v186 offset:6144
	ds_read_b128 v[216:219], v186 offset:7168
	global_load_lds_dwordx4 v162, s[26:27]
	s_add_i32 m0, s40, 0xe000
	s_nop 0
	global_load_lds_dwordx4 v164, s[26:27]
	s_waitcnt vmcnt(8)
	s_waitcnt lgkmcnt(0)
	s_barrier
	s_setprio 0
	s_waitcnt lgkmcnt(0)
	v_mfma_f32_16x16x32_bf16 v[126:129], v[130:133], v[178:181], v[126:129]
	v_mfma_f32_16x16x32_bf16 v[122:125], v[138:141], v[178:181], v[122:125]
	v_mfma_f32_16x16x32_bf16 v[110:113], v[130:133], v[194:197], v[110:113]
	v_mfma_f32_16x16x32_bf16 v[106:109], v[138:141], v[194:197], v[106:109]
	v_mfma_f32_16x16x32_bf16 v[94:97], v[130:133], v[204:207], v[94:97]
	v_mfma_f32_16x16x32_bf16 v[90:93], v[138:141], v[204:207], v[90:93]
	v_mfma_f32_16x16x32_bf16 v[78:81], v[130:133], v[212:215], v[78:81]
	v_mfma_f32_16x16x32_bf16 v[74:77], v[138:141], v[212:215], v[74:77]
	v_mfma_f32_16x16x32_bf16 v[126:129], v[134:137], v[190:193], v[126:129]
	v_mfma_f32_16x16x32_bf16 v[122:125], v[142:145], v[190:193], v[122:125]
	v_mfma_f32_16x16x32_bf16 v[110:113], v[134:137], v[200:203], v[110:113]
	v_mfma_f32_16x16x32_bf16 v[106:109], v[142:145], v[200:203], v[106:109]
	v_mfma_f32_16x16x32_bf16 v[94:97], v[134:137], v[208:211], v[94:97]
	v_mfma_f32_16x16x32_bf16 v[90:93], v[142:145], v[208:211], v[90:93]
	v_mfma_f32_16x16x32_bf16 v[78:81], v[134:137], v[216:219], v[78:81]
	v_mfma_f32_16x16x32_bf16 v[74:77], v[142:145], v[216:219], v[74:77]
	s_setprio 1
	s_setprio 0
	v_mfma_f32_16x16x32_bf16 v[118:121], v[146:149], v[178:181], v[118:121]
	v_mfma_f32_16x16x32_bf16 v[114:117], v[170:173], v[178:181], v[114:117]
	v_mfma_f32_16x16x32_bf16 v[102:105], v[146:149], v[194:197], v[102:105]
	v_mfma_f32_16x16x32_bf16 v[98:101], v[170:173], v[194:197], v[98:101]
	v_mfma_f32_16x16x32_bf16 v[86:89], v[146:149], v[204:207], v[86:89]
	v_mfma_f32_16x16x32_bf16 v[82:85], v[170:173], v[204:207], v[82:85]
	v_mfma_f32_16x16x32_bf16 v[70:73], v[146:149], v[212:215], v[70:73]
	v_mfma_f32_16x16x32_bf16 v[66:69], v[170:173], v[212:215], v[66:69]
	v_mfma_f32_16x16x32_bf16 v[118:121], v[150:153], v[190:193], v[118:121]
	v_mfma_f32_16x16x32_bf16 v[114:117], v[174:177], v[190:193], v[114:117]
	v_mfma_f32_16x16x32_bf16 v[102:105], v[150:153], v[200:203], v[102:105]
	v_mfma_f32_16x16x32_bf16 v[98:101], v[174:177], v[200:203], v[98:101]
	v_mfma_f32_16x16x32_bf16 v[86:89], v[150:153], v[208:211], v[86:89]
	v_mfma_f32_16x16x32_bf16 v[82:85], v[174:177], v[208:211], v[82:85]
	v_mfma_f32_16x16x32_bf16 v[70:73], v[150:153], v[216:219], v[70:73]
	v_mfma_f32_16x16x32_bf16 v[66:69], v[174:177], v[216:219], v[66:69]
	s_setprio 1
	s_barrier
	s_add_i32 s54, s48, s39
	s_mov_b32 m0, s54
	ds_read_b128 v[178:181], v186 offset:16384
	ds_read_b128 v[190:193], v186 offset:17408
	ds_read_b128 v[194:197], v186 offset:18432
	ds_read_b128 v[200:203], v186 offset:19456
	ds_read_b128 v[204:207], v186 offset:20480
	ds_read_b128 v[208:211], v186 offset:21504
	ds_read_b128 v[212:215], v186 offset:22528
	ds_read_b128 v[216:219], v186 offset:23552
	global_load_lds_dwordx4 v156, s[28:29]
	s_add_i32 m0, s54, 0x2000
	s_add_u32 s54, s28, 0x20000
	s_addc_u32 s55, s29, 0
	s_add_i32 s56, s49, s39
	global_load_lds_dwordx4 v160, s[28:29]
	s_mov_b32 m0, s56
	s_nop 0
	global_load_lds_dwordx4 v156, s[54:55]
	s_add_i32 m0, s56, 0x2000
	s_nop 0
	global_load_lds_dwordx4 v160, s[54:55]
	s_mov_b32 m0, s40
	s_nop 0
	s_mov_b64 s[98:99], s[30:31]
	global_load_lds_dwordx4 v154, s[30:31]
	s_mov_b32 m0, s41
	s_nop 0
	global_load_lds_dwordx4 v158, s[30:31]
	s_waitcnt vmcnt(8)
	s_waitcnt lgkmcnt(0)
	s_barrier
	s_setprio 0
	s_waitcnt lgkmcnt(0)
	v_mfma_f32_16x16x32_bf16 v[54:57], v[130:133], v[178:181], v[54:57]
	v_mfma_f32_16x16x32_bf16 v[50:53], v[138:141], v[178:181], v[50:53]
	v_mfma_f32_16x16x32_bf16 v[46:49], v[130:133], v[194:197], v[46:49]
	v_mfma_f32_16x16x32_bf16 v[34:37], v[138:141], v[194:197], v[34:37]
	v_mfma_f32_16x16x32_bf16 v[22:25], v[130:133], v[204:207], v[22:25]
	v_mfma_f32_16x16x32_bf16 v[18:21], v[138:141], v[204:207], v[18:21]
	v_mfma_f32_16x16x32_bf16 v[6:9], v[130:133], v[212:215], v[6:9]
	v_mfma_f32_16x16x32_bf16 v[2:5], v[138:141], v[212:215], v[2:5]
	v_mfma_f32_16x16x32_bf16 v[54:57], v[134:137], v[190:193], v[54:57]
	v_mfma_f32_16x16x32_bf16 v[50:53], v[142:145], v[190:193], v[50:53]
	v_mfma_f32_16x16x32_bf16 v[46:49], v[134:137], v[200:203], v[46:49]
	v_mfma_f32_16x16x32_bf16 v[34:37], v[142:145], v[200:203], v[34:37]
	v_mfma_f32_16x16x32_bf16 v[22:25], v[134:137], v[208:211], v[22:25]
	v_mfma_f32_16x16x32_bf16 v[18:21], v[142:145], v[208:211], v[18:21]
	v_mfma_f32_16x16x32_bf16 v[6:9], v[134:137], v[216:219], v[6:9]
	v_mfma_f32_16x16x32_bf16 v[2:5], v[142:145], v[216:219], v[2:5]
	s_setprio 1
	s_setprio 0
	v_mfma_f32_16x16x32_bf16 v[62:65], v[146:149], v[178:181], v[62:65]
	v_mfma_f32_16x16x32_bf16 v[58:61], v[170:173], v[178:181], v[58:61]
	v_mfma_f32_16x16x32_bf16 v[42:45], v[146:149], v[194:197], v[42:45]
	v_mfma_f32_16x16x32_bf16 v[38:41], v[170:173], v[194:197], v[38:41]
	v_mfma_f32_16x16x32_bf16 v[30:33], v[146:149], v[204:207], v[30:33]
	v_mfma_f32_16x16x32_bf16 v[26:29], v[170:173], v[204:207], v[26:29]
	v_mfma_f32_16x16x32_bf16 v[14:17], v[146:149], v[212:215], v[14:17]
	v_mfma_f32_16x16x32_bf16 v[10:13], v[170:173], v[212:215], v[10:13]
	v_mfma_f32_16x16x32_bf16 v[62:65], v[150:153], v[190:193], v[62:65]
	v_mfma_f32_16x16x32_bf16 v[58:61], v[174:177], v[190:193], v[58:61]
	v_mfma_f32_16x16x32_bf16 v[42:45], v[150:153], v[200:203], v[42:45]
	v_mfma_f32_16x16x32_bf16 v[38:41], v[174:177], v[200:203], v[38:41]
	v_mfma_f32_16x16x32_bf16 v[30:33], v[150:153], v[208:211], v[30:33]
	v_mfma_f32_16x16x32_bf16 v[26:29], v[174:177], v[208:211], v[26:29]
	v_mfma_f32_16x16x32_bf16 v[14:17], v[150:153], v[216:219], v[14:17]
	v_mfma_f32_16x16x32_bf16 v[10:13], v[174:177], v[216:219], v[10:13]
	s_setprio 1
	s_barrier
; #define PG8_STAGE(bufoff, gbase, voff) do { _Pragma("unroll") for (int _i = 0; _i < 2; ++_i) \
;         __builtin_amdgcn_global_load_lds((const unsigned*)((const char*)(gbase) + (voff)[_i]), (LAS unsigned*)(lds + (bufoff) + ldsw + _i * 8192), 16, 0, 0); } while (0)
; #define PG8_LDA(dst, b, h) do { if constexpr (F8) { _Pragma("unroll") for (int m = 0; m < 4; ++m) dst##8[m] = PG8_LD8(lds, PG8_SA(b, h) + aoff + m * 2048); } \
;         else { _Pragma("unroll") for (int m = 0; m < 4; ++m) _Pragma("unroll") for (int k = 0; k < 2; ++k) dst[m][k] = *(const LAS bf16x8*)(lds + PG8_SA(b, h) + aoff + m * 2048 + k * 1024); } } while (0)
; #define PG8_LDB(dst, b, h) do { if constexpr (F8) { _Pragma("unroll") for (int n = 0; n < 2; ++n) dst##8[n] = PG8_LD8(ldsB, PG8_SBR(b, h) + boff + n * 2048); } \
;         else { _Pragma("unroll") for (int n = 0; n < 2; ++n) _Pragma("unroll") for (int k = 0; k < 2; ++k) dst[n][k] = *(const LAS bf16x8*)(ldsB + PG8_SBR(b, h) + boff + n * 2048 + k * 1024); } } while (0)
; #define PG8_WAIT_V(n) asm volatile("s_waitcnt vmcnt(" #n ")" ::: "memory")
; #define PG8_WAIT_L(n) asm volatile("s_waitcnt lgkmcnt(" #n ")" ::: "memory")
; template <bool GATHER, bool F8, class Epi, class Sched>
; __device__ __forceinline__ void gemm_phase(LAS unsigned char* lds, const int nt, const unsigned lda, const unsigned ldb, const Sched& S, const Epi& E) {
;     ...
;             PG8_LDB(B0, 0, 0); PG8_LDB(B1, 0, 1); PG8_SCHED; PG8_LDA(At, 0, 0); PG8_STAGE(PG8_SA(1, 1), a1 + hA, vA1);
;             PG8_WAIT_V(8); PG8_WAIT_L(0); PG8_BAR; PG8_MMA(0, 0, At, B0); PG8_MMA(0, 1, At, B1); PG8_BAR; PG8_SCHED;
;             PG8_LDA(At, 0, 1); PG8_STAGE(PG8_SB(0, 0), b2, voffB); PG8_STAGE(PG8_SB(0, 1), b2 + hB, voffB); PG8_STAGE(PG8_SA(0, 0), a2, w0);
;             PG8_WAIT_V(8); PG8_WAIT_L(0); PG8_BAR; PG8_MMA(1, 0, At, B0); PG8_MMA(1, 1, At, B1); PG8_BAR; PG8_SCHED;
;             PG8_LDB(B0, 1, 0); PG8_LDB(B1, 1, 1); PG8_SCHED; PG8_LDA(At, 1, 0); PG8_STAGE(PG8_SA(0, 1), a2 + hA, w1);
;             PG8_WAIT_V(8); PG8_WAIT_L(0); PG8_BAR; PG8_MMA(0, 0, At, B0); PG8_MMA(0, 1, At, B1); PG8_BAR; PG8_SCHED;
;             PG8_LDA(At, 1, 1); PG8_STAGE(PG8_SB(1, 0), b3, voffB); PG8_STAGE(PG8_SB(1, 1), b3 + hB, voffB); PG8_STAGE(PG8_SA(1, 0), a3, w0);
;             PG8_WAIT_V(8); PG8_WAIT_L(0); PG8_BAR; PG8_MMA(1, 0, At, B0); PG8_MMA(1, 1, At, B1); PG8_BAR; PG8_SCHED;
	s_add_i32 s54, 0, 0x18000
	s_add_i32 s55, 0, 0x1c000
	v_add_u32_e32 v142, s54, v182
	v_add_u32_e32 v174, s55, v182
	ds_read_b128 v[130:133], v142
	ds_read_b128 v[134:137], v142 offset:1024
	ds_read_b128 v[138:141], v142 offset:2048
	ds_read_b128 v[142:145], v142 offset:3072
	ds_read_b128 v[146:149], v174
	ds_read_b128 v[150:153], v174 offset:1024
	ds_read_b128 v[170:173], v174 offset:2048
	ds_read_b128 v[174:177], v174 offset:3072
	s_add_u32 s30, s30, 0x20000
	s_addc_u32 s31, s31, 0
	s_mov_b32 m0, s42
	ds_read_b128 v[178:181], v186 offset:32768
	ds_read_b128 v[190:193], v186 offset:33792
	ds_read_b128 v[194:197], v186 offset:34816
	ds_read_b128 v[200:203], v186 offset:35840
	ds_read_b128 v[204:207], v186 offset:36864
	ds_read_b128 v[208:211], v186 offset:37888
	ds_read_b128 v[212:215], v186 offset:38912
	ds_read_b128 v[216:219], v186 offset:39936
	global_load_lds_dwordx4 v154, s[30:31]
	s_mov_b32 m0, s43
	s_nop 0
	global_load_lds_dwordx4 v158, s[30:31]
	s_waitcnt vmcnt(8)
	s_waitcnt lgkmcnt(0)
	s_barrier
	s_setprio 0
	s_waitcnt lgkmcnt(0)
	v_mfma_f32_16x16x32_bf16 v[126:129], v[130:133], v[178:181], v[126:129]
	v_mfma_f32_16x16x32_bf16 v[122:125], v[138:141], v[178:181], v[122:125]
	v_mfma_f32_16x16x32_bf16 v[110:113], v[130:133], v[194:197], v[110:113]
	v_mfma_f32_16x16x32_bf16 v[106:109], v[138:141], v[194:197], v[106:109]
	v_mfma_f32_16x16x32_bf16 v[94:97], v[130:133], v[204:207], v[94:97]
	v_mfma_f32_16x16x32_bf16 v[90:93], v[138:141], v[204:207], v[90:93]
	v_mfma_f32_16x16x32_bf16 v[78:81], v[130:133], v[212:215], v[78:81]
	v_mfma_f32_16x16x32_bf16 v[74:77], v[138:141], v[212:215], v[74:77]
	v_mfma_f32_16x16x32_bf16 v[126:129], v[134:137], v[190:193], v[126:129]
	v_mfma_f32_16x16x32_bf16 v[122:125], v[142:145], v[190:193], v[122:125]
	v_mfma_f32_16x16x32_bf16 v[110:113], v[134:137], v[200:203], v[110:113]
	v_mfma_f32_16x16x32_bf16 v[106:109], v[142:145], v[200:203], v[106:109]
	v_mfma_f32_16x16x32_bf16 v[94:97], v[134:137], v[208:211], v[94:97]
	v_mfma_f32_16x16x32_bf16 v[90:93], v[142:145], v[208:211], v[90:93]
	v_mfma_f32_16x16x32_bf16 v[78:81], v[134:137], v[216:219], v[78:81]
	v_mfma_f32_16x16x32_bf16 v[74:77], v[142:145], v[216:219], v[74:77]
	s_setprio 1
	s_setprio 0
	v_mfma_f32_16x16x32_bf16 v[118:121], v[146:149], v[178:181], v[118:121]
	v_mfma_f32_16x16x32_bf16 v[114:117], v[170:173], v[178:181], v[114:117]
	v_mfma_f32_16x16x32_bf16 v[102:105], v[146:149], v[194:197], v[102:105]
	v_mfma_f32_16x16x32_bf16 v[98:101], v[170:173], v[194:197], v[98:101]
	v_mfma_f32_16x16x32_bf16 v[86:89], v[146:149], v[204:207], v[86:89]
	v_mfma_f32_16x16x32_bf16 v[82:85], v[170:173], v[204:207], v[82:85]
	v_mfma_f32_16x16x32_bf16 v[70:73], v[146:149], v[212:215], v[70:73]
	v_mfma_f32_16x16x32_bf16 v[66:69], v[170:173], v[212:215], v[66:69]
	v_mfma_f32_16x16x32_bf16 v[118:121], v[150:153], v[190:193], v[118:121]
	v_mfma_f32_16x16x32_bf16 v[114:117], v[174:177], v[190:193], v[114:117]
	v_mfma_f32_16x16x32_bf16 v[102:105], v[150:153], v[200:203], v[102:105]
	v_mfma_f32_16x16x32_bf16 v[98:101], v[174:177], v[200:203], v[98:101]
	v_mfma_f32_16x16x32_bf16 v[86:89], v[150:153], v[208:211], v[86:89]
	v_mfma_f32_16x16x32_bf16 v[82:85], v[174:177], v[208:211], v[82:85]
	v_mfma_f32_16x16x32_bf16 v[70:73], v[150:153], v[216:219], v[70:73]
	v_mfma_f32_16x16x32_bf16 v[66:69], v[174:177], v[216:219], v[66:69]
	s_setprio 1
	s_barrier
	s_add_i32 s30, s54, s39
	s_add_i32 m0, s30, 0xffffff80
	ds_read_b128 v[178:181], v186 offset:49152
	ds_read_b128 v[190:193], v186 offset:50176
	ds_read_b128 v[194:197], v186 offset:51200
	ds_read_b128 v[200:203], v186 offset:52224
	ds_read_b128 v[204:207], v186 offset:53248
	ds_read_b128 v[208:211], v186 offset:54272
	ds_read_b128 v[212:215], v186 offset:55296
	ds_read_b128 v[216:219], v186 offset:56320
	global_load_lds_dwordx4 v156, s[28:29] offset:128
	s_add_i32 m0, s30, 0x1f80
	s_add_i32 s30, s55, s39
	global_load_lds_dwordx4 v160, s[28:29] offset:128
	s_add_u32 s28, s28, 0x20080
	s_addc_u32 s29, s29, 0
	s_mov_b32 m0, s30
	s_nop 0
	global_load_lds_dwordx4 v156, s[28:29]
	s_add_i32 m0, s30, 0x2000
	s_nop 0
	global_load_lds_dwordx4 v160, s[28:29]
	s_add_i32 m0, s45, 0xffffff80
	s_nop 0
	global_load_lds_dwordx4 v154, s[98:99] offset:128
	s_add_i32 m0, s46, 0xffffff80
	s_nop 0
	global_load_lds_dwordx4 v158, s[98:99] offset:128
	s_waitcnt vmcnt(8)
	s_waitcnt lgkmcnt(0)
	s_barrier
	s_setprio 0
	s_waitcnt lgkmcnt(0)
	v_mfma_f32_16x16x32_bf16 v[54:57], v[130:133], v[178:181], v[54:57]
	v_mfma_f32_16x16x32_bf16 v[50:53], v[138:141], v[178:181], v[50:53]
	v_mfma_f32_16x16x32_bf16 v[46:49], v[130:133], v[194:197], v[46:49]
	v_mfma_f32_16x16x32_bf16 v[34:37], v[138:141], v[194:197], v[34:37]
	v_mfma_f32_16x16x32_bf16 v[22:25], v[130:133], v[204:207], v[22:25]
	v_mfma_f32_16x16x32_bf16 v[18:21], v[138:141], v[204:207], v[18:21]
	v_mfma_f32_16x16x32_bf16 v[6:9], v[130:133], v[212:215], v[6:9]
	v_mfma_f32_16x16x32_bf16 v[2:5], v[138:141], v[212:215], v[2:5]
	v_mfma_f32_16x16x32_bf16 v[54:57], v[134:137], v[190:193], v[54:57]
	v_mfma_f32_16x16x32_bf16 v[50:53], v[142:145], v[190:193], v[50:53]
	v_mfma_f32_16x16x32_bf16 v[46:49], v[134:137], v[200:203], v[46:49]
	v_mfma_f32_16x16x32_bf16 v[34:37], v[142:145], v[200:203], v[34:37]
	v_mfma_f32_16x16x32_bf16 v[22:25], v[134:137], v[208:211], v[22:25]
	v_mfma_f32_16x16x32_bf16 v[18:21], v[142:145], v[208:211], v[18:21]
	v_mfma_f32_16x16x32_bf16 v[6:9], v[134:137], v[216:219], v[6:9]
	v_mfma_f32_16x16x32_bf16 v[2:5], v[142:145], v[216:219], v[2:5]
	s_setprio 1
	s_setprio 0
	v_mfma_f32_16x16x32_bf16 v[62:65], v[146:149], v[178:181], v[62:65]
	v_mfma_f32_16x16x32_bf16 v[58:61], v[170:173], v[178:181], v[58:61]
	v_mfma_f32_16x16x32_bf16 v[42:45], v[146:149], v[194:197], v[42:45]
	v_mfma_f32_16x16x32_bf16 v[38:41], v[170:173], v[194:197], v[38:41]
	v_mfma_f32_16x16x32_bf16 v[30:33], v[146:149], v[204:207], v[30:33]
	v_mfma_f32_16x16x32_bf16 v[26:29], v[170:173], v[204:207], v[26:29]
	v_mfma_f32_16x16x32_bf16 v[14:17], v[146:149], v[212:215], v[14:17]
	v_mfma_f32_16x16x32_bf16 v[10:13], v[170:173], v[212:215], v[10:13]
	v_mfma_f32_16x16x32_bf16 v[62:65], v[150:153], v[190:193], v[62:65]
	v_mfma_f32_16x16x32_bf16 v[58:61], v[174:177], v[190:193], v[58:61]
	v_mfma_f32_16x16x32_bf16 v[42:45], v[150:153], v[200:203], v[42:45]
	v_mfma_f32_16x16x32_bf16 v[38:41], v[174:177], v[200:203], v[38:41]
	v_mfma_f32_16x16x32_bf16 v[30:33], v[150:153], v[208:211], v[30:33]
	v_mfma_f32_16x16x32_bf16 v[26:29], v[174:177], v[208:211], v[26:29]
	v_mfma_f32_16x16x32_bf16 v[14:17], v[150:153], v[216:219], v[14:17]
	v_mfma_f32_16x16x32_bf16 v[10:13], v[174:177], v[216:219], v[10:13]
	s_setprio 1
	s_barrier
	s_add_i32 s53, s53, 2
	s_add_u32 s26, s26, 0x100
	s_addc_u32 s27, s27, 0
	s_add_u32 s25, s25, 0x100
	s_addc_u32 s34, s34, 0
	s_cmp_gt_u32 s53, 5
	s_cbranch_scc0 .LBB0_1432
	s_and_b64 vcc, exec, s[20:21]
	s_cbranch_vccz .LBB0_1435
	s_barrier

; #define PG8_STAGE(bufoff, gbase, voff) do { _Pragma("unroll") for (int _i = 0; _i < 2; ++_i) \
;         __builtin_amdgcn_global_load_lds((const unsigned*)((const char*)(gbase) + (voff)[_i]), (LAS unsigned*)(lds + (bufoff) + ldsw + _i * 8192), 16, 0, 0); } while (0)
; #define PG8_LDA(dst, b, h) do { if constexpr (F8) { _Pragma("unroll") for (int m = 0; m < 4; ++m) dst##8[m] = PG8_LD8(lds, PG8_SA(b, h) + aoff + m * 2048); } \
;         else { _Pragma("unroll") for (int m = 0; m < 4; ++m) _Pragma("unroll") for (int k = 0; k < 2; ++k) dst[m][k] = *(const LAS bf16x8*)(lds + PG8_SA(b, h) + aoff + m * 2048 + k * 1024); } } while (0)
; #define PG8_LDB(dst, b, h) do { if constexpr (F8) { _Pragma("unroll") for (int n = 0; n < 2; ++n) dst##8[n] = PG8_LD8(ldsB, PG8_SBR(b, h) + boff + n * 2048); } \
;         else { _Pragma("unroll") for (int n = 0; n < 2; ++n) _Pragma("unroll") for (int k = 0; k < 2; ++k) dst[n][k] = *(const LAS bf16x8*)(ldsB + PG8_SBR(b, h) + boff + n * 2048 + k * 1024); } } while (0)
; #define PG8_WAIT_V(n) asm volatile("s_waitcnt vmcnt(" #n ")" ::: "memory")
; #define PG8_WAIT_L(n) asm volatile("s_waitcnt lgkmcnt(" #n ")" ::: "memory")
; template <bool GATHER, bool F8, class Epi, class Sched>
; __device__ __forceinline__ void gemm_phase(LAS unsigned char* lds, const int nt, const unsigned lda, const unsigned ldb, const Sched& S, const Epi& E) {
;     ...
;             PG8_LDB(B0, 0, 0); PG8_LDB(B1, 0, 1); PG8_SCHED; PG8_LDA(At, 0, 0); PG8_STAGE(PG8_SA(1, 1), a1 + hA, vA1);
;             PG8_WAIT_V(8); PG8_WAIT_L(0); PG8_BAR; PG8_MMA(0, 0, At, B0); PG8_MMA(0, 1, At, B1); PG8_BAR; PG8_SCHED;
;             PG8_LDA(At, 0, 1); PG8_STAGE(PG8_SB(0, 0), b2, voffB); PG8_STAGE(PG8_SB(0, 1), b2 + hB, voffB); PG8_STAGE(PG8_SA(0, 0), a2, w0);
;             PG8_WAIT_V(8); PG8_WAIT_L(0); PG8_BAR; PG8_MMA(1, 0, At, B0); PG8_MMA(1, 1, At, B1); PG8_BAR; PG8_SCHED;
;             PG8_LDB(B0, 1, 0); PG8_LDB(B1, 1, 1); PG8_SCHED; PG8_LDA(At, 1, 0); PG8_STAGE(PG8_SA(0, 1), a2 + hA, w1);
;             PG8_WAIT_V(8); PG8_WAIT_L(0); PG8_BAR; PG8_MMA(0, 0, At, B0); PG8_MMA(0, 1, At, B1); PG8_BAR; PG8_SCHED;
;             PG8_LDA(At, 1, 1); PG8_STAGE(PG8_SB(1, 0), b3, voffB); PG8_STAGE(PG8_SB(1, 1), b3 + hB, voffB); PG8_STAGE(PG8_SA(1, 0), a3, w0);
;             PG8_WAIT_V(8); PG8_WAIT_L(0); PG8_BAR; PG8_MMA(1, 0, At, B0); PG8_MMA(1, 1, At, B1); PG8_BAR; PG8_SCHED;
.Lp10_not_last:
	s_and_b64 s[34:35], vcc, exec
	v_cndmask_b32_e32 v164, v209, v208, vcc
	s_cselect_b32 s37, s23, s37
	s_cselect_b32 s36, s22, s36
	v_cndmask_b32_e32 v173, v172, v205, vcc
	v_cndmask_b32_e32 v242, v170, v207, vcc
	v_cndmask_b32_e32 v175, v174, v206, vcc
	s_cselect_b32 s35, s25, s68
	s_cselect_b32 s34, s24, s67
	s_add_i32 m0, s40, 0xbf80
	ds_read_b128 v[180:183], v202
	ds_read_b128 v[184:187], v202 offset:1024
	ds_read_b128 v[210:213], v202 offset:2048
	ds_read_b128 v[214:217], v202 offset:3072
	ds_read_b128 v[218:221], v202 offset:4096
	ds_read_b128 v[222:225], v202 offset:5120
	ds_read_b128 v[226:229], v202 offset:6144
	ds_read_b128 v[230:233], v202 offset:7168
	global_load_lds_dwordx4 v172, s[100:101] offset:128
	s_add_i32 m0, s40, 0xdf80
	s_nop 0
	global_load_lds_dwordx4 v174, s[100:101] offset:128
	s_waitcnt vmcnt(8)
	s_waitcnt lgkmcnt(0)
	s_barrier
	s_setprio 0
	s_waitcnt lgkmcnt(0)
	v_mfma_scale_f32_16x16x128_f8f6f4 v[158:161], v[18:25], v[180:187], v[158:161], v203, v203 op_sel_hi:[0,0,0]
	v_mfma_scale_f32_16x16x128_f8f6f4 v[150:153], v[26:33], v[180:187], v[150:153], v203, v203 op_sel_hi:[0,0,0]
	v_mfma_scale_f32_16x16x128_f8f6f4 v[142:145], v[18:25], v[210:217], v[142:145], v203, v203 op_sel_hi:[0,0,0]
	v_mfma_scale_f32_16x16x128_f8f6f4 v[134:137], v[26:33], v[210:217], v[134:137], v203, v203 op_sel_hi:[0,0,0]
	v_mfma_scale_f32_16x16x128_f8f6f4 v[126:129], v[18:25], v[218:225], v[126:129], v203, v203 op_sel_hi:[0,0,0]
	v_mfma_scale_f32_16x16x128_f8f6f4 v[118:121], v[26:33], v[218:225], v[118:121], v203, v203 op_sel_hi:[0,0,0]
	v_mfma_scale_f32_16x16x128_f8f6f4 v[110:113], v[18:25], v[226:233], v[110:113], v203, v203 op_sel_hi:[0,0,0]
	v_mfma_scale_f32_16x16x128_f8f6f4 v[102:105], v[26:33], v[226:233], v[102:105], v203, v203 op_sel_hi:[0,0,0]
	s_setprio 1
	s_setprio 0
	v_mfma_scale_f32_16x16x128_f8f6f4 v[154:157], v[2:9], v[180:187], v[154:157], v203, v203 op_sel_hi:[0,0,0]
	v_mfma_scale_f32_16x16x128_f8f6f4 v[146:149], v[10:17], v[180:187], v[146:149], v203, v203 op_sel_hi:[0,0,0]
	v_mfma_scale_f32_16x16x128_f8f6f4 v[138:141], v[2:9], v[210:217], v[138:141], v203, v203 op_sel_hi:[0,0,0]
	v_mfma_scale_f32_16x16x128_f8f6f4 v[130:133], v[10:17], v[210:217], v[130:133], v203, v203 op_sel_hi:[0,0,0]
	v_mfma_scale_f32_16x16x128_f8f6f4 v[122:125], v[2:9], v[218:225], v[122:125], v203, v203 op_sel_hi:[0,0,0]
	v_mfma_scale_f32_16x16x128_f8f6f4 v[114:117], v[10:17], v[218:225], v[114:117], v203, v203 op_sel_hi:[0,0,0]
	v_mfma_scale_f32_16x16x128_f8f6f4 v[106:109], v[2:9], v[226:233], v[106:109], v203, v203 op_sel_hi:[0,0,0]
	v_mfma_scale_f32_16x16x128_f8f6f4 v[98:101], v[10:17], v[226:233], v[98:101], v203, v203 op_sel_hi:[0,0,0]
	s_setprio 1
	s_barrier
	s_mov_b32 m0, s41
	s_add_u32 s68, s34, 0x40000
	ds_read_b128 v[210:213], v202 offset:16384
	ds_read_b128 v[214:217], v202 offset:17408
	ds_read_b128 v[218:221], v202 offset:18432
	ds_read_b128 v[222:225], v202 offset:19456
	ds_read_b128 v[226:229], v202 offset:20480
	ds_read_b128 v[230:233], v202 offset:21504
	ds_read_b128 v[234:237], v202 offset:22528
	ds_read_b128 v[238:241], v202 offset:23552
	global_load_lds_dwordx4 v166, s[34:35]
	s_mov_b32 m0, s42
	s_addc_u32 s69, s35, 0
	global_load_lds_dwordx4 v168, s[34:35]
	s_mov_b32 m0, s43
	s_nop 0
	global_load_lds_dwordx4 v166, s[68:69]
	s_mov_b32 m0, s44
	s_nop 0
	global_load_lds_dwordx4 v168, s[68:69]
	s_mov_b32 m0, s40
	s_nop 0
	global_load_lds_dwordx4 v164, s[36:37]
	s_mov_b32 m0, s45
	s_nop 0
	global_load_lds_dwordx4 v242, s[36:37]
	s_waitcnt vmcnt(8)
	s_waitcnt lgkmcnt(0)
	s_barrier
	s_setprio 0
	s_waitcnt lgkmcnt(0)
	v_mfma_scale_f32_16x16x128_f8f6f4 v[94:97], v[18:25], v[210:217], v[94:97], v203, v203 op_sel_hi:[0,0,0]
	v_mfma_scale_f32_16x16x128_f8f6f4 v[86:89], v[26:33], v[210:217], v[86:89], v203, v203 op_sel_hi:[0,0,0]
	v_mfma_scale_f32_16x16x128_f8f6f4 v[78:81], v[18:25], v[218:225], v[78:81], v203, v203 op_sel_hi:[0,0,0]
	v_mfma_scale_f32_16x16x128_f8f6f4 v[70:73], v[26:33], v[218:225], v[70:73], v203, v203 op_sel_hi:[0,0,0]
	v_mfma_scale_f32_16x16x128_f8f6f4 v[54:57], v[18:25], v[226:233], v[54:57], v203, v203 op_sel_hi:[0,0,0]
	v_mfma_scale_f32_16x16x128_f8f6f4 v[50:53], v[26:33], v[226:233], v[50:53], v203, v203 op_sel_hi:[0,0,0]
	v_mfma_scale_f32_16x16x128_f8f6f4 v[38:41], v[18:25], v[234:241], v[38:41], v203, v203 op_sel_hi:[0,0,0]
	v_mfma_scale_f32_16x16x128_f8f6f4 v[34:37], v[26:33], v[234:241], v[34:37], v203, v203 op_sel_hi:[0,0,0]
	s_setprio 1
	s_setprio 0
	v_mfma_scale_f32_16x16x128_f8f6f4 v[90:93], v[2:9], v[210:217], v[90:93], v203, v203 op_sel_hi:[0,0,0]
	v_mfma_scale_f32_16x16x128_f8f6f4 v[82:85], v[10:17], v[210:217], v[82:85], v203, v203 op_sel_hi:[0,0,0]
	v_mfma_scale_f32_16x16x128_f8f6f4 v[74:77], v[2:9], v[218:225], v[74:77], v203, v203 op_sel_hi:[0,0,0]
	v_mfma_scale_f32_16x16x128_f8f6f4 v[62:65], v[10:17], v[218:225], v[62:65], v203, v203 op_sel_hi:[0,0,0]
	v_mfma_scale_f32_16x16x128_f8f6f4 v[66:69], v[2:9], v[226:233], v[66:69], v203, v203 op_sel_hi:[0,0,0]
	v_mfma_scale_f32_16x16x128_f8f6f4 v[58:61], v[10:17], v[226:233], v[58:61], v203, v203 op_sel_hi:[0,0,0]
	v_mfma_scale_f32_16x16x128_f8f6f4 v[46:49], v[2:9], v[234:241], v[46:49], v203, v203 op_sel_hi:[0,0,0]
	v_mfma_scale_f32_16x16x128_f8f6f4 v[42:45], v[10:17], v[234:241], v[42:45], v203, v203 op_sel_hi:[0,0,0]
	s_setprio 1
	s_barrier
; #define PG8_STAGE(bufoff, gbase, voff) do { _Pragma("unroll") for (int _i = 0; _i < 2; ++_i) \
;         __builtin_amdgcn_global_load_lds((const unsigned*)((const char*)(gbase) + (voff)[_i]), (LAS unsigned*)(lds + (bufoff) + ldsw + _i * 8192), 16, 0, 0); } while (0)
; #define PG8_LDA(dst, b, h) do { if constexpr (F8) { _Pragma("unroll") for (int m = 0; m < 4; ++m) dst##8[m] = PG8_LD8(lds, PG8_SA(b, h) + aoff + m * 2048); } \
;         else { _Pragma("unroll") for (int m = 0; m < 4; ++m) _Pragma("unroll") for (int k = 0; k < 2; ++k) dst[m][k] = *(const LAS bf16x8*)(lds + PG8_SA(b, h) + aoff + m * 2048 + k * 1024); } } while (0)
; #define PG8_LDB(dst, b, h) do { if constexpr (F8) { _Pragma("unroll") for (int n = 0; n < 2; ++n) dst##8[n] = PG8_LD8(ldsB, PG8_SBR(b, h) + boff + n * 2048); } \
;         else { _Pragma("unroll") for (int n = 0; n < 2; ++n) _Pragma("unroll") for (int k = 0; k < 2; ++k) dst[n][k] = *(const LAS bf16x8*)(ldsB + PG8_SBR(b, h) + boff + n * 2048 + k * 1024); } } while (0)
; #define PG8_WAIT_V(n) asm volatile("s_waitcnt vmcnt(" #n ")" ::: "memory")
; #define PG8_WAIT_L(n) asm volatile("s_waitcnt lgkmcnt(" #n ")" ::: "memory")
; template <bool GATHER, bool F8, class Epi, class Sched>
; __device__ __forceinline__ void gemm_phase(LAS unsigned char* lds, const int nt, const unsigned lda, const unsigned ldb, const Sched& S, const Epi& E) {
;     ...
;             PG8_LDB(B0, 0, 0); PG8_LDB(B1, 0, 1); PG8_SCHED; PG8_LDA(At, 0, 0); PG8_STAGE(PG8_SA(1, 1), a1 + hA, vA1);
;             PG8_WAIT_V(8); PG8_WAIT_L(0); PG8_BAR; PG8_MMA(0, 0, At, B0); PG8_MMA(0, 1, At, B1); PG8_BAR; PG8_SCHED;
;             PG8_LDA(At, 0, 1); PG8_STAGE(PG8_SB(0, 0), b2, voffB); PG8_STAGE(PG8_SB(0, 1), b2 + hB, voffB); PG8_STAGE(PG8_SA(0, 0), a2, w0);
;             PG8_WAIT_V(8); PG8_WAIT_L(0); PG8_BAR; PG8_MMA(1, 0, At, B0); PG8_MMA(1, 1, At, B1); PG8_BAR; PG8_SCHED;
;             PG8_LDB(B0, 1, 0); PG8_LDB(B1, 1, 1); PG8_SCHED; PG8_LDA(At, 1, 0); PG8_STAGE(PG8_SA(0, 1), a2 + hA, w1);
;             PG8_WAIT_V(8); PG8_WAIT_L(0); PG8_BAR; PG8_MMA(0, 0, At, B0); PG8_MMA(0, 1, At, B1); PG8_BAR; PG8_SCHED;
;             PG8_LDA(At, 1, 1); PG8_STAGE(PG8_SB(1, 0), b3, voffB); PG8_STAGE(PG8_SB(1, 1), b3 + hB, voffB); PG8_STAGE(PG8_SA(1, 0), a3, w0);
;             PG8_WAIT_V(8); PG8_WAIT_L(0); PG8_BAR; PG8_MMA(1, 0, At, B0); PG8_MMA(1, 1, At, B1); PG8_BAR; PG8_SCHED;
	ds_read_b128 v[2:5], v201 offset:32768
	ds_read_b128 v[6:9], v201 offset:33792
	ds_read_b128 v[10:13], v201 offset:34816
	ds_read_b128 v[14:17], v201 offset:35840
	ds_read_b128 v[18:21], v201 offset:49152
	ds_read_b128 v[22:25], v201 offset:50176
	ds_read_b128 v[26:29], v201 offset:51200
	ds_read_b128 v[30:33], v201 offset:52224
	s_mov_b32 m0, s46
	ds_read_b128 v[210:213], v202 offset:32768
	ds_read_b128 v[214:217], v202 offset:33792
	ds_read_b128 v[218:221], v202 offset:34816
	ds_read_b128 v[222:225], v202 offset:35840
	ds_read_b128 v[226:229], v202 offset:36864
	ds_read_b128 v[230:233], v202 offset:37888
	ds_read_b128 v[234:237], v202 offset:38912
	ds_read_b128 v[238:241], v202 offset:39936
	global_load_lds_dwordx4 v173, s[36:37]
	s_mov_b32 m0, s47
	s_nop 0
	global_load_lds_dwordx4 v175, s[36:37]
	s_waitcnt vmcnt(8)
	s_waitcnt lgkmcnt(0)
	s_barrier
	s_setprio 0
	s_waitcnt lgkmcnt(0)
	v_mfma_scale_f32_16x16x128_f8f6f4 v[158:161], v[2:9], v[210:217], v[158:161], v203, v203 op_sel_hi:[0,0,0]
	v_mfma_scale_f32_16x16x128_f8f6f4 v[150:153], v[10:17], v[210:217], v[150:153], v203, v203 op_sel_hi:[0,0,0]
	v_mfma_scale_f32_16x16x128_f8f6f4 v[142:145], v[2:9], v[218:225], v[142:145], v203, v203 op_sel_hi:[0,0,0]
	v_mfma_scale_f32_16x16x128_f8f6f4 v[134:137], v[10:17], v[218:225], v[134:137], v203, v203 op_sel_hi:[0,0,0]
	v_mfma_scale_f32_16x16x128_f8f6f4 v[126:129], v[2:9], v[226:233], v[126:129], v203, v203 op_sel_hi:[0,0,0]
	v_mfma_scale_f32_16x16x128_f8f6f4 v[118:121], v[10:17], v[226:233], v[118:121], v203, v203 op_sel_hi:[0,0,0]
	v_mfma_scale_f32_16x16x128_f8f6f4 v[110:113], v[2:9], v[234:241], v[110:113], v203, v203 op_sel_hi:[0,0,0]
	v_mfma_scale_f32_16x16x128_f8f6f4 v[102:105], v[10:17], v[234:241], v[102:105], v203, v203 op_sel_hi:[0,0,0]
	s_setprio 1
	s_setprio 0
	v_mfma_scale_f32_16x16x128_f8f6f4 v[154:157], v[18:25], v[210:217], v[154:157], v203, v203 op_sel_hi:[0,0,0]
	v_mfma_scale_f32_16x16x128_f8f6f4 v[146:149], v[26:33], v[210:217], v[146:149], v203, v203 op_sel_hi:[0,0,0]
	v_mfma_scale_f32_16x16x128_f8f6f4 v[138:141], v[18:25], v[218:225], v[138:141], v203, v203 op_sel_hi:[0,0,0]
	v_mfma_scale_f32_16x16x128_f8f6f4 v[130:133], v[26:33], v[218:225], v[130:133], v203, v203 op_sel_hi:[0,0,0]
	v_mfma_scale_f32_16x16x128_f8f6f4 v[122:125], v[18:25], v[226:233], v[122:125], v203, v203 op_sel_hi:[0,0,0]
	v_mfma_scale_f32_16x16x128_f8f6f4 v[114:117], v[26:33], v[226:233], v[114:117], v203, v203 op_sel_hi:[0,0,0]
	v_mfma_scale_f32_16x16x128_f8f6f4 v[106:109], v[18:25], v[234:241], v[106:109], v203, v203 op_sel_hi:[0,0,0]
	v_mfma_scale_f32_16x16x128_f8f6f4 v[98:101], v[26:33], v[234:241], v[98:101], v203, v203 op_sel_hi:[0,0,0]
	s_setprio 1
	s_barrier
	s_add_i32 m0, s50, 0xffffff80
	ds_read_b128 v[210:213], v202 offset:49152
	ds_read_b128 v[214:217], v202 offset:50176
	ds_read_b128 v[218:221], v202 offset:51200
	ds_read_b128 v[222:225], v202 offset:52224
	ds_read_b128 v[226:229], v202 offset:53248
	ds_read_b128 v[230:233], v202 offset:54272
	ds_read_b128 v[234:237], v202 offset:55296
	ds_read_b128 v[238:241], v202 offset:56320
	global_load_lds_dwordx4 v166, s[34:35] offset:128
	s_add_i32 m0, s51, 0xffffff80
	s_nop 0
	global_load_lds_dwordx4 v168, s[34:35] offset:128
	s_add_u32 s34, s34, 0x40080
	s_addc_u32 s35, s35, 0
	s_mov_b32 m0, s54
	s_nop 0
	global_load_lds_dwordx4 v166, s[34:35]
	s_mov_b32 m0, s55
	s_nop 0
	global_load_lds_dwordx4 v168, s[34:35]
	s_add_i32 m0, s52, 0xffffff80
	s_nop 0
	global_load_lds_dwordx4 v164, s[36:37] offset:128
	s_add_i32 m0, s53, 0xffffff80
	s_nop 0
	global_load_lds_dwordx4 v242, s[36:37] offset:128
	s_waitcnt vmcnt(8)
	s_waitcnt lgkmcnt(0)
	s_barrier
	s_setprio 0
	s_waitcnt lgkmcnt(0)
	v_mfma_scale_f32_16x16x128_f8f6f4 v[94:97], v[2:9], v[210:217], v[94:97], v203, v203 op_sel_hi:[0,0,0]
	v_mfma_scale_f32_16x16x128_f8f6f4 v[86:89], v[10:17], v[210:217], v[86:89], v203, v203 op_sel_hi:[0,0,0]
	v_mfma_scale_f32_16x16x128_f8f6f4 v[78:81], v[2:9], v[218:225], v[78:81], v203, v203 op_sel_hi:[0,0,0]
	v_mfma_scale_f32_16x16x128_f8f6f4 v[70:73], v[10:17], v[218:225], v[70:73], v203, v203 op_sel_hi:[0,0,0]
	v_mfma_scale_f32_16x16x128_f8f6f4 v[54:57], v[2:9], v[226:233], v[54:57], v203, v203 op_sel_hi:[0,0,0]
	v_mfma_scale_f32_16x16x128_f8f6f4 v[50:53], v[10:17], v[226:233], v[50:53], v203, v203 op_sel_hi:[0,0,0]
	v_mfma_scale_f32_16x16x128_f8f6f4 v[38:41], v[2:9], v[234:241], v[38:41], v203, v203 op_sel_hi:[0,0,0]
	v_mfma_scale_f32_16x16x128_f8f6f4 v[34:37], v[10:17], v[234:241], v[34:37], v203, v203 op_sel_hi:[0,0,0]
	s_setprio 1
	s_setprio 0
	v_mfma_scale_f32_16x16x128_f8f6f4 v[90:93], v[18:25], v[210:217], v[90:93], v203, v203 op_sel_hi:[0,0,0]
	v_mfma_scale_f32_16x16x128_f8f6f4 v[82:85], v[26:33], v[210:217], v[82:85], v203, v203 op_sel_hi:[0,0,0]
	v_mfma_scale_f32_16x16x128_f8f6f4 v[74:77], v[18:25], v[218:225], v[74:77], v203, v203 op_sel_hi:[0,0,0]
	v_mfma_scale_f32_16x16x128_f8f6f4 v[62:65], v[26:33], v[218:225], v[62:65], v203, v203 op_sel_hi:[0,0,0]
	v_mfma_scale_f32_16x16x128_f8f6f4 v[66:69], v[18:25], v[226:233], v[66:69], v203, v203 op_sel_hi:[0,0,0]
	v_mfma_scale_f32_16x16x128_f8f6f4 v[58:61], v[26:33], v[226:233], v[58:61], v203, v203 op_sel_hi:[0,0,0]
	v_mfma_scale_f32_16x16x128_f8f6f4 v[46:49], v[18:25], v[234:241], v[46:49], v203, v203 op_sel_hi:[0,0,0]
	v_mfma_scale_f32_16x16x128_f8f6f4 v[42:45], v[26:33], v[234:241], v[42:45], v203, v203 op_sel_hi:[0,0,0]
	s_setprio 1
	s_barrier
	s_add_i32 s39, s39, 2
	s_add_u32 s0, s0, 0x100
	s_addc_u32 s1, s1, 0
	s_cmp_gt_u32 s39, 13
	s_cbranch_scc0 .LBB0_1927
	s_and_b64 vcc, exec, s[12:13]
	s_cbranch_vccz .LBB0_1930
	s_barrier

; #define PG8_STAGE(bufoff, gbase, voff) do { _Pragma("unroll") for (int _i = 0; _i < 2; ++_i) \
;         __builtin_amdgcn_global_load_lds((const unsigned*)((const char*)(gbase) + (voff)[_i]), (LAS unsigned*)(lds + (bufoff) + ldsw + _i * 8192), 16, 0, 0); } while (0)
; #define PG8_LDA(dst, b, h) do { if constexpr (F8) { _Pragma("unroll") for (int m = 0; m < 4; ++m) dst##8[m] = PG8_LD8(lds, PG8_SA(b, h) + aoff + m * 2048); } \
;         else { _Pragma("unroll") for (int m = 0; m < 4; ++m) _Pragma("unroll") for (int k = 0; k < 2; ++k) dst[m][k] = *(const LAS bf16x8*)(lds + PG8_SA(b, h) + aoff + m * 2048 + k * 1024); } } while (0)
; #define PG8_LDB(dst, b, h) do { if constexpr (F8) { _Pragma("unroll") for (int n = 0; n < 2; ++n) dst##8[n] = PG8_LD8(ldsB, PG8_SBR(b, h) + boff + n * 2048); } \
;         else { _Pragma("unroll") for (int n = 0; n < 2; ++n) _Pragma("unroll") for (int k = 0; k < 2; ++k) dst[n][k] = *(const LAS bf16x8*)(ldsB + PG8_SBR(b, h) + boff + n * 2048 + k * 1024); } } while (0)
; #define PG8_WAIT_V(n) asm volatile("s_waitcnt vmcnt(" #n ")" ::: "memory")
; #define PG8_WAIT_L(n) asm volatile("s_waitcnt lgkmcnt(" #n ")" ::: "memory")
; template <bool GATHER, bool F8, class Epi, class Sched>
; __device__ __forceinline__ void gemm_phase(LAS unsigned char* lds, const int nt, const unsigned lda, const unsigned ldb, const Sched& S, const Epi& E) {
;     ...
;             PG8_LDB(B0, 0, 0); PG8_LDB(B1, 0, 1); PG8_SCHED; PG8_LDA(At, 0, 0); PG8_STAGE(PG8_SA(1, 1), a1 + hA, vA1);
;             PG8_WAIT_V(8); PG8_WAIT_L(0); PG8_BAR; PG8_MMA(0, 0, At, B0); PG8_MMA(0, 1, At, B1); PG8_BAR; PG8_SCHED;
;             PG8_LDA(At, 0, 1); PG8_STAGE(PG8_SB(0, 0), b2, voffB); PG8_STAGE(PG8_SB(0, 1), b2 + hB, voffB); PG8_STAGE(PG8_SA(0, 0), a2, w0);
;             PG8_WAIT_V(8); PG8_WAIT_L(0); PG8_BAR; PG8_MMA(1, 0, At, B0); PG8_MMA(1, 1, At, B1); PG8_BAR; PG8_SCHED;
;             PG8_LDB(B0, 1, 0); PG8_LDB(B1, 1, 1); PG8_SCHED; PG8_LDA(At, 1, 0); PG8_STAGE(PG8_SA(0, 1), a2 + hA, w1);
;             PG8_WAIT_V(8); PG8_WAIT_L(0); PG8_BAR; PG8_MMA(0, 0, At, B0); PG8_MMA(0, 1, At, B1); PG8_BAR; PG8_SCHED;
;             PG8_LDA(At, 1, 1); PG8_STAGE(PG8_SB(1, 0), b3, voffB); PG8_STAGE(PG8_SB(1, 1), b3 + hB, voffB); PG8_STAGE(PG8_SA(1, 0), a3, w0);
;             PG8_WAIT_V(8); PG8_WAIT_L(0); PG8_BAR; PG8_MMA(1, 0, At, B0); PG8_MMA(1, 1, At, B1); PG8_BAR; PG8_SCHED;
.LBB0_2018:
	ds_read_b128 v[18:21], v186
	ds_read_b128 v[22:25], v186 offset:1024
	ds_read_b128 v[26:29], v186 offset:2048
	ds_read_b128 v[30:33], v186 offset:3072
	ds_read_b128 v[2:5], v186 offset:16384
	ds_read_b128 v[6:9], v186 offset:17408
	ds_read_b128 v[10:13], v186 offset:18432
	ds_read_b128 v[14:17], v186 offset:19456
	s_add_u32 s28, s26, 0xfffc0080
	s_addc_u32 s29, s27, -1
	s_cmp_eq_u32 s58, 12
	s_cselect_b32 s31, s25, s29
	s_cselect_b32 s30, s24, s28
	s_cselect_b32 s29, s23, s12
	s_cselect_b32 s28, s22, s7
	s_add_i32 m0, s1, 0xc000
	ds_read_b128 v[174:177], v187
	ds_read_b128 v[178:181], v187 offset:1024
	ds_read_b128 v[190:193], v187 offset:2048
	ds_read_b128 v[194:197], v187 offset:3072
	ds_read_b128 v[200:203], v187 offset:4096
	ds_read_b128 v[204:207], v187 offset:5120
	ds_read_b128 v[208:211], v187 offset:6144
	ds_read_b128 v[212:215], v187 offset:7168
	global_load_lds_dwordx4 v170, s[26:27]
	s_add_i32 m0, s1, 0xe000
	s_nop 0
	global_load_lds_dwordx4 v172, s[26:27]
	s_waitcnt vmcnt(8)
	s_waitcnt lgkmcnt(0)
	s_barrier
	s_setprio 0
	s_waitcnt lgkmcnt(0)
	v_mfma_scale_f32_16x16x128_f8f6f4 v[158:161], v[18:25], v[174:181], v[158:161], v188, v188 op_sel_hi:[0,0,0]
	v_mfma_scale_f32_16x16x128_f8f6f4 v[154:157], v[26:33], v[174:181], v[154:157], v188, v188 op_sel_hi:[0,0,0]
	v_mfma_scale_f32_16x16x128_f8f6f4 v[142:145], v[18:25], v[190:197], v[142:145], v188, v188 op_sel_hi:[0,0,0]
	v_mfma_scale_f32_16x16x128_f8f6f4 v[138:141], v[26:33], v[190:197], v[138:141], v188, v188 op_sel_hi:[0,0,0]
	v_mfma_scale_f32_16x16x128_f8f6f4 v[126:129], v[18:25], v[200:207], v[126:129], v188, v188 op_sel_hi:[0,0,0]
	v_mfma_scale_f32_16x16x128_f8f6f4 v[122:125], v[26:33], v[200:207], v[122:125], v188, v188 op_sel_hi:[0,0,0]
	v_mfma_scale_f32_16x16x128_f8f6f4 v[110:113], v[18:25], v[208:215], v[110:113], v188, v188 op_sel_hi:[0,0,0]
	v_mfma_scale_f32_16x16x128_f8f6f4 v[106:109], v[26:33], v[208:215], v[106:109], v188, v188 op_sel_hi:[0,0,0]
	s_setprio 1
	s_setprio 0
	v_mfma_scale_f32_16x16x128_f8f6f4 v[150:153], v[2:9], v[174:181], v[150:153], v188, v188 op_sel_hi:[0,0,0]
	v_mfma_scale_f32_16x16x128_f8f6f4 v[146:149], v[10:17], v[174:181], v[146:149], v188, v188 op_sel_hi:[0,0,0]
	v_mfma_scale_f32_16x16x128_f8f6f4 v[134:137], v[2:9], v[190:197], v[134:137], v188, v188 op_sel_hi:[0,0,0]
	v_mfma_scale_f32_16x16x128_f8f6f4 v[130:133], v[10:17], v[190:197], v[130:133], v188, v188 op_sel_hi:[0,0,0]
	v_mfma_scale_f32_16x16x128_f8f6f4 v[118:121], v[2:9], v[200:207], v[118:121], v188, v188 op_sel_hi:[0,0,0]
	v_mfma_scale_f32_16x16x128_f8f6f4 v[114:117], v[10:17], v[200:207], v[114:117], v188, v188 op_sel_hi:[0,0,0]
	v_mfma_scale_f32_16x16x128_f8f6f4 v[102:105], v[2:9], v[208:215], v[102:105], v188, v188 op_sel_hi:[0,0,0]
	v_mfma_scale_f32_16x16x128_f8f6f4 v[98:101], v[10:17], v[208:215], v[98:101], v188, v188 op_sel_hi:[0,0,0]
	s_setprio 1
	s_barrier
	s_mov_b32 m0, s35
	s_add_u32 s60, s28, 0x40000
	ds_read_b128 v[190:193], v187 offset:16384
	ds_read_b128 v[194:197], v187 offset:17408
	ds_read_b128 v[200:203], v187 offset:18432
	ds_read_b128 v[204:207], v187 offset:19456
	ds_read_b128 v[208:211], v187 offset:20480
	ds_read_b128 v[212:215], v187 offset:21504
	ds_read_b128 v[216:219], v187 offset:22528
	ds_read_b128 v[220:223], v187 offset:23552
	global_load_lds_dwordx4 v166, s[28:29]
	s_mov_b32 m0, s36
	s_addc_u32 s61, s29, 0
	global_load_lds_dwordx4 v162, s[28:29]
	s_mov_b32 m0, s37
	s_nop 0
	global_load_lds_dwordx4 v166, s[60:61]
	s_mov_b32 m0, s38
	s_nop 0
	global_load_lds_dwordx4 v162, s[60:61]
	s_mov_b32 m0, s1
	s_nop 0
	s_mov_b64 s[98:99], s[30:31]
	global_load_lds_dwordx4 v168, s[30:31]
	s_mov_b32 m0, s39
	s_nop 0
	global_load_lds_dwordx4 v164, s[30:31]
	s_waitcnt vmcnt(8)
	s_waitcnt lgkmcnt(0)
	s_barrier
	s_setprio 0
	s_waitcnt lgkmcnt(0)
	v_mfma_scale_f32_16x16x128_f8f6f4 v[86:89], v[18:25], v[190:197], v[86:89], v188, v188 op_sel_hi:[0,0,0]
	v_mfma_scale_f32_16x16x128_f8f6f4 v[82:85], v[26:33], v[190:197], v[82:85], v188, v188 op_sel_hi:[0,0,0]
	v_mfma_scale_f32_16x16x128_f8f6f4 v[70:73], v[18:25], v[200:207], v[70:73], v188, v188 op_sel_hi:[0,0,0]
	v_mfma_scale_f32_16x16x128_f8f6f4 v[66:69], v[26:33], v[200:207], v[66:69], v188, v188 op_sel_hi:[0,0,0]
	v_mfma_scale_f32_16x16x128_f8f6f4 v[54:57], v[18:25], v[208:215], v[54:57], v188, v188 op_sel_hi:[0,0,0]
	v_mfma_scale_f32_16x16x128_f8f6f4 v[42:45], v[26:33], v[208:215], v[42:45], v188, v188 op_sel_hi:[0,0,0]
	v_mfma_scale_f32_16x16x128_f8f6f4 v[38:41], v[18:25], v[216:223], v[38:41], v188, v188 op_sel_hi:[0,0,0]
	v_mfma_scale_f32_16x16x128_f8f6f4 v[34:37], v[26:33], v[216:223], v[34:37], v188, v188 op_sel_hi:[0,0,0]
	s_setprio 1
	s_setprio 0
	v_mfma_scale_f32_16x16x128_f8f6f4 v[94:97], v[2:9], v[190:197], v[94:97], v188, v188 op_sel_hi:[0,0,0]
	v_mfma_scale_f32_16x16x128_f8f6f4 v[90:93], v[10:17], v[190:197], v[90:93], v188, v188 op_sel_hi:[0,0,0]
	v_mfma_scale_f32_16x16x128_f8f6f4 v[78:81], v[2:9], v[200:207], v[78:81], v188, v188 op_sel_hi:[0,0,0]
	v_mfma_scale_f32_16x16x128_f8f6f4 v[74:77], v[10:17], v[200:207], v[74:77], v188, v188 op_sel_hi:[0,0,0]
	v_mfma_scale_f32_16x16x128_f8f6f4 v[62:65], v[2:9], v[208:215], v[62:65], v188, v188 op_sel_hi:[0,0,0]
	v_mfma_scale_f32_16x16x128_f8f6f4 v[58:61], v[10:17], v[208:215], v[58:61], v188, v188 op_sel_hi:[0,0,0]
	v_mfma_scale_f32_16x16x128_f8f6f4 v[50:53], v[2:9], v[216:223], v[50:53], v188, v188 op_sel_hi:[0,0,0]
	v_mfma_scale_f32_16x16x128_f8f6f4 v[46:49], v[10:17], v[216:223], v[46:49], v188, v188 op_sel_hi:[0,0,0]
	s_setprio 1
	s_barrier
; #define PG8_STAGE(bufoff, gbase, voff) do { _Pragma("unroll") for (int _i = 0; _i < 2; ++_i) \
;         __builtin_amdgcn_global_load_lds((const unsigned*)((const char*)(gbase) + (voff)[_i]), (LAS unsigned*)(lds + (bufoff) + ldsw + _i * 8192), 16, 0, 0); } while (0)
; #define PG8_LDA(dst, b, h) do { if constexpr (F8) { _Pragma("unroll") for (int m = 0; m < 4; ++m) dst##8[m] = PG8_LD8(lds, PG8_SA(b, h) + aoff + m * 2048); } \
;         else { _Pragma("unroll") for (int m = 0; m < 4; ++m) _Pragma("unroll") for (int k = 0; k < 2; ++k) dst[m][k] = *(const LAS bf16x8*)(lds + PG8_SA(b, h) + aoff + m * 2048 + k * 1024); } } while (0)
; #define PG8_LDB(dst, b, h) do { if constexpr (F8) { _Pragma("unroll") for (int n = 0; n < 2; ++n) dst##8[n] = PG8_LD8(ldsB, PG8_SBR(b, h) + boff + n * 2048); } \
;         else { _Pragma("unroll") for (int n = 0; n < 2; ++n) _Pragma("unroll") for (int k = 0; k < 2; ++k) dst[n][k] = *(const LAS bf16x8*)(ldsB + PG8_SBR(b, h) + boff + n * 2048 + k * 1024); } } while (0)
; #define PG8_WAIT_V(n) asm volatile("s_waitcnt vmcnt(" #n ")" ::: "memory")
; #define PG8_WAIT_L(n) asm volatile("s_waitcnt lgkmcnt(" #n ")" ::: "memory")
; template <bool GATHER, bool F8, class Epi, class Sched>
; __device__ __forceinline__ void gemm_phase(LAS unsigned char* lds, const int nt, const unsigned lda, const unsigned ldb, const Sched& S, const Epi& E) {
;     ...
;             PG8_LDB(B0, 0, 0); PG8_LDB(B1, 0, 1); PG8_SCHED; PG8_LDA(At, 0, 0); PG8_STAGE(PG8_SA(1, 1), a1 + hA, vA1);
;             PG8_WAIT_V(8); PG8_WAIT_L(0); PG8_BAR; PG8_MMA(0, 0, At, B0); PG8_MMA(0, 1, At, B1); PG8_BAR; PG8_SCHED;
;             PG8_LDA(At, 0, 1); PG8_STAGE(PG8_SB(0, 0), b2, voffB); PG8_STAGE(PG8_SB(0, 1), b2 + hB, voffB); PG8_STAGE(PG8_SA(0, 0), a2, w0);
;             PG8_WAIT_V(8); PG8_WAIT_L(0); PG8_BAR; PG8_MMA(1, 0, At, B0); PG8_MMA(1, 1, At, B1); PG8_BAR; PG8_SCHED;
;             PG8_LDB(B0, 1, 0); PG8_LDB(B1, 1, 1); PG8_SCHED; PG8_LDA(At, 1, 0); PG8_STAGE(PG8_SA(0, 1), a2 + hA, w1);
;             PG8_WAIT_V(8); PG8_WAIT_L(0); PG8_BAR; PG8_MMA(0, 0, At, B0); PG8_MMA(0, 1, At, B1); PG8_BAR; PG8_SCHED;
;             PG8_LDA(At, 1, 1); PG8_STAGE(PG8_SB(1, 0), b3, voffB); PG8_STAGE(PG8_SB(1, 1), b3 + hB, voffB); PG8_STAGE(PG8_SA(1, 0), a3, w0);
;             PG8_WAIT_V(8); PG8_WAIT_L(0); PG8_BAR; PG8_MMA(1, 0, At, B0); PG8_MMA(1, 1, At, B1); PG8_BAR; PG8_SCHED;
	ds_read_b128 v[2:5], v186 offset:32768
	ds_read_b128 v[6:9], v186 offset:33792
	ds_read_b128 v[10:13], v186 offset:34816
	ds_read_b128 v[14:17], v186 offset:35840
	ds_read_b128 v[18:21], v186 offset:49152
	ds_read_b128 v[22:25], v186 offset:50176
	ds_read_b128 v[26:29], v186 offset:51200
	ds_read_b128 v[30:33], v186 offset:52224
	s_add_u32 s30, s30, 0x40000
	s_addc_u32 s31, s31, 0
	s_mov_b32 m0, s40
	ds_read_b128 v[190:193], v187 offset:32768
	ds_read_b128 v[194:197], v187 offset:33792
	ds_read_b128 v[200:203], v187 offset:34816
	ds_read_b128 v[204:207], v187 offset:35840
	ds_read_b128 v[208:211], v187 offset:36864
	ds_read_b128 v[212:215], v187 offset:37888
	ds_read_b128 v[216:219], v187 offset:38912
	ds_read_b128 v[220:223], v187 offset:39936
	global_load_lds_dwordx4 v168, s[30:31]
	s_mov_b32 m0, s41
	s_nop 0
	global_load_lds_dwordx4 v164, s[30:31]
	s_waitcnt vmcnt(8)
	s_waitcnt lgkmcnt(0)
	s_barrier
	s_setprio 0
	s_waitcnt lgkmcnt(0)
	v_mfma_scale_f32_16x16x128_f8f6f4 v[158:161], v[2:9], v[190:197], v[158:161], v188, v188 op_sel_hi:[0,0,0]
	v_mfma_scale_f32_16x16x128_f8f6f4 v[154:157], v[10:17], v[190:197], v[154:157], v188, v188 op_sel_hi:[0,0,0]
	v_mfma_scale_f32_16x16x128_f8f6f4 v[142:145], v[2:9], v[200:207], v[142:145], v188, v188 op_sel_hi:[0,0,0]
	v_mfma_scale_f32_16x16x128_f8f6f4 v[138:141], v[10:17], v[200:207], v[138:141], v188, v188 op_sel_hi:[0,0,0]
	v_mfma_scale_f32_16x16x128_f8f6f4 v[126:129], v[2:9], v[208:215], v[126:129], v188, v188 op_sel_hi:[0,0,0]
	v_mfma_scale_f32_16x16x128_f8f6f4 v[122:125], v[10:17], v[208:215], v[122:125], v188, v188 op_sel_hi:[0,0,0]
	v_mfma_scale_f32_16x16x128_f8f6f4 v[110:113], v[2:9], v[216:223], v[110:113], v188, v188 op_sel_hi:[0,0,0]
	v_mfma_scale_f32_16x16x128_f8f6f4 v[106:109], v[10:17], v[216:223], v[106:109], v188, v188 op_sel_hi:[0,0,0]
	s_setprio 1
	s_setprio 0
	v_mfma_scale_f32_16x16x128_f8f6f4 v[150:153], v[18:25], v[190:197], v[150:153], v188, v188 op_sel_hi:[0,0,0]
	v_mfma_scale_f32_16x16x128_f8f6f4 v[146:149], v[26:33], v[190:197], v[146:149], v188, v188 op_sel_hi:[0,0,0]
	v_mfma_scale_f32_16x16x128_f8f6f4 v[134:137], v[18:25], v[200:207], v[134:137], v188, v188 op_sel_hi:[0,0,0]
	v_mfma_scale_f32_16x16x128_f8f6f4 v[130:133], v[26:33], v[200:207], v[130:133], v188, v188 op_sel_hi:[0,0,0]
	v_mfma_scale_f32_16x16x128_f8f6f4 v[118:121], v[18:25], v[208:215], v[118:121], v188, v188 op_sel_hi:[0,0,0]
	v_mfma_scale_f32_16x16x128_f8f6f4 v[114:117], v[26:33], v[208:215], v[114:117], v188, v188 op_sel_hi:[0,0,0]
	v_mfma_scale_f32_16x16x128_f8f6f4 v[102:105], v[18:25], v[216:223], v[102:105], v188, v188 op_sel_hi:[0,0,0]
	v_mfma_scale_f32_16x16x128_f8f6f4 v[98:101], v[26:33], v[216:223], v[98:101], v188, v188 op_sel_hi:[0,0,0]
	s_setprio 1
	s_barrier
	s_add_i32 m0, s43, 0xffffff80
	ds_read_b128 v[190:193], v187 offset:49152
	ds_read_b128 v[194:197], v187 offset:50176
	ds_read_b128 v[200:203], v187 offset:51200
	ds_read_b128 v[204:207], v187 offset:52224
	ds_read_b128 v[208:211], v187 offset:53248
	ds_read_b128 v[212:215], v187 offset:54272
	ds_read_b128 v[216:219], v187 offset:55296
	ds_read_b128 v[220:223], v187 offset:56320
	global_load_lds_dwordx4 v166, s[28:29] offset:128
	s_add_i32 m0, s44, 0xffffff80
	s_nop 0
	global_load_lds_dwordx4 v162, s[28:29] offset:128
	s_add_u32 s28, s28, 0x40080
	s_addc_u32 s29, s29, 0
	s_mov_b32 m0, s47
	s_nop 0
	global_load_lds_dwordx4 v166, s[28:29]
	s_mov_b32 m0, s48
	s_nop 0
	global_load_lds_dwordx4 v162, s[28:29]
	s_add_i32 m0, s45, 0xffffff80
	s_nop 0
	global_load_lds_dwordx4 v168, s[98:99] offset:128
	s_add_i32 m0, s46, 0xffffff80
	s_nop 0
	global_load_lds_dwordx4 v164, s[98:99] offset:128
	s_waitcnt vmcnt(8)
	s_waitcnt lgkmcnt(0)
	s_barrier
	s_setprio 0
	s_waitcnt lgkmcnt(0)
	v_mfma_scale_f32_16x16x128_f8f6f4 v[86:89], v[2:9], v[190:197], v[86:89], v188, v188 op_sel_hi:[0,0,0]
	v_mfma_scale_f32_16x16x128_f8f6f4 v[82:85], v[10:17], v[190:197], v[82:85], v188, v188 op_sel_hi:[0,0,0]
	v_mfma_scale_f32_16x16x128_f8f6f4 v[70:73], v[2:9], v[200:207], v[70:73], v188, v188 op_sel_hi:[0,0,0]
	v_mfma_scale_f32_16x16x128_f8f6f4 v[66:69], v[10:17], v[200:207], v[66:69], v188, v188 op_sel_hi:[0,0,0]
	v_mfma_scale_f32_16x16x128_f8f6f4 v[54:57], v[2:9], v[208:215], v[54:57], v188, v188 op_sel_hi:[0,0,0]
	v_mfma_scale_f32_16x16x128_f8f6f4 v[42:45], v[10:17], v[208:215], v[42:45], v188, v188 op_sel_hi:[0,0,0]
	v_mfma_scale_f32_16x16x128_f8f6f4 v[38:41], v[2:9], v[216:223], v[38:41], v188, v188 op_sel_hi:[0,0,0]
	v_mfma_scale_f32_16x16x128_f8f6f4 v[34:37], v[10:17], v[216:223], v[34:37], v188, v188 op_sel_hi:[0,0,0]
	s_setprio 1
	s_setprio 0
	v_mfma_scale_f32_16x16x128_f8f6f4 v[94:97], v[18:25], v[190:197], v[94:97], v188, v188 op_sel_hi:[0,0,0]
	v_mfma_scale_f32_16x16x128_f8f6f4 v[90:93], v[26:33], v[190:197], v[90:93], v188, v188 op_sel_hi:[0,0,0]
	v_mfma_scale_f32_16x16x128_f8f6f4 v[78:81], v[18:25], v[200:207], v[78:81], v188, v188 op_sel_hi:[0,0,0]
	v_mfma_scale_f32_16x16x128_f8f6f4 v[74:77], v[26:33], v[200:207], v[74:77], v188, v188 op_sel_hi:[0,0,0]
	v_mfma_scale_f32_16x16x128_f8f6f4 v[62:65], v[18:25], v[208:215], v[62:65], v188, v188 op_sel_hi:[0,0,0]
	v_mfma_scale_f32_16x16x128_f8f6f4 v[58:61], v[26:33], v[208:215], v[58:61], v188, v188 op_sel_hi:[0,0,0]
	v_mfma_scale_f32_16x16x128_f8f6f4 v[50:53], v[18:25], v[216:223], v[50:53], v188, v188 op_sel_hi:[0,0,0]
	v_mfma_scale_f32_16x16x128_f8f6f4 v[46:49], v[26:33], v[216:223], v[46:49], v188, v188 op_sel_hi:[0,0,0]
	s_setprio 1
	s_barrier
	s_add_i32 s58, s58, 2
	s_add_u32 s26, s26, 0x100
	s_addc_u32 s27, s27, 0
	s_add_u32 s7, s7, 0x100
	s_addc_u32 s12, s12, 0
	s_cmp_gt_u32 s58, 13
	s_cbranch_scc0 .LBB0_2018
	s_and_b64 vcc, exec, s[14:15]
	s_cbranch_vccz .LBB0_2021
	s_barrier
